# baseline (speedup 1.0000x reference)
.LBB2_3:
	s_setprio 2
	s_lshl_b32 s3, s2, 2
	s_and_b32 s3, s3, 28
	s_bfe_u32 s2, s2, 0x20003
	s_load_dwordx2 s[12:13], s[0:1], 0x8
	s_load_dwordx2 s[4:5], s[0:1], 0x28
	s_or_b32 s6, s3, s2
	s_lshl_b32 s2, s6, 8
	s_lshl_b32 s3, s9, 6
	s_or_b32 s3, s3, s2
	s_lshl_b32 s2, s3, 10
	s_waitcnt lgkmcnt(0)
	s_add_u32 s12, s12, s2
	s_addc_u32 s13, s13, 0
	v_lshl_add_u64 v[132:133], s[12:13], 0, v[130:131]
	s_movk_i32 s2, 0x1000
	v_add_co_u32_e32 v6, vcc, s2, v132
	s_movk_i32 s2, 0x2000
	s_nop 0
	v_addc_co_u32_e32 v7, vcc, 0, v133, vcc
	v_add_co_u32_e32 v8, vcc, s2, v132
	global_load_dwordx4 v[66:69], v130, s[12:13] offset:1024
	global_load_dwordx4 v[74:77], v130, s[12:13] offset:2048
	v_addc_co_u32_e32 v9, vcc, 0, v133, vcc
	global_load_dwordx4 v[78:81], v130, s[12:13] offset:3072
	global_load_dwordx4 v[82:85], v[8:9], off offset:-4096
	global_load_dwordx4 v[106:109], v[6:7], off offset:1024
	global_load_dwordx4 v[114:117], v[6:7], off offset:2048
	global_load_dwordx4 v[2:5], v130, s[12:13]
	global_load_dwordx4 v[118:121], v[6:7], off offset:3072
	global_load_dwordx4 v[122:125], v[8:9], off
	global_load_dwordx4 v[102:105], v[8:9], off offset:1024
	global_load_dwordx4 v[86:89], v[8:9], off offset:2048
	global_load_dwordx4 v[70:73], v[8:9], off offset:3072
	s_barrier
	ds_read_b128 v[6:9], v130
	ds_read_b128 v[10:13], v130 offset:4096
	ds_read_b128 v[14:17], v130 offset:8192
	ds_read_b128 v[94:97], v130 offset:12288
	ds_read_b128 v[98:101], v130 offset:1024
	s_waitcnt vmcnt(5) lgkmcnt(4)
	v_mfma_f32_32x32x16_f16 v[50:65], v[6:9], v[2:5], 0
	s_movk_i32 s2, 0x4000
	v_add_co_u32_e32 v146, vcc, s2, v132
	ds_read_b128 v[110:113], v130 offset:5120
	s_nop 0
	v_addc_co_u32_e32 v147, vcc, 0, v133, vcc
	global_load_dwordx4 v[90:93], v[146:147], off offset:-4096
	s_movk_i32 s2, 0x3000
	v_add_co_u32_e32 v148, vcc, s2, v132
	s_waitcnt lgkmcnt(4)
	v_mfma_f32_32x32x16_f16 v[34:49], v[10:13], v[2:5], 0
	v_addc_co_u32_e32 v149, vcc, 0, v133, vcc
	ds_read_b128 v[126:129], v130 offset:9216
	s_waitcnt lgkmcnt(4)
	v_mfma_f32_32x32x16_f16 v[18:33], v[14:17], v[2:5], 0
	s_waitcnt lgkmcnt(3)
	v_mfma_f32_32x32x16_f16 v[2:17], v[94:97], v[2:5], 0
	ds_read_b128 v[134:137], v130 offset:13312
	ds_read_b128 v[138:141], v130 offset:2048
	s_waitcnt lgkmcnt(4)
	v_mfma_f32_32x32x16_f16 v[50:65], v[98:101], v[66:69], v[50:65]
	global_load_dwordx4 v[94:97], v[148:149], off offset:1024
	ds_read_b128 v[98:101], v130 offset:6144
	s_waitcnt lgkmcnt(4)
	v_mfma_f32_32x32x16_f16 v[34:49], v[110:113], v[66:69], v[34:49]
	ds_read_b128 v[142:145], v130 offset:10240
	s_waitcnt lgkmcnt(4)
	v_mfma_f32_32x32x16_f16 v[18:33], v[126:129], v[66:69], v[18:33]
	s_waitcnt lgkmcnt(3)
	v_mfma_f32_32x32x16_f16 v[2:17], v[134:137], v[66:69], v[2:17]
	ds_read_b128 v[126:129], v130 offset:14336
	ds_read_b128 v[66:69], v130 offset:3072
	s_waitcnt lgkmcnt(4)
	v_mfma_f32_32x32x16_f16 v[50:65], v[138:141], v[74:77], v[50:65]
	global_load_dwordx4 v[110:113], v[148:149], off offset:2048
	ds_read_b128 v[134:137], v130 offset:7168
	s_waitcnt lgkmcnt(4)
	v_mfma_f32_32x32x16_f16 v[34:49], v[98:101], v[74:77], v[34:49]
	ds_read_b128 v[138:141], v130 offset:11264
	s_waitcnt lgkmcnt(4)
	v_mfma_f32_32x32x16_f16 v[18:33], v[142:145], v[74:77], v[18:33]
	s_waitcnt lgkmcnt(3)
	v_mfma_f32_32x32x16_f16 v[2:17], v[126:129], v[74:77], v[2:17]
	ds_read_b128 v[142:145], v130 offset:15360
	global_load_dwordx4 v[98:101], v[148:149], off offset:3072
	s_waitcnt lgkmcnt(3)
	v_mfma_f32_32x32x16_f16 v[50:65], v[66:69], v[78:81], v[50:65]
	s_waitcnt lgkmcnt(0)
	s_barrier
	ds_read_b128 v[66:69], v130 offset:16384
	ds_read_b128 v[126:129], v130 offset:20480
	v_mfma_f32_32x32x16_f16 v[34:49], v[134:137], v[78:81], v[34:49]
	ds_read_b128 v[134:137], v130 offset:24576
	v_mfma_f32_32x32x16_f16 v[18:33], v[138:141], v[78:81], v[18:33]
	v_mfma_f32_32x32x16_f16 v[2:17], v[142:145], v[78:81], v[2:17]
	ds_read_b128 v[138:141], v130 offset:28672
	ds_read_b128 v[78:81], v130 offset:17408
	s_waitcnt lgkmcnt(4)
	v_mfma_f32_32x32x16_f16 v[50:65], v[66:69], v[82:85], v[50:65]
	global_load_dwordx4 v[74:77], v[146:147], off
	ds_read_b128 v[66:69], v130 offset:21504
	s_waitcnt lgkmcnt(4)
	v_mfma_f32_32x32x16_f16 v[34:49], v[126:129], v[82:85], v[34:49]
	ds_read_b128 v[126:129], v130 offset:25600
	s_waitcnt lgkmcnt(4)
	v_mfma_f32_32x32x16_f16 v[18:33], v[134:137], v[82:85], v[18:33]
	s_waitcnt lgkmcnt(3)
	v_mfma_f32_32x32x16_f16 v[2:17], v[138:141], v[82:85], v[2:17]
	ds_read_b128 v[134:137], v130 offset:29696
	ds_read_b128 v[82:85], v130 offset:18432
	s_waitcnt lgkmcnt(4)
	v_mfma_f32_32x32x16_f16 v[50:65], v[78:81], v[106:109], v[50:65]
	global_load_dwordx4 v[78:81], v[146:147], off offset:1024
	ds_read_b128 v[138:141], v130 offset:22528
	s_waitcnt lgkmcnt(4)
	v_mfma_f32_32x32x16_f16 v[34:49], v[66:69], v[106:109], v[34:49]
	ds_read_b128 v[66:69], v130 offset:26624
	s_waitcnt lgkmcnt(4)
	v_mfma_f32_32x32x16_f16 v[18:33], v[126:129], v[106:109], v[18:33]
	s_waitcnt lgkmcnt(3)
	v_mfma_f32_32x32x16_f16 v[2:17], v[134:137], v[106:109], v[2:17]
	ds_read_b128 v[126:129], v130 offset:30720
	ds_read_b128 v[106:109], v130 offset:19456
	s_waitcnt lgkmcnt(4)
	v_mfma_f32_32x32x16_f16 v[50:65], v[82:85], v[114:117], v[50:65]
	global_load_dwordx4 v[82:85], v[146:147], off offset:2048
	ds_read_b128 v[134:137], v130 offset:23552
	s_waitcnt lgkmcnt(4)
	v_mfma_f32_32x32x16_f16 v[34:49], v[138:141], v[114:117], v[34:49]
	ds_read_b128 v[138:141], v130 offset:27648
	s_waitcnt lgkmcnt(4)
	v_mfma_f32_32x32x16_f16 v[18:33], v[66:69], v[114:117], v[18:33]
	s_waitcnt lgkmcnt(3)
	v_mfma_f32_32x32x16_f16 v[2:17], v[126:129], v[114:117], v[2:17]
	ds_read_b128 v[142:145], v130 offset:31744
	global_load_dwordx4 v[66:69], v[146:147], off offset:3072
	s_waitcnt vmcnt(12) lgkmcnt(3)
	v_mfma_f32_32x32x16_f16 v[50:65], v[106:109], v[118:121], v[50:65]
	s_waitcnt lgkmcnt(0)
	s_barrier
	ds_read_b128 v[106:109], v130
	ds_read_b128 v[114:117], v130 offset:4096
	v_mfma_f32_32x32x16_f16 v[34:49], v[134:137], v[118:121], v[34:49]
	ds_read_b128 v[126:129], v130 offset:8192
	v_mfma_f32_32x32x16_f16 v[18:33], v[138:141], v[118:121], v[18:33]
	v_mfma_f32_32x32x16_f16 v[2:17], v[142:145], v[118:121], v[2:17]
	ds_read_b128 v[134:137], v130 offset:12288
	ds_read_b128 v[118:121], v130 offset:1024
	s_waitcnt vmcnt(11) lgkmcnt(4)
	v_mfma_f32_32x32x16_f16 v[50:65], v[106:109], v[122:125], v[50:65]
	s_movk_i32 s2, 0x6000
	v_add_co_u32_e32 v146, vcc, s2, v132
	ds_read_b128 v[138:141], v130 offset:5120
	s_nop 0
	v_addc_co_u32_e32 v147, vcc, 0, v133, vcc
	global_load_dwordx4 v[106:109], v[146:147], off offset:-4096
	s_movk_i32 s2, 0x5000
	v_add_co_u32_e32 v148, vcc, s2, v132
	s_waitcnt lgkmcnt(4)
	v_mfma_f32_32x32x16_f16 v[34:49], v[114:117], v[122:125], v[34:49]
	v_addc_co_u32_e32 v149, vcc, 0, v133, vcc
	ds_read_b128 v[142:145], v130 offset:9216
	s_waitcnt lgkmcnt(4)
	v_mfma_f32_32x32x16_f16 v[18:33], v[126:129], v[122:125], v[18:33]
	s_waitcnt lgkmcnt(3)
	v_mfma_f32_32x32x16_f16 v[2:17], v[134:137], v[122:125], v[2:17]
	ds_read_b128 v[126:129], v130 offset:13312
	ds_read_b128 v[122:125], v130 offset:2048
	s_waitcnt vmcnt(11) lgkmcnt(4)
	v_mfma_f32_32x32x16_f16 v[50:65], v[118:121], v[102:105], v[50:65]
	global_load_dwordx4 v[114:117], v[148:149], off offset:1024
	ds_read_b128 v[134:137], v130 offset:6144
	s_waitcnt lgkmcnt(4)
	v_mfma_f32_32x32x16_f16 v[34:49], v[138:141], v[102:105], v[34:49]
	ds_read_b128 v[138:141], v130 offset:10240
	s_waitcnt lgkmcnt(4)
	v_mfma_f32_32x32x16_f16 v[18:33], v[142:145], v[102:105], v[18:33]
	s_waitcnt lgkmcnt(3)
	v_mfma_f32_32x32x16_f16 v[2:17], v[126:129], v[102:105], v[2:17]
	ds_read_b128 v[142:145], v130 offset:14336
	ds_read_b128 v[126:129], v130 offset:3072
	s_waitcnt vmcnt(11) lgkmcnt(4)
	v_mfma_f32_32x32x16_f16 v[50:65], v[122:125], v[86:89], v[50:65]
	global_load_dwordx4 v[118:121], v[148:149], off offset:2048
	ds_read_b128 v[122:125], v130 offset:7168
	s_waitcnt lgkmcnt(4)
	v_mfma_f32_32x32x16_f16 v[34:49], v[134:137], v[86:89], v[34:49]
	ds_read_b128 v[134:137], v130 offset:11264
	s_waitcnt lgkmcnt(4)
	v_mfma_f32_32x32x16_f16 v[18:33], v[138:141], v[86:89], v[18:33]
	s_waitcnt lgkmcnt(3)
	v_mfma_f32_32x32x16_f16 v[2:17], v[142:145], v[86:89], v[2:17]
	ds_read_b128 v[138:141], v130 offset:15360
	global_load_dwordx4 v[102:105], v[148:149], off offset:3072
	s_waitcnt vmcnt(12) lgkmcnt(3)
	v_mfma_f32_32x32x16_f16 v[50:65], v[126:129], v[70:73], v[50:65]
	s_waitcnt lgkmcnt(0)
	s_barrier
	ds_read_b128 v[86:89], v130 offset:16384
	ds_read_b128 v[126:129], v130 offset:20480
	v_mfma_f32_32x32x16_f16 v[34:49], v[122:125], v[70:73], v[34:49]
	ds_read_b128 v[122:125], v130 offset:24576
	v_mfma_f32_32x32x16_f16 v[18:33], v[134:137], v[70:73], v[18:33]
	v_mfma_f32_32x32x16_f16 v[2:17], v[138:141], v[70:73], v[2:17]
	ds_read_b128 v[134:137], v130 offset:28672
	ds_read_b128 v[70:73], v130 offset:17408
	s_waitcnt vmcnt(11) lgkmcnt(4)
	v_mfma_f32_32x32x16_f16 v[50:65], v[86:89], v[90:93], v[50:65]
	global_load_dwordx4 v[86:89], v[146:147], off
	ds_read_b128 v[138:141], v130 offset:21504
	s_waitcnt lgkmcnt(4)
	v_mfma_f32_32x32x16_f16 v[34:49], v[126:129], v[90:93], v[34:49]
	ds_read_b128 v[126:129], v130 offset:25600
	s_waitcnt lgkmcnt(4)
	v_mfma_f32_32x32x16_f16 v[18:33], v[122:125], v[90:93], v[18:33]
	s_waitcnt lgkmcnt(3)
	v_mfma_f32_32x32x16_f16 v[2:17], v[134:137], v[90:93], v[2:17]
	ds_read_b128 v[122:125], v130 offset:29696
	ds_read_b128 v[134:137], v130 offset:18432
	s_waitcnt vmcnt(11) lgkmcnt(4)
	v_mfma_f32_32x32x16_f16 v[50:65], v[70:73], v[94:97], v[50:65]
	global_load_dwordx4 v[90:93], v[146:147], off offset:1024
	ds_read_b128 v[70:73], v130 offset:22528
	s_waitcnt lgkmcnt(4)
	v_mfma_f32_32x32x16_f16 v[34:49], v[138:141], v[94:97], v[34:49]
	ds_read_b128 v[138:141], v130 offset:26624
	s_waitcnt lgkmcnt(4)
	v_mfma_f32_32x32x16_f16 v[18:33], v[126:129], v[94:97], v[18:33]
	s_waitcnt lgkmcnt(3)
	v_mfma_f32_32x32x16_f16 v[2:17], v[122:125], v[94:97], v[2:17]
	ds_read_b128 v[126:129], v130 offset:30720
	ds_read_b128 v[122:125], v130 offset:19456
	s_waitcnt vmcnt(11) lgkmcnt(4)
	v_mfma_f32_32x32x16_f16 v[50:65], v[134:137], v[110:113], v[50:65]
	global_load_dwordx4 v[94:97], v[146:147], off offset:2048
	ds_read_b128 v[134:137], v130 offset:23552
	s_waitcnt lgkmcnt(4)
	v_mfma_f32_32x32x16_f16 v[34:49], v[70:73], v[110:113], v[34:49]
	ds_read_b128 v[142:145], v130 offset:27648
	s_waitcnt lgkmcnt(4)
	v_mfma_f32_32x32x16_f16 v[18:33], v[138:141], v[110:113], v[18:33]
	s_waitcnt lgkmcnt(3)
	v_mfma_f32_32x32x16_f16 v[2:17], v[126:129], v[110:113], v[2:17]
	ds_read_b128 v[138:141], v130 offset:31744
	global_load_dwordx4 v[70:73], v[146:147], off offset:3072
	s_waitcnt vmcnt(12) lgkmcnt(3)
	v_mfma_f32_32x32x16_f16 v[50:65], v[122:125], v[98:101], v[50:65]
	s_waitcnt lgkmcnt(0)
	s_barrier
	ds_read_b128 v[110:113], v130
	ds_read_b128 v[122:125], v130 offset:4096
	v_mfma_f32_32x32x16_f16 v[34:49], v[134:137], v[98:101], v[34:49]
	ds_read_b128 v[126:129], v130 offset:8192
	v_mfma_f32_32x32x16_f16 v[18:33], v[142:145], v[98:101], v[18:33]
	v_mfma_f32_32x32x16_f16 v[2:17], v[138:141], v[98:101], v[2:17]
	ds_read_b128 v[134:137], v130 offset:12288
	ds_read_b128 v[98:101], v130 offset:1024
	s_waitcnt vmcnt(11) lgkmcnt(4)
	v_mfma_f32_32x32x16_f16 v[50:65], v[110:113], v[74:77], v[50:65]
	s_mov_b32 s2, 0x8000
	v_add_co_u32_e32 v146, vcc, s2, v132
	ds_read_b128 v[138:141], v130 offset:5120
	s_nop 0
	v_addc_co_u32_e32 v147, vcc, 0, v133, vcc
	global_load_dwordx4 v[110:113], v[146:147], off offset:-4096
	s_movk_i32 s2, 0x7000
	v_add_co_u32_e32 v148, vcc, s2, v132
	s_waitcnt lgkmcnt(4)
	v_mfma_f32_32x32x16_f16 v[34:49], v[122:125], v[74:77], v[34:49]
	v_addc_co_u32_e32 v149, vcc, 0, v133, vcc
	ds_read_b128 v[142:145], v130 offset:9216
	s_waitcnt lgkmcnt(4)
	v_mfma_f32_32x32x16_f16 v[18:33], v[126:129], v[74:77], v[18:33]
	s_waitcnt lgkmcnt(3)
	v_mfma_f32_32x32x16_f16 v[2:17], v[134:137], v[74:77], v[2:17]
	ds_read_b128 v[126:129], v130 offset:13312
	ds_read_b128 v[74:77], v130 offset:2048
	s_waitcnt vmcnt(11) lgkmcnt(4)
	v_mfma_f32_32x32x16_f16 v[50:65], v[98:101], v[78:81], v[50:65]
	global_load_dwordx4 v[122:125], v[148:149], off offset:1024
	ds_read_b128 v[98:101], v130 offset:6144
	s_waitcnt lgkmcnt(4)
	v_mfma_f32_32x32x16_f16 v[34:49], v[138:141], v[78:81], v[34:49]
	ds_read_b128 v[134:137], v130 offset:10240
	s_waitcnt lgkmcnt(4)
	v_mfma_f32_32x32x16_f16 v[18:33], v[142:145], v[78:81], v[18:33]
	s_waitcnt lgkmcnt(3)
	v_mfma_f32_32x32x16_f16 v[2:17], v[126:129], v[78:81], v[2:17]
	ds_read_b128 v[138:141], v130 offset:14336
	ds_read_b128 v[78:81], v130 offset:3072
	s_waitcnt vmcnt(11) lgkmcnt(4)
	v_mfma_f32_32x32x16_f16 v[50:65], v[74:77], v[82:85], v[50:65]
	global_load_dwordx4 v[126:129], v[148:149], off offset:2048
	ds_read_b128 v[74:77], v130 offset:7168
	s_waitcnt lgkmcnt(4)
	v_mfma_f32_32x32x16_f16 v[34:49], v[98:101], v[82:85], v[34:49]
	ds_read_b128 v[142:145], v130 offset:11264
	s_waitcnt lgkmcnt(4)
	v_mfma_f32_32x32x16_f16 v[18:33], v[134:137], v[82:85], v[18:33]
	s_waitcnt lgkmcnt(3)
	v_mfma_f32_32x32x16_f16 v[2:17], v[138:141], v[82:85], v[2:17]
	ds_read_b128 v[134:137], v130 offset:15360
	global_load_dwordx4 v[98:101], v[148:149], off offset:3072
	s_waitcnt vmcnt(12) lgkmcnt(3)
	v_mfma_f32_32x32x16_f16 v[50:65], v[78:81], v[66:69], v[50:65]
	s_waitcnt lgkmcnt(0)
	s_barrier
	ds_read_b128 v[78:81], v130 offset:16384
	ds_read_b128 v[82:85], v130 offset:20480
	v_mfma_f32_32x32x16_f16 v[34:49], v[74:77], v[66:69], v[34:49]
	ds_read_b128 v[138:141], v130 offset:24576
	v_mfma_f32_32x32x16_f16 v[18:33], v[142:145], v[66:69], v[18:33]
	v_mfma_f32_32x32x16_f16 v[2:17], v[134:137], v[66:69], v[2:17]
	ds_read_b128 v[142:145], v130 offset:28672
	ds_read_b128 v[66:69], v130 offset:17408
	s_waitcnt vmcnt(11) lgkmcnt(4)
	v_mfma_f32_32x32x16_f16 v[50:65], v[78:81], v[106:109], v[50:65]
	global_load_dwordx4 v[74:77], v[146:147], off
	ds_read_b128 v[134:137], v130 offset:21504
	s_waitcnt lgkmcnt(4)
	v_mfma_f32_32x32x16_f16 v[34:49], v[82:85], v[106:109], v[34:49]
	ds_read_b128 v[82:85], v130 offset:25600
	s_waitcnt lgkmcnt(4)
	v_mfma_f32_32x32x16_f16 v[18:33], v[138:141], v[106:109], v[18:33]
	s_waitcnt lgkmcnt(3)
	v_mfma_f32_32x32x16_f16 v[2:17], v[142:145], v[106:109], v[2:17]
	ds_read_b128 v[138:141], v130 offset:29696
	ds_read_b128 v[106:109], v130 offset:18432
	s_waitcnt vmcnt(11) lgkmcnt(4)
	v_mfma_f32_32x32x16_f16 v[50:65], v[66:69], v[114:117], v[50:65]
	global_load_dwordx4 v[78:81], v[146:147], off offset:1024
	ds_read_b128 v[66:69], v130 offset:22528
	s_waitcnt lgkmcnt(4)
	v_mfma_f32_32x32x16_f16 v[34:49], v[134:137], v[114:117], v[34:49]
	ds_read_b128 v[134:137], v130 offset:26624
	s_waitcnt lgkmcnt(4)
	v_mfma_f32_32x32x16_f16 v[18:33], v[82:85], v[114:117], v[18:33]
	s_waitcnt lgkmcnt(3)
	v_mfma_f32_32x32x16_f16 v[2:17], v[138:141], v[114:117], v[2:17]
	ds_read_b128 v[142:145], v130 offset:30720
	ds_read_b128 v[114:117], v130 offset:19456
	s_waitcnt vmcnt(11) lgkmcnt(4)
	v_mfma_f32_32x32x16_f16 v[50:65], v[106:109], v[118:121], v[50:65]
	global_load_dwordx4 v[82:85], v[146:147], off offset:2048
	ds_read_b128 v[106:109], v130 offset:23552
	s_waitcnt lgkmcnt(4)
	v_mfma_f32_32x32x16_f16 v[34:49], v[66:69], v[118:121], v[34:49]
	ds_read_b128 v[138:141], v130 offset:27648
	s_waitcnt lgkmcnt(4)
	v_mfma_f32_32x32x16_f16 v[18:33], v[134:137], v[118:121], v[18:33]
	s_waitcnt lgkmcnt(3)
	v_mfma_f32_32x32x16_f16 v[2:17], v[142:145], v[118:121], v[2:17]
	ds_read_b128 v[134:137], v130 offset:31744
	global_load_dwordx4 v[66:69], v[146:147], off offset:3072
	s_waitcnt vmcnt(12) lgkmcnt(3)
	v_mfma_f32_32x32x16_f16 v[50:65], v[114:117], v[102:105], v[50:65]
	s_waitcnt lgkmcnt(0)
	s_barrier
	ds_read_b128 v[114:117], v130
	ds_read_b128 v[118:121], v130 offset:4096
	v_mfma_f32_32x32x16_f16 v[34:49], v[106:109], v[102:105], v[34:49]
	ds_read_b128 v[142:145], v130 offset:8192
	v_mfma_f32_32x32x16_f16 v[18:33], v[138:141], v[102:105], v[18:33]
	v_mfma_f32_32x32x16_f16 v[2:17], v[134:137], v[102:105], v[2:17]
	ds_read_b128 v[138:141], v130 offset:12288
	ds_read_b128 v[102:105], v130 offset:1024
	s_waitcnt vmcnt(11) lgkmcnt(4)
	v_mfma_f32_32x32x16_f16 v[50:65], v[114:117], v[86:89], v[50:65]
	s_mov_b32 s2, 0xa000
	v_add_co_u32_e32 v146, vcc, s2, v132
	s_waitcnt lgkmcnt(3)
	v_mfma_f32_32x32x16_f16 v[34:49], v[118:121], v[86:89], v[34:49]
	v_addc_co_u32_e32 v147, vcc, 0, v133, vcc
	global_load_dwordx4 v[106:109], v[146:147], off offset:-4096
	ds_read_b128 v[118:121], v130 offset:5120
	s_mov_b32 s2, 0x9000
	v_add_co_u32_e32 v148, vcc, s2, v132
	s_nop 1
	v_addc_co_u32_e32 v149, vcc, 0, v133, vcc
	ds_read_b128 v[134:137], v130 offset:9216
	s_waitcnt lgkmcnt(4)
	v_mfma_f32_32x32x16_f16 v[18:33], v[142:145], v[86:89], v[18:33]
	s_waitcnt lgkmcnt(3)
	v_mfma_f32_32x32x16_f16 v[2:17], v[138:141], v[86:89], v[2:17]
	ds_read_b128 v[142:145], v130 offset:13312
	ds_read_b128 v[86:89], v130 offset:2048
	s_waitcnt vmcnt(11) lgkmcnt(4)
	v_mfma_f32_32x32x16_f16 v[50:65], v[102:105], v[90:93], v[50:65]
	global_load_dwordx4 v[114:117], v[148:149], off offset:1024
	ds_read_b128 v[102:105], v130 offset:6144
	s_waitcnt lgkmcnt(4)
	v_mfma_f32_32x32x16_f16 v[34:49], v[118:121], v[90:93], v[34:49]
	ds_read_b128 v[138:141], v130 offset:10240
	s_waitcnt lgkmcnt(4)
	v_mfma_f32_32x32x16_f16 v[18:33], v[134:137], v[90:93], v[18:33]
	s_waitcnt lgkmcnt(3)
	v_mfma_f32_32x32x16_f16 v[2:17], v[142:145], v[90:93], v[2:17]
	ds_read_b128 v[134:137], v130 offset:14336
	ds_read_b128 v[90:93], v130 offset:3072
	s_waitcnt vmcnt(11) lgkmcnt(4)
	v_mfma_f32_32x32x16_f16 v[50:65], v[86:89], v[94:97], v[50:65]
	global_load_dwordx4 v[118:121], v[148:149], off offset:2048
	ds_read_b128 v[86:89], v130 offset:7168
	s_waitcnt lgkmcnt(4)
	v_mfma_f32_32x32x16_f16 v[34:49], v[102:105], v[94:97], v[34:49]
	ds_read_b128 v[142:145], v130 offset:11264
	s_waitcnt lgkmcnt(4)
	v_mfma_f32_32x32x16_f16 v[18:33], v[138:141], v[94:97], v[18:33]
	s_waitcnt lgkmcnt(3)
	v_mfma_f32_32x32x16_f16 v[2:17], v[134:137], v[94:97], v[2:17]
	ds_read_b128 v[138:141], v130 offset:15360
	global_load_dwordx4 v[102:105], v[148:149], off offset:3072
	s_waitcnt vmcnt(12) lgkmcnt(3)
	v_mfma_f32_32x32x16_f16 v[50:65], v[90:93], v[70:73], v[50:65]
	s_waitcnt lgkmcnt(0)
	s_barrier
	ds_read_b128 v[90:93], v130 offset:16384
	ds_read_b128 v[94:97], v130 offset:20480
	v_mfma_f32_32x32x16_f16 v[34:49], v[86:89], v[70:73], v[34:49]
	ds_read_b128 v[134:137], v130 offset:24576
	v_mfma_f32_32x32x16_f16 v[18:33], v[142:145], v[70:73], v[18:33]
	v_mfma_f32_32x32x16_f16 v[2:17], v[138:141], v[70:73], v[2:17]
	ds_read_b128 v[142:145], v130 offset:28672
	ds_read_b128 v[70:73], v130 offset:17408
	s_waitcnt vmcnt(11) lgkmcnt(4)
	v_mfma_f32_32x32x16_f16 v[50:65], v[90:93], v[110:113], v[50:65]
	global_load_dwordx4 v[86:89], v[146:147], off
	ds_read_b128 v[138:141], v130 offset:21504
	s_waitcnt lgkmcnt(4)
	v_mfma_f32_32x32x16_f16 v[34:49], v[94:97], v[110:113], v[34:49]
	ds_read_b128 v[94:97], v130 offset:25600
	s_waitcnt lgkmcnt(4)
	v_mfma_f32_32x32x16_f16 v[18:33], v[134:137], v[110:113], v[18:33]
	s_waitcnt lgkmcnt(3)
	v_mfma_f32_32x32x16_f16 v[2:17], v[142:145], v[110:113], v[2:17]
	ds_read_b128 v[134:137], v130 offset:29696
	ds_read_b128 v[110:113], v130 offset:18432
	s_waitcnt vmcnt(11) lgkmcnt(4)
	v_mfma_f32_32x32x16_f16 v[50:65], v[70:73], v[122:125], v[50:65]
	global_load_dwordx4 v[90:93], v[146:147], off offset:1024
	ds_read_b128 v[70:73], v130 offset:22528
	s_waitcnt lgkmcnt(4)
	v_mfma_f32_32x32x16_f16 v[34:49], v[138:141], v[122:125], v[34:49]
	ds_read_b128 v[138:141], v130 offset:26624
	s_waitcnt lgkmcnt(4)
	v_mfma_f32_32x32x16_f16 v[18:33], v[94:97], v[122:125], v[18:33]
	s_waitcnt lgkmcnt(3)
	v_mfma_f32_32x32x16_f16 v[2:17], v[134:137], v[122:125], v[2:17]
	ds_read_b128 v[142:145], v130 offset:30720
	ds_read_b128 v[122:125], v130 offset:19456
	s_waitcnt vmcnt(11) lgkmcnt(4)
	v_mfma_f32_32x32x16_f16 v[50:65], v[110:113], v[126:129], v[50:65]
	global_load_dwordx4 v[94:97], v[146:147], off offset:2048
	ds_read_b128 v[110:113], v130 offset:23552
	s_waitcnt lgkmcnt(4)
	v_mfma_f32_32x32x16_f16 v[34:49], v[70:73], v[126:129], v[34:49]
	ds_read_b128 v[134:137], v130 offset:27648
	s_waitcnt lgkmcnt(4)
	v_mfma_f32_32x32x16_f16 v[18:33], v[138:141], v[126:129], v[18:33]
	s_waitcnt lgkmcnt(3)
	v_mfma_f32_32x32x16_f16 v[2:17], v[142:145], v[126:129], v[2:17]
	ds_read_b128 v[138:141], v130 offset:31744
	global_load_dwordx4 v[70:73], v[146:147], off offset:3072
	s_waitcnt vmcnt(12) lgkmcnt(3)
	v_mfma_f32_32x32x16_f16 v[50:65], v[122:125], v[98:101], v[50:65]
	s_waitcnt lgkmcnt(0)
	s_barrier
	ds_read_b128 v[122:125], v130
	ds_read_b128 v[126:129], v130 offset:4096
	v_mfma_f32_32x32x16_f16 v[34:49], v[110:113], v[98:101], v[34:49]
	ds_read_b128 v[142:145], v130 offset:8192
	v_mfma_f32_32x32x16_f16 v[18:33], v[134:137], v[98:101], v[18:33]
	v_mfma_f32_32x32x16_f16 v[2:17], v[138:141], v[98:101], v[2:17]
	ds_read_b128 v[134:137], v130 offset:12288
	ds_read_b128 v[98:101], v130 offset:1024
	s_waitcnt vmcnt(11) lgkmcnt(4)
	v_mfma_f32_32x32x16_f16 v[50:65], v[122:125], v[74:77], v[50:65]
	s_mov_b32 s2, 0xc000
	v_add_co_u32_e32 v146, vcc, s2, v132
	s_waitcnt lgkmcnt(3)
	v_mfma_f32_32x32x16_f16 v[34:49], v[126:129], v[74:77], v[34:49]
	v_addc_co_u32_e32 v147, vcc, 0, v133, vcc
	global_load_dwordx4 v[110:113], v[146:147], off offset:-4096
	ds_read_b128 v[126:129], v130 offset:5120
	s_mov_b32 s2, 0xb000
	v_add_co_u32_e32 v148, vcc, s2, v132
	s_nop 1
	v_addc_co_u32_e32 v149, vcc, 0, v133, vcc
	ds_read_b128 v[138:141], v130 offset:9216
	s_waitcnt lgkmcnt(4)
	v_mfma_f32_32x32x16_f16 v[18:33], v[142:145], v[74:77], v[18:33]
	s_waitcnt lgkmcnt(3)
	v_mfma_f32_32x32x16_f16 v[2:17], v[134:137], v[74:77], v[2:17]
	ds_read_b128 v[142:145], v130 offset:13312
	ds_read_b128 v[74:77], v130 offset:2048
	s_waitcnt vmcnt(11) lgkmcnt(4)
	v_mfma_f32_32x32x16_f16 v[50:65], v[98:101], v[78:81], v[50:65]
	global_load_dwordx4 v[122:125], v[148:149], off offset:1024
	ds_read_b128 v[98:101], v130 offset:6144
	s_waitcnt lgkmcnt(4)
	v_mfma_f32_32x32x16_f16 v[34:49], v[126:129], v[78:81], v[34:49]
	ds_read_b128 v[134:137], v130 offset:10240
	s_waitcnt lgkmcnt(4)
	v_mfma_f32_32x32x16_f16 v[18:33], v[138:141], v[78:81], v[18:33]
	s_waitcnt lgkmcnt(3)
	v_mfma_f32_32x32x16_f16 v[2:17], v[142:145], v[78:81], v[2:17]
	ds_read_b128 v[138:141], v130 offset:14336
	ds_read_b128 v[78:81], v130 offset:3072
	s_waitcnt vmcnt(11) lgkmcnt(4)
	v_mfma_f32_32x32x16_f16 v[50:65], v[74:77], v[82:85], v[50:65]
	global_load_dwordx4 v[126:129], v[148:149], off offset:2048
	ds_read_b128 v[142:145], v130 offset:7168
	s_waitcnt lgkmcnt(4)
	v_mfma_f32_32x32x16_f16 v[34:49], v[98:101], v[82:85], v[34:49]
	ds_read_b128 v[98:101], v130 offset:11264
	s_waitcnt lgkmcnt(4)
	v_mfma_f32_32x32x16_f16 v[18:33], v[134:137], v[82:85], v[18:33]
	s_waitcnt lgkmcnt(3)
	v_mfma_f32_32x32x16_f16 v[2:17], v[138:141], v[82:85], v[2:17]
	ds_read_b128 v[134:137], v130 offset:15360
	global_load_dwordx4 v[74:77], v[148:149], off offset:3072
	s_waitcnt vmcnt(12) lgkmcnt(3)
	v_mfma_f32_32x32x16_f16 v[50:65], v[78:81], v[66:69], v[50:65]
	s_waitcnt lgkmcnt(0)
	s_barrier
	ds_read_b128 v[78:81], v130 offset:16384
	ds_read_b128 v[82:85], v130 offset:20480
	v_mfma_f32_32x32x16_f16 v[34:49], v[142:145], v[66:69], v[34:49]
	ds_read_b128 v[138:141], v130 offset:24576
	v_mfma_f32_32x32x16_f16 v[18:33], v[98:101], v[66:69], v[18:33]
	v_mfma_f32_32x32x16_f16 v[2:17], v[134:137], v[66:69], v[2:17]
	ds_read_b128 v[98:101], v130 offset:28672
	ds_read_b128 v[66:69], v130 offset:17408
	s_waitcnt vmcnt(11) lgkmcnt(4)
	v_mfma_f32_32x32x16_f16 v[50:65], v[78:81], v[106:109], v[50:65]
	global_load_dwordx4 v[78:81], v[146:147], off
	ds_read_b128 v[134:137], v130 offset:21504
	s_waitcnt lgkmcnt(4)
	v_mfma_f32_32x32x16_f16 v[34:49], v[82:85], v[106:109], v[34:49]
	ds_read_b128 v[142:145], v130 offset:25600
	s_waitcnt lgkmcnt(4)
	v_mfma_f32_32x32x16_f16 v[18:33], v[138:141], v[106:109], v[18:33]
	s_waitcnt lgkmcnt(3)
	v_mfma_f32_32x32x16_f16 v[2:17], v[98:101], v[106:109], v[2:17]
	ds_read_b128 v[138:141], v130 offset:29696
	ds_read_b128 v[98:101], v130 offset:18432
	s_waitcnt vmcnt(11) lgkmcnt(4)
	v_mfma_f32_32x32x16_f16 v[50:65], v[66:69], v[114:117], v[50:65]
	global_load_dwordx4 v[82:85], v[146:147], off offset:1024
	ds_read_b128 v[66:69], v130 offset:22528
	s_waitcnt lgkmcnt(4)
	v_mfma_f32_32x32x16_f16 v[34:49], v[134:137], v[114:117], v[34:49]
	ds_read_b128 v[106:109], v130 offset:26624
	s_waitcnt lgkmcnt(4)
	v_mfma_f32_32x32x16_f16 v[18:33], v[142:145], v[114:117], v[18:33]
	s_waitcnt lgkmcnt(3)
	v_mfma_f32_32x32x16_f16 v[2:17], v[138:141], v[114:117], v[2:17]
	ds_read_b128 v[134:137], v130 offset:30720
	ds_read_b128 v[114:117], v130 offset:19456
	s_waitcnt vmcnt(11) lgkmcnt(4)
	v_mfma_f32_32x32x16_f16 v[50:65], v[98:101], v[118:121], v[50:65]
	global_load_dwordx4 v[98:101], v[146:147], off offset:2048
	ds_read_b128 v[138:141], v130 offset:23552
	s_waitcnt lgkmcnt(4)
	v_mfma_f32_32x32x16_f16 v[34:49], v[66:69], v[118:121], v[34:49]
	ds_read_b128 v[142:145], v130 offset:27648
	s_waitcnt lgkmcnt(4)
	v_mfma_f32_32x32x16_f16 v[18:33], v[106:109], v[118:121], v[18:33]
	s_waitcnt lgkmcnt(3)
	v_mfma_f32_32x32x16_f16 v[2:17], v[134:137], v[118:121], v[2:17]
	ds_read_b128 v[106:109], v130 offset:31744
	global_load_dwordx4 v[66:69], v[146:147], off offset:3072
	s_waitcnt vmcnt(12) lgkmcnt(3)
	v_mfma_f32_32x32x16_f16 v[50:65], v[114:117], v[102:105], v[50:65]
	s_waitcnt lgkmcnt(0)
	s_barrier
	ds_read_b128 v[114:117], v130
	ds_read_b128 v[118:121], v130 offset:4096
	v_mfma_f32_32x32x16_f16 v[34:49], v[138:141], v[102:105], v[34:49]
	ds_read_b128 v[134:137], v130 offset:8192
	v_mfma_f32_32x32x16_f16 v[18:33], v[142:145], v[102:105], v[18:33]
	v_mfma_f32_32x32x16_f16 v[2:17], v[106:109], v[102:105], v[2:17]
	ds_read_b128 v[138:141], v130 offset:12288
	ds_read_b128 v[106:109], v130 offset:1024
	s_waitcnt vmcnt(11) lgkmcnt(4)
	v_mfma_f32_32x32x16_f16 v[50:65], v[114:117], v[86:89], v[50:65]
	s_mov_b32 s2, 0xe000
	v_add_co_u32_e32 v146, vcc, s2, v132
	ds_read_b128 v[114:117], v130 offset:5120
	s_nop 0
	v_addc_co_u32_e32 v147, vcc, 0, v133, vcc
	global_load_dwordx4 v[102:105], v[146:147], off offset:-4096
	s_mov_b32 s2, 0xd000
	v_add_co_u32_e32 v148, vcc, s2, v132
	s_waitcnt lgkmcnt(4)
	v_mfma_f32_32x32x16_f16 v[34:49], v[118:121], v[86:89], v[34:49]
	v_addc_co_u32_e32 v149, vcc, 0, v133, vcc
	ds_read_b128 v[118:121], v130 offset:9216
	s_waitcnt lgkmcnt(4)
	v_mfma_f32_32x32x16_f16 v[18:33], v[134:137], v[86:89], v[18:33]
	s_waitcnt lgkmcnt(3)
	v_mfma_f32_32x32x16_f16 v[2:17], v[138:141], v[86:89], v[2:17]
	ds_read_b128 v[134:137], v130 offset:13312
	ds_read_b128 v[86:89], v130 offset:2048
	s_waitcnt vmcnt(11) lgkmcnt(4)
	v_mfma_f32_32x32x16_f16 v[50:65], v[106:109], v[90:93], v[50:65]
	global_load_dwordx4 v[106:109], v[148:149], off offset:1024
	ds_read_b128 v[138:141], v130 offset:6144
	s_waitcnt lgkmcnt(4)
	v_mfma_f32_32x32x16_f16 v[34:49], v[114:117], v[90:93], v[34:49]
	ds_read_b128 v[114:117], v130 offset:10240
	s_waitcnt lgkmcnt(4)
	v_mfma_f32_32x32x16_f16 v[18:33], v[118:121], v[90:93], v[18:33]
	s_waitcnt lgkmcnt(3)
	v_mfma_f32_32x32x16_f16 v[2:17], v[134:137], v[90:93], v[2:17]
	ds_read_b128 v[118:121], v130 offset:14336
	ds_read_b128 v[134:137], v130 offset:3072
	s_waitcnt vmcnt(11) lgkmcnt(4)
	v_mfma_f32_32x32x16_f16 v[50:65], v[86:89], v[94:97], v[50:65]
	global_load_dwordx4 v[90:93], v[148:149], off offset:2048
	ds_read_b128 v[142:145], v130 offset:7168
	s_waitcnt lgkmcnt(4)
	v_mfma_f32_32x32x16_f16 v[34:49], v[138:141], v[94:97], v[34:49]
	ds_read_b128 v[138:141], v130 offset:11264
	s_waitcnt lgkmcnt(4)
	v_mfma_f32_32x32x16_f16 v[18:33], v[114:117], v[94:97], v[18:33]
	s_waitcnt lgkmcnt(3)
	v_mfma_f32_32x32x16_f16 v[2:17], v[118:121], v[94:97], v[2:17]
	ds_read_b128 v[114:117], v130 offset:15360
	global_load_dwordx4 v[86:89], v[148:149], off offset:3072
	s_waitcnt vmcnt(12) lgkmcnt(3)
	v_mfma_f32_32x32x16_f16 v[50:65], v[134:137], v[70:73], v[50:65]
	s_waitcnt lgkmcnt(0)
	s_barrier
	ds_read_b128 v[94:97], v130 offset:16384
	ds_read_b128 v[118:121], v130 offset:20480
	v_mfma_f32_32x32x16_f16 v[34:49], v[142:145], v[70:73], v[34:49]
	ds_read_b128 v[134:137], v130 offset:24576
	v_mfma_f32_32x32x16_f16 v[18:33], v[138:141], v[70:73], v[18:33]
	v_mfma_f32_32x32x16_f16 v[2:17], v[114:117], v[70:73], v[2:17]
	ds_read_b128 v[138:141], v130 offset:28672
	ds_read_b128 v[70:73], v130 offset:17408
	s_waitcnt vmcnt(11) lgkmcnt(4)
	v_mfma_f32_32x32x16_f16 v[50:65], v[94:97], v[110:113], v[50:65]
	global_load_dwordx4 v[94:97], v[146:147], off
	ds_read_b128 v[114:117], v130 offset:21504
	s_waitcnt lgkmcnt(4)
	v_mfma_f32_32x32x16_f16 v[34:49], v[118:121], v[110:113], v[34:49]
	ds_read_b128 v[118:121], v130 offset:25600
	s_waitcnt lgkmcnt(4)
	v_mfma_f32_32x32x16_f16 v[18:33], v[134:137], v[110:113], v[18:33]
	s_waitcnt lgkmcnt(3)
	v_mfma_f32_32x32x16_f16 v[2:17], v[138:141], v[110:113], v[2:17]
	ds_read_b128 v[134:137], v130 offset:29696
	ds_read_b128 v[138:141], v130 offset:18432
	s_waitcnt vmcnt(11) lgkmcnt(4)
	v_mfma_f32_32x32x16_f16 v[50:65], v[70:73], v[122:125], v[50:65]
	global_load_dwordx4 v[110:113], v[146:147], off offset:1024
	ds_read_b128 v[70:73], v130 offset:22528
	s_waitcnt lgkmcnt(4)
	v_mfma_f32_32x32x16_f16 v[34:49], v[114:117], v[122:125], v[34:49]
	ds_read_b128 v[142:145], v130 offset:26624
	s_waitcnt lgkmcnt(4)
	v_mfma_f32_32x32x16_f16 v[18:33], v[118:121], v[122:125], v[18:33]
	s_waitcnt lgkmcnt(3)
	v_mfma_f32_32x32x16_f16 v[2:17], v[134:137], v[122:125], v[2:17]
	ds_read_b128 v[118:121], v130 offset:30720
	ds_read_b128 v[122:125], v130 offset:19456
	s_waitcnt vmcnt(11) lgkmcnt(4)
	v_mfma_f32_32x32x16_f16 v[50:65], v[138:141], v[126:129], v[50:65]
	global_load_dwordx4 v[114:117], v[146:147], off offset:2048
	ds_read_b128 v[134:137], v130 offset:23552
	s_waitcnt lgkmcnt(4)
	v_mfma_f32_32x32x16_f16 v[34:49], v[70:73], v[126:129], v[34:49]
	ds_read_b128 v[138:141], v130 offset:27648
	s_waitcnt lgkmcnt(4)
	v_mfma_f32_32x32x16_f16 v[18:33], v[142:145], v[126:129], v[18:33]
	s_waitcnt lgkmcnt(3)
	v_mfma_f32_32x32x16_f16 v[2:17], v[118:121], v[126:129], v[2:17]
	ds_read_b128 v[142:145], v130 offset:31744
	global_load_dwordx4 v[70:73], v[146:147], off offset:3072
	s_waitcnt vmcnt(12) lgkmcnt(3)
	v_mfma_f32_32x32x16_f16 v[50:65], v[122:125], v[74:77], v[50:65]
	s_waitcnt lgkmcnt(0)
	s_barrier
	ds_read_b128 v[118:121], v130
	ds_read_b128 v[122:125], v130 offset:4096
	v_mfma_f32_32x32x16_f16 v[34:49], v[134:137], v[74:77], v[34:49]
	ds_read_b128 v[126:129], v130 offset:8192
	v_mfma_f32_32x32x16_f16 v[18:33], v[138:141], v[74:77], v[18:33]
	v_mfma_f32_32x32x16_f16 v[2:17], v[142:145], v[74:77], v[2:17]
	ds_read_b128 v[134:137], v130 offset:12288
	ds_read_b128 v[138:141], v130 offset:1024
	s_waitcnt vmcnt(11) lgkmcnt(4)
	v_mfma_f32_32x32x16_f16 v[50:65], v[118:121], v[78:81], v[50:65]
	s_mov_b32 s2, 0xf000
	v_add_co_u32_e32 v142, vcc, s2, v132
	ds_read_b128 v[118:121], v130 offset:5120
	s_nop 0
	v_addc_co_u32_e32 v143, vcc, 0, v133, vcc
	global_load_dwordx4 v[74:77], v[142:143], off
	s_waitcnt lgkmcnt(4)
	v_mfma_f32_32x32x16_f16 v[34:49], v[122:125], v[78:81], v[34:49]
	ds_read_b128 v[122:125], v130 offset:9216
	s_waitcnt lgkmcnt(4)
	v_mfma_f32_32x32x16_f16 v[18:33], v[126:129], v[78:81], v[18:33]
	s_waitcnt lgkmcnt(3)
	v_mfma_f32_32x32x16_f16 v[2:17], v[134:137], v[78:81], v[2:17]
	ds_read_b128 v[126:129], v130 offset:13312
	ds_read_b128 v[132:135], v130 offset:2048
	s_waitcnt vmcnt(11) lgkmcnt(4)
	v_mfma_f32_32x32x16_f16 v[50:65], v[138:141], v[82:85], v[50:65]
	global_load_dwordx4 v[78:81], v[142:143], off offset:1024
	ds_read_b128 v[136:139], v130 offset:6144
	s_waitcnt lgkmcnt(4)
	v_mfma_f32_32x32x16_f16 v[34:49], v[118:121], v[82:85], v[34:49]
	ds_read_b128 v[118:121], v130 offset:10240
	s_waitcnt lgkmcnt(4)
	v_mfma_f32_32x32x16_f16 v[18:33], v[122:125], v[82:85], v[18:33]
	s_waitcnt lgkmcnt(3)
	v_mfma_f32_32x32x16_f16 v[2:17], v[126:129], v[82:85], v[2:17]
	ds_read_b128 v[122:125], v130 offset:14336
	ds_read_b128 v[126:129], v130 offset:3072
	s_waitcnt vmcnt(11) lgkmcnt(4)
	v_mfma_f32_32x32x16_f16 v[50:65], v[132:135], v[98:101], v[50:65]
	global_load_dwordx4 v[82:85], v[142:143], off offset:2048
	ds_read_b128 v[132:135], v130 offset:7168
	s_waitcnt lgkmcnt(4)
	v_mfma_f32_32x32x16_f16 v[34:49], v[136:139], v[98:101], v[34:49]
	ds_read_b128 v[136:139], v130 offset:11264
	s_waitcnt lgkmcnt(4)
	v_mfma_f32_32x32x16_f16 v[18:33], v[118:121], v[98:101], v[18:33]
	s_waitcnt lgkmcnt(3)
	v_mfma_f32_32x32x16_f16 v[2:17], v[122:125], v[98:101], v[2:17]
	ds_read_b128 v[118:121], v130 offset:15360
	global_load_dwordx4 v[98:101], v[142:143], off offset:3072
	s_waitcnt vmcnt(12) lgkmcnt(3)
	v_mfma_f32_32x32x16_f16 v[50:65], v[126:129], v[66:69], v[50:65]
	s_waitcnt lgkmcnt(0)
	s_barrier
	ds_read_b128 v[122:125], v130 offset:16384
	ds_read_b128 v[126:129], v130 offset:20480
	v_mfma_f32_32x32x16_f16 v[34:49], v[132:135], v[66:69], v[34:49]
	ds_read_b128 v[132:135], v130 offset:24576
	v_mfma_f32_32x32x16_f16 v[18:33], v[136:139], v[66:69], v[18:33]
	v_mfma_f32_32x32x16_f16 v[2:17], v[118:121], v[66:69], v[2:17]
	ds_read_b128 v[136:139], v130 offset:28672
	ds_read_b128 v[66:69], v130 offset:17408
	s_waitcnt vmcnt(11) lgkmcnt(4)
	v_mfma_f32_32x32x16_f16 v[50:65], v[122:125], v[102:105], v[50:65]
	ds_read_b128 v[118:121], v130 offset:21504
	s_waitcnt lgkmcnt(4)
	v_mfma_f32_32x32x16_f16 v[34:49], v[126:129], v[102:105], v[34:49]
	ds_read_b128 v[122:125], v130 offset:25600
	s_waitcnt lgkmcnt(4)
	v_mfma_f32_32x32x16_f16 v[18:33], v[132:135], v[102:105], v[18:33]
	s_waitcnt lgkmcnt(3)
	v_mfma_f32_32x32x16_f16 v[2:17], v[136:139], v[102:105], v[2:17]
	ds_read_b128 v[126:129], v130 offset:29696
	s_waitcnt vmcnt(10) lgkmcnt(3)
	v_mfma_f32_32x32x16_f16 v[50:65], v[66:69], v[106:109], v[50:65]
	ds_read_b128 v[66:69], v130 offset:18432
	ds_read_b128 v[102:105], v130 offset:22528
	s_waitcnt lgkmcnt(4)
	v_mfma_f32_32x32x16_f16 v[34:49], v[118:121], v[106:109], v[34:49]
	ds_read_b128 v[118:121], v130 offset:26624
	s_waitcnt lgkmcnt(4)
	v_mfma_f32_32x32x16_f16 v[18:33], v[122:125], v[106:109], v[18:33]
	s_waitcnt lgkmcnt(3)
	v_mfma_f32_32x32x16_f16 v[2:17], v[126:129], v[106:109], v[2:17]
	ds_read_b128 v[106:109], v130 offset:30720
	ds_read_b128 v[122:125], v130 offset:19456
	s_waitcnt vmcnt(9) lgkmcnt(4)
	v_mfma_f32_32x32x16_f16 v[50:65], v[66:69], v[90:93], v[50:65]
	ds_read_b128 v[66:69], v130 offset:23552
	s_waitcnt lgkmcnt(4)
	v_mfma_f32_32x32x16_f16 v[34:49], v[102:105], v[90:93], v[34:49]
	ds_read_b128 v[102:105], v130 offset:27648
	s_waitcnt lgkmcnt(4)
	v_mfma_f32_32x32x16_f16 v[18:33], v[118:121], v[90:93], v[18:33]
	s_waitcnt lgkmcnt(3)
	v_mfma_f32_32x32x16_f16 v[2:17], v[106:109], v[90:93], v[2:17]
	ds_read_b128 v[118:121], v130 offset:31744
	s_waitcnt vmcnt(8) lgkmcnt(3)
	v_mfma_f32_32x32x16_f16 v[50:65], v[122:125], v[86:89], v[50:65]
	s_waitcnt lgkmcnt(0)
	s_barrier
	ds_read_b128 v[90:93], v130
	ds_read_b128 v[106:109], v130 offset:4096
	v_mfma_f32_32x32x16_f16 v[34:49], v[66:69], v[86:89], v[34:49]
	ds_read_b128 v[66:69], v130 offset:8192
	v_mfma_f32_32x32x16_f16 v[18:33], v[102:105], v[86:89], v[18:33]
	v_mfma_f32_32x32x16_f16 v[2:17], v[118:121], v[86:89], v[2:17]
	ds_read_b128 v[102:105], v130 offset:12288
	ds_read_b128 v[86:89], v130 offset:1024
	s_waitcnt vmcnt(7) lgkmcnt(4)
	v_mfma_f32_32x32x16_f16 v[50:65], v[90:93], v[94:97], v[50:65]
	ds_read_b128 v[90:93], v130 offset:5120
	s_waitcnt lgkmcnt(4)
	v_mfma_f32_32x32x16_f16 v[34:49], v[106:109], v[94:97], v[34:49]
	ds_read_b128 v[106:109], v130 offset:9216
	s_waitcnt lgkmcnt(4)
	v_mfma_f32_32x32x16_f16 v[18:33], v[66:69], v[94:97], v[18:33]
	s_waitcnt lgkmcnt(3)
	v_mfma_f32_32x32x16_f16 v[2:17], v[102:105], v[94:97], v[2:17]
	ds_read_b128 v[66:69], v130 offset:13312
	ds_read_b128 v[94:97], v130 offset:2048
	s_waitcnt vmcnt(6) lgkmcnt(4)
	v_mfma_f32_32x32x16_f16 v[50:65], v[86:89], v[110:113], v[50:65]
	ds_read_b128 v[86:89], v130 offset:6144
	s_waitcnt lgkmcnt(4)
	v_mfma_f32_32x32x16_f16 v[34:49], v[90:93], v[110:113], v[34:49]
	ds_read_b128 v[90:93], v130 offset:10240
	s_waitcnt lgkmcnt(4)
	v_mfma_f32_32x32x16_f16 v[18:33], v[106:109], v[110:113], v[18:33]
	s_waitcnt lgkmcnt(3)
	v_mfma_f32_32x32x16_f16 v[2:17], v[66:69], v[110:113], v[2:17]
	ds_read_b128 v[102:105], v130 offset:14336
	ds_read_b128 v[66:69], v130 offset:3072
	s_waitcnt vmcnt(5) lgkmcnt(4)
	v_mfma_f32_32x32x16_f16 v[50:65], v[94:97], v[114:117], v[50:65]
	ds_read_b128 v[94:97], v130 offset:7168
	s_waitcnt lgkmcnt(4)
	v_mfma_f32_32x32x16_f16 v[34:49], v[86:89], v[114:117], v[34:49]
	ds_read_b128 v[86:89], v130 offset:11264
	s_waitcnt lgkmcnt(4)
	v_mfma_f32_32x32x16_f16 v[18:33], v[90:93], v[114:117], v[18:33]
	s_waitcnt lgkmcnt(3)
	v_mfma_f32_32x32x16_f16 v[2:17], v[102:105], v[114:117], v[2:17]
	ds_read_b128 v[90:93], v130 offset:15360
	s_waitcnt vmcnt(4) lgkmcnt(3)
	v_mfma_f32_32x32x16_f16 v[50:65], v[66:69], v[70:73], v[50:65]
	s_waitcnt lgkmcnt(0)
	s_barrier
	ds_read_b128 v[66:69], v130 offset:16384
	ds_read_b128 v[102:105], v130 offset:20480
	v_mfma_f32_32x32x16_f16 v[34:49], v[94:97], v[70:73], v[34:49]
	ds_read_b128 v[94:97], v130 offset:24576
	v_mfma_f32_32x32x16_f16 v[18:33], v[86:89], v[70:73], v[18:33]
	v_mfma_f32_32x32x16_f16 v[2:17], v[90:93], v[70:73], v[2:17]
	ds_read_b128 v[86:89], v130 offset:28672
	ds_read_b128 v[70:73], v130 offset:17408
	s_waitcnt vmcnt(3) lgkmcnt(4)
	v_mfma_f32_32x32x16_f16 v[50:65], v[66:69], v[74:77], v[50:65]
	ds_read_b128 v[66:69], v130 offset:21504
	s_waitcnt lgkmcnt(4)
	v_mfma_f32_32x32x16_f16 v[34:49], v[102:105], v[74:77], v[34:49]
	ds_read_b128 v[90:93], v130 offset:25600
	s_waitcnt lgkmcnt(4)
	v_mfma_f32_32x32x16_f16 v[18:33], v[94:97], v[74:77], v[18:33]
	s_waitcnt lgkmcnt(3)
	v_mfma_f32_32x32x16_f16 v[2:17], v[86:89], v[74:77], v[2:17]
	ds_read_b128 v[94:97], v130 offset:29696
	ds_read_b128 v[74:77], v130 offset:18432
	s_waitcnt vmcnt(2) lgkmcnt(4)
	v_mfma_f32_32x32x16_f16 v[50:65], v[70:73], v[78:81], v[50:65]
	ds_read_b128 v[70:73], v130 offset:22528
	s_waitcnt lgkmcnt(4)
	v_mfma_f32_32x32x16_f16 v[34:49], v[66:69], v[78:81], v[34:49]
	ds_read_b128 v[66:69], v130 offset:26624
	s_waitcnt lgkmcnt(4)
	v_mfma_f32_32x32x16_f16 v[18:33], v[90:93], v[78:81], v[18:33]
	s_waitcnt lgkmcnt(3)
	v_mfma_f32_32x32x16_f16 v[2:17], v[94:97], v[78:81], v[2:17]
	ds_read_b128 v[86:89], v130 offset:30720
	ds_read_b128 v[78:81], v130 offset:19456
	s_waitcnt vmcnt(1) lgkmcnt(4)
	v_mfma_f32_32x32x16_f16 v[50:65], v[74:77], v[82:85], v[50:65]
	ds_read_b128 v[74:77], v130 offset:23552
	s_waitcnt lgkmcnt(4)
	v_mfma_f32_32x32x16_f16 v[34:49], v[70:73], v[82:85], v[34:49]
	ds_read_b128 v[70:73], v130 offset:27648
	s_waitcnt lgkmcnt(4)
	v_mfma_f32_32x32x16_f16 v[18:33], v[66:69], v[82:85], v[18:33]
	s_waitcnt lgkmcnt(3)
	v_mfma_f32_32x32x16_f16 v[2:17], v[86:89], v[82:85], v[2:17]
	ds_read_b128 v[66:69], v130 offset:31744
	s_waitcnt vmcnt(0) lgkmcnt(3)
	v_mfma_f32_32x32x16_f16 v[50:65], v[78:81], v[98:101], v[50:65]
	s_waitcnt lgkmcnt(2)
	v_mfma_f32_32x32x16_f16 v[34:49], v[74:77], v[98:101], v[34:49]
	s_waitcnt lgkmcnt(1)
	v_mfma_f32_32x32x16_f16 v[18:33], v[70:73], v[98:101], v[18:33]
	s_waitcnt lgkmcnt(0)
	v_mfma_f32_32x32x16_f16 v[2:17], v[66:69], v[98:101], v[2:17]
	v_lshrrev_b32_e32 v66, 1, v0
	v_and_b32_e32 v66, 16, v66
	ds_read_b128 v[68:71], v66 offset:32768
	ds_read_b128 v[72:75], v66 offset:32800
	ds_read_b128 v[76:79], v66 offset:32832
	s_mov_b32 s2, 0x4038aa3b
	s_waitcnt lgkmcnt(1)
	v_pk_fma_f32 v[72:73], v[54:55], s[2:3], v[72:73] op_sel_hi:[1,0,1]
	v_pk_fma_f32 v[68:69], v[50:51], s[2:3], v[68:69] op_sel_hi:[1,0,1]
	v_pk_fma_f32 v[70:71], v[52:53], s[2:3], v[70:71] op_sel_hi:[1,0,1]
	ds_read_b128 v[50:53], v66 offset:32864
	v_exp_f32_e32 v54, v68
	v_exp_f32_e32 v55, v69
	v_pk_fma_f32 v[74:75], v[56:57], s[2:3], v[74:75] op_sel_hi:[1,0,1]
	v_exp_f32_e32 v56, v70
	v_exp_f32_e32 v57, v71
	v_pk_add_f32 v[54:55], v[54:55], 1.0 op_sel_hi:[1,0]
	s_waitcnt lgkmcnt(1)
	v_pk_fma_f32 v[58:59], v[58:59], s[2:3], v[76:77] op_sel_hi:[1,0,1]
	s_waitcnt lgkmcnt(0)
	v_pk_fma_f32 v[76:77], v[62:63], s[2:3], v[50:51] op_sel_hi:[1,0,1]
	v_pk_fma_f32 v[64:65], v[64:65], s[2:3], v[52:53] op_sel_hi:[1,0,1]
	ds_read_b128 v[50:53], v66 offset:33280
	v_rcp_f32_e32 v62, v54
	v_rcp_f32_e32 v63, v55
	v_pk_add_f32 v[54:55], v[56:57], 1.0 op_sel_hi:[1,0]
	v_pk_fma_f32 v[60:61], v[60:61], s[2:3], v[78:79] op_sel_hi:[1,0,1]
	v_rcp_f32_e32 v68, v54
	v_rcp_f32_e32 v69, v55
	v_pk_fma_f32 v[70:71], v[62:63], 2.0, 1.0 op_sel_hi:[1,0,0] neg_lo:[1,0,0] neg_hi:[1,0,0]
	ds_read_b128 v[54:57], v66 offset:33312
	s_waitcnt lgkmcnt(1)
	v_pk_fma_f32 v[70:71], v[50:51], v[70:71], 0 op_sel_hi:[1,1,0]
	v_pk_fma_f32 v[78:79], v[68:69], 2.0, 1.0 op_sel_hi:[1,0,0] neg_lo:[1,0,0] neg_hi:[1,0,0]
	v_pk_fma_f32 v[62:63], v[62:63], v[62:63], v[62:63] neg_lo:[1,0,0] neg_hi:[1,0,0]
	v_pk_mul_f32 v[50:51], v[50:51], 4.0 op_sel_hi:[1,0]
	v_pk_fma_f32 v[70:71], v[52:53], v[78:79], v[70:71]
	v_pk_mul_f32 v[50:51], v[50:51], v[62:63]
	v_pk_mul_f32 v[52:53], v[52:53], 4.0 op_sel_hi:[1,0]
	v_exp_f32_e32 v62, v72
	v_exp_f32_e32 v63, v73
	v_pk_fma_f32 v[68:69], v[68:69], v[68:69], v[68:69] neg_lo:[1,0,0] neg_hi:[1,0,0]
	v_exp_f32_e32 v60, v60
	v_pk_mul_f32 v[52:53], v[52:53], v[68:69]
	v_exp_f32_e32 v68, v74
	v_exp_f32_e32 v69, v75
	v_pk_add_f32 v[62:63], v[62:63], 1.0 op_sel_hi:[1,0]
	v_cvt_pk_f16_f32 v53, v52, v53
	v_rcp_f32_e32 v62, v62
	v_rcp_f32_e32 v63, v63
	v_pk_add_f32 v[68:69], v[68:69], 1.0 op_sel_hi:[1,0]
	v_cvt_pk_f16_f32 v52, v50, v51
	v_rcp_f32_e32 v68, v68
	v_rcp_f32_e32 v69, v69
	v_pk_fma_f32 v[50:51], v[62:63], 2.0, 1.0 op_sel_hi:[1,0,0] neg_lo:[1,0,0] neg_hi:[1,0,0]
	v_pk_fma_f32 v[62:63], v[62:63], v[62:63], v[62:63] neg_lo:[1,0,0] neg_hi:[1,0,0]
	s_waitcnt lgkmcnt(0)
	v_pk_fma_f32 v[50:51], v[54:55], v[50:51], v[70:71]
	v_pk_fma_f32 v[70:71], v[68:69], 2.0, 1.0 op_sel_hi:[1,0,0] neg_lo:[1,0,0] neg_hi:[1,0,0]
	v_pk_mul_f32 v[54:55], v[54:55], 4.0 op_sel_hi:[1,0]
	v_pk_fma_f32 v[50:51], v[56:57], v[70:71], v[50:51]
	v_pk_mul_f32 v[62:63], v[54:55], v[62:63]
	v_pk_mul_f32 v[54:55], v[56:57], 4.0 op_sel_hi:[1,0]
	v_pk_fma_f32 v[56:57], v[68:69], v[68:69], v[68:69] neg_lo:[1,0,0] neg_hi:[1,0,0]
	v_exp_f32_e32 v61, v61
	v_pk_mul_f32 v[54:55], v[54:55], v[56:57]
	v_pk_add_f32 v[60:61], v[60:61], 1.0 op_sel_hi:[1,0]
	v_cvt_pk_f16_f32 v55, v54, v55
	v_cvt_pk_f16_f32 v54, v62, v63
	v_exp_f32_e32 v62, v58
	v_exp_f32_e32 v63, v59
	ds_read_b128 v[56:59], v66 offset:33344
	v_rcp_f32_e32 v70, v60
	v_rcp_f32_e32 v71, v61
	v_pk_add_f32 v[62:63], v[62:63], 1.0 op_sel_hi:[1,0]
	v_permlane32_swap_b32_e32 v52, v54
	v_rcp_f32_e32 v68, v62
	v_rcp_f32_e32 v69, v63
	ds_read_b128 v[60:63], v66 offset:33376
	v_permlane32_swap_b32_e32 v53, v55
	v_pk_fma_f32 v[72:73], v[68:69], 2.0, 1.0 op_sel_hi:[1,0,0] neg_lo:[1,0,0] neg_hi:[1,0,0]
	s_waitcnt lgkmcnt(1)
	v_pk_fma_f32 v[50:51], v[56:57], v[72:73], v[50:51]
	v_pk_fma_f32 v[72:73], v[70:71], 2.0, 1.0 op_sel_hi:[1,0,0] neg_lo:[1,0,0] neg_hi:[1,0,0]
	v_pk_mul_f32 v[56:57], v[56:57], 4.0 op_sel_hi:[1,0]
	v_pk_fma_f32 v[72:73], v[58:59], v[72:73], v[50:51]
	v_pk_fma_f32 v[50:51], v[68:69], v[68:69], v[68:69] neg_lo:[1,0,0] neg_hi:[1,0,0]
	s_nop 0
	v_pk_mul_f32 v[50:51], v[56:57], v[50:51]
	v_pk_mul_f32 v[56:57], v[58:59], 4.0 op_sel_hi:[1,0]
	v_pk_fma_f32 v[58:59], v[70:71], v[70:71], v[70:71] neg_lo:[1,0,0] neg_hi:[1,0,0]
	s_nop 0
	v_pk_mul_f32 v[56:57], v[56:57], v[58:59]
	v_exp_f32_e32 v58, v76
	v_exp_f32_e32 v59, v77
	v_cvt_pk_f16_f32 v57, v56, v57
	v_cvt_pk_f16_f32 v56, v50, v51
	v_exp_f32_e32 v50, v64
	v_exp_f32_e32 v51, v65
	v_pk_add_f32 v[58:59], v[58:59], 1.0 op_sel_hi:[1,0]
	v_pk_add_f32 v[50:51], v[50:51], 1.0 op_sel_hi:[1,0]
	v_rcp_f32_e32 v64, v58
	v_rcp_f32_e32 v65, v59
	v_rcp_f32_e32 v68, v50
	v_rcp_f32_e32 v69, v51
	s_waitcnt lgkmcnt(0)
	v_pk_mul_f32 v[50:51], v[60:61], 4.0 op_sel_hi:[1,0]
	v_pk_fma_f32 v[58:59], v[64:65], v[64:65], v[64:65] neg_lo:[1,0,0] neg_hi:[1,0,0]
	v_pk_fma_f32 v[64:65], v[64:65], 2.0, 1.0 op_sel_hi:[1,0,0] neg_lo:[1,0,0] neg_hi:[1,0,0]
	v_pk_mul_f32 v[70:71], v[50:51], v[58:59]
	v_pk_mul_f32 v[50:51], v[62:63], 4.0 op_sel_hi:[1,0]
	v_pk_fma_f32 v[58:59], v[68:69], v[68:69], v[68:69] neg_lo:[1,0,0] neg_hi:[1,0,0]
	v_pk_fma_f32 v[68:69], v[68:69], 2.0, 1.0 op_sel_hi:[1,0,0] neg_lo:[1,0,0] neg_hi:[1,0,0]
	v_pk_mul_f32 v[50:51], v[50:51], v[58:59]
	v_cvt_pk_f16_f32 v58, v70, v71
	v_cvt_pk_f16_f32 v59, v50, v51
	v_lshl_add_u64 v[50:51], s[4:5], 0, v[130:131]
	s_lshl_b32 s4, s10, 3
	s_add_i32 s4, s4, s3
	s_ashr_i32 s5, s4, 31
	s_lshl_b64 s[12:13], s[4:5], 10
	v_lshl_add_u64 v[70:71], v[50:51], 0, s[12:13]
	s_or_b32 s12, s4, 1
	s_ashr_i32 s13, s12, 31
	s_lshl_b64 s[12:13], s[12:13], 10
	global_store_dwordx4 v[70:71], v[52:55], off sc1
	v_permlane32_swap_b32_e32 v56, v58
	v_permlane32_swap_b32_e32 v57, v59
	v_lshl_add_u64 v[52:53], v[50:51], 0, s[12:13]
	global_store_dwordx4 v[52:53], v[56:59], off sc1
	ds_read_b128 v[52:55], v66 offset:32896
	s_or_b32 s12, s4, 2
	v_pk_fma_f32 v[56:57], v[60:61], v[64:65], v[72:73]
	s_ashr_i32 s13, s12, 31
	v_pk_fma_f32 v[64:65], v[62:63], v[68:69], v[56:57]
	ds_read_b128 v[56:59], v66 offset:33408
	ds_read_b128 v[60:63], v66 offset:32928
	s_waitcnt lgkmcnt(2)
	v_pk_fma_f32 v[34:35], v[34:35], s[2:3], v[52:53] op_sel_hi:[1,0,1]
	v_pk_fma_f32 v[36:37], v[36:37], s[2:3], v[54:55] op_sel_hi:[1,0,1]
	v_exp_f32_e32 v34, v34
	v_exp_f32_e32 v35, v35
	v_exp_f32_e32 v36, v36
	v_exp_f32_e32 v37, v37
	s_waitcnt lgkmcnt(0)
	v_pk_fma_f32 v[38:39], v[38:39], s[2:3], v[60:61] op_sel_hi:[1,0,1]
	v_pk_fma_f32 v[40:41], v[40:41], s[2:3], v[62:63] op_sel_hi:[1,0,1]
	v_exp_f32_e32 v38, v38
	v_exp_f32_e32 v39, v39
	v_pk_add_f32 v[34:35], v[34:35], 1.0 op_sel_hi:[1,0]
	v_exp_f32_e32 v40, v40
	v_exp_f32_e32 v41, v41
	v_rcp_f32_e32 v52, v34
	v_rcp_f32_e32 v53, v35
	v_pk_add_f32 v[34:35], v[36:37], 1.0 op_sel_hi:[1,0]
	v_pk_add_f32 v[38:39], v[38:39], 1.0 op_sel_hi:[1,0]
	v_rcp_f32_e32 v54, v34
	v_rcp_f32_e32 v55, v35
	ds_read_b128 v[34:37], v66 offset:33440
	v_rcp_f32_e32 v38, v38
	v_rcp_f32_e32 v39, v39
	v_pk_add_f32 v[40:41], v[40:41], 1.0 op_sel_hi:[1,0]
	v_pk_fma_f32 v[68:69], v[52:53], 2.0, 1.0 op_sel_hi:[1,0,0] neg_lo:[1,0,0] neg_hi:[1,0,0]
	v_rcp_f32_e32 v40, v40
	v_rcp_f32_e32 v41, v41
	v_pk_fma_f32 v[64:65], v[56:57], v[68:69], v[64:65]
	v_pk_mul_f32 v[56:57], v[56:57], 4.0 op_sel_hi:[1,0]
	v_pk_fma_f32 v[52:53], v[52:53], v[52:53], v[52:53] neg_lo:[1,0,0] neg_hi:[1,0,0]
	v_pk_fma_f32 v[68:69], v[54:55], 2.0, 1.0 op_sel_hi:[1,0,0] neg_lo:[1,0,0] neg_hi:[1,0,0]
	v_pk_mul_f32 v[56:57], v[56:57], v[52:53]
	v_pk_mul_f32 v[52:53], v[58:59], 4.0 op_sel_hi:[1,0]
	v_pk_fma_f32 v[54:55], v[54:55], v[54:55], v[54:55] neg_lo:[1,0,0] neg_hi:[1,0,0]
	v_pk_fma_f32 v[64:65], v[58:59], v[68:69], v[64:65]
	v_pk_mul_f32 v[52:53], v[52:53], v[54:55]
	v_pk_fma_f32 v[54:55], v[38:39], 2.0, 1.0 op_sel_hi:[1,0,0] neg_lo:[1,0,0] neg_hi:[1,0,0]
	v_cvt_pk_f16_f32 v53, v52, v53
	v_cvt_pk_f16_f32 v52, v56, v57
	s_waitcnt lgkmcnt(0)
	v_pk_fma_f32 v[54:55], v[34:35], v[54:55], v[64:65]
	v_pk_fma_f32 v[56:57], v[40:41], 2.0, 1.0 op_sel_hi:[1,0,0] neg_lo:[1,0,0] neg_hi:[1,0,0]
	v_pk_mul_f32 v[34:35], v[34:35], 4.0 op_sel_hi:[1,0]
	v_pk_fma_f32 v[38:39], v[38:39], v[38:39], v[38:39] neg_lo:[1,0,0] neg_hi:[1,0,0]
	v_pk_fma_f32 v[60:61], v[36:37], v[56:57], v[54:55]
	v_pk_mul_f32 v[38:39], v[34:35], v[38:39]
	v_pk_mul_f32 v[54:55], v[36:37], 4.0 op_sel_hi:[1,0]
	ds_read_b128 v[34:37], v66 offset:32960
	v_pk_fma_f32 v[40:41], v[40:41], v[40:41], v[40:41] neg_lo:[1,0,0] neg_hi:[1,0,0]
	ds_read_b128 v[56:59], v66 offset:33472
	v_pk_mul_f32 v[40:41], v[54:55], v[40:41]
	v_cvt_pk_f16_f32 v54, v38, v39
	v_cvt_pk_f16_f32 v55, v40, v41
	ds_read_b128 v[38:41], v66 offset:32992
	s_waitcnt lgkmcnt(2)
	v_pk_fma_f32 v[34:35], v[42:43], s[2:3], v[34:35] op_sel_hi:[1,0,1]
	v_pk_fma_f32 v[36:37], v[44:45], s[2:3], v[36:37] op_sel_hi:[1,0,1]
	v_exp_f32_e32 v34, v34
	v_exp_f32_e32 v35, v35
	v_exp_f32_e32 v36, v36
	v_exp_f32_e32 v37, v37
	s_waitcnt lgkmcnt(0)
	v_pk_fma_f32 v[38:39], v[46:47], s[2:3], v[38:39] op_sel_hi:[1,0,1]
	v_pk_fma_f32 v[40:41], v[48:49], s[2:3], v[40:41] op_sel_hi:[1,0,1]
	v_exp_f32_e32 v38, v38
	v_exp_f32_e32 v39, v39
	v_pk_add_f32 v[34:35], v[34:35], 1.0 op_sel_hi:[1,0]
	v_exp_f32_e32 v40, v40
	v_exp_f32_e32 v41, v41
	v_rcp_f32_e32 v42, v34
	v_rcp_f32_e32 v43, v35
	v_pk_add_f32 v[34:35], v[36:37], 1.0 op_sel_hi:[1,0]
	v_pk_add_f32 v[38:39], v[38:39], 1.0 op_sel_hi:[1,0]
	v_rcp_f32_e32 v44, v34
	v_rcp_f32_e32 v45, v35
	ds_read_b128 v[34:37], v66 offset:33504
	v_rcp_f32_e32 v46, v38
	v_rcp_f32_e32 v47, v39
	v_pk_add_f32 v[38:39], v[40:41], 1.0 op_sel_hi:[1,0]
	v_pk_fma_f32 v[62:63], v[42:43], 2.0, 1.0 op_sel_hi:[1,0,0] neg_lo:[1,0,0] neg_hi:[1,0,0]
	v_rcp_f32_e32 v40, v38
	v_rcp_f32_e32 v41, v39
	v_pk_fma_f32 v[60:61], v[56:57], v[62:63], v[60:61]
	v_pk_fma_f32 v[42:43], v[42:43], v[42:43], v[42:43] neg_lo:[1,0,0] neg_hi:[1,0,0]
	v_pk_mul_f32 v[56:57], v[56:57], 4.0 op_sel_hi:[1,0]
	v_pk_fma_f32 v[62:63], v[44:45], 2.0, 1.0 op_sel_hi:[1,0,0] neg_lo:[1,0,0] neg_hi:[1,0,0]
	v_pk_mul_f32 v[42:43], v[56:57], v[42:43]
	v_pk_mul_f32 v[56:57], v[58:59], 4.0 op_sel_hi:[1,0]
	v_pk_fma_f32 v[44:45], v[44:45], v[44:45], v[44:45] neg_lo:[1,0,0] neg_hi:[1,0,0]
	v_cvt_pk_f16_f32 v38, v42, v43
	v_pk_mul_f32 v[44:45], v[56:57], v[44:45]
	v_pk_fma_f32 v[42:43], v[46:47], 2.0, 1.0 op_sel_hi:[1,0,0] neg_lo:[1,0,0] neg_hi:[1,0,0]
	s_waitcnt lgkmcnt(0)
	v_pk_mul_f32 v[48:49], v[34:35], 4.0 op_sel_hi:[1,0]
	v_pk_fma_f32 v[46:47], v[46:47], v[46:47], v[46:47] neg_lo:[1,0,0] neg_hi:[1,0,0]
	v_cvt_pk_f16_f32 v39, v44, v45
	v_pk_fma_f32 v[44:45], v[40:41], 2.0, 1.0 op_sel_hi:[1,0,0] neg_lo:[1,0,0] neg_hi:[1,0,0]
	v_pk_mul_f32 v[46:47], v[48:49], v[46:47]
	v_pk_mul_f32 v[48:49], v[36:37], 4.0 op_sel_hi:[1,0]
	v_pk_fma_f32 v[40:41], v[40:41], v[40:41], v[40:41] neg_lo:[1,0,0] neg_hi:[1,0,0]
	s_lshl_b64 s[12:13], s[12:13], 10
	v_pk_mul_f32 v[40:41], v[48:49], v[40:41]
	v_permlane32_swap_b32_e32 v52, v54
	v_cvt_pk_f16_f32 v41, v40, v41
	v_cvt_pk_f16_f32 v40, v46, v47
	v_lshl_add_u64 v[46:47], v[50:51], 0, s[12:13]
	s_or_b32 s12, s4, 3
	s_ashr_i32 s13, s12, 31
	v_permlane32_swap_b32_e32 v53, v55
	s_lshl_b64 s[12:13], s[12:13], 10
	global_store_dwordx4 v[46:47], v[52:55], off sc1
	v_permlane32_swap_b32_e32 v38, v40
	v_permlane32_swap_b32_e32 v39, v41
	v_lshl_add_u64 v[46:47], v[50:51], 0, s[12:13]
	global_store_dwordx4 v[46:47], v[38:41], off sc1
	ds_read_b128 v[38:41], v66 offset:33024
	v_pk_fma_f32 v[60:61], v[58:59], v[62:63], v[60:61]
	s_or_b32 s12, s4, 4
	v_pk_fma_f32 v[34:35], v[34:35], v[42:43], v[60:61]
	s_ashr_i32 s13, s12, 31
	v_pk_fma_f32 v[46:47], v[36:37], v[44:45], v[34:35]
	ds_read_b128 v[34:37], v66 offset:33056
	ds_read_b128 v[42:45], v66 offset:33536
	s_waitcnt lgkmcnt(2)
	v_pk_fma_f32 v[18:19], v[18:19], s[2:3], v[38:39] op_sel_hi:[1,0,1]
	v_pk_fma_f32 v[20:21], v[20:21], s[2:3], v[40:41] op_sel_hi:[1,0,1]
	v_exp_f32_e32 v18, v18
	v_exp_f32_e32 v19, v19
	v_exp_f32_e32 v20, v20
	v_exp_f32_e32 v21, v21
	s_waitcnt lgkmcnt(1)
	v_pk_fma_f32 v[22:23], v[22:23], s[2:3], v[34:35] op_sel_hi:[1,0,1]
	v_pk_fma_f32 v[24:25], v[24:25], s[2:3], v[36:37] op_sel_hi:[1,0,1]
	v_exp_f32_e32 v22, v22
	v_exp_f32_e32 v23, v23
	v_exp_f32_e32 v24, v24
	v_exp_f32_e32 v25, v25
	v_pk_add_f32 v[18:19], v[18:19], 1.0 op_sel_hi:[1,0]
	v_pk_add_f32 v[22:23], v[22:23], 1.0 op_sel_hi:[1,0]
	v_rcp_f32_e32 v38, v18
	v_rcp_f32_e32 v39, v19
	v_pk_add_f32 v[18:19], v[20:21], 1.0 op_sel_hi:[1,0]
	v_rcp_f32_e32 v22, v22
	v_rcp_f32_e32 v40, v18
	v_rcp_f32_e32 v41, v19
	ds_read_b128 v[18:21], v66 offset:33568
	v_rcp_f32_e32 v23, v23
	v_pk_add_f32 v[24:25], v[24:25], 1.0 op_sel_hi:[1,0]
	v_pk_fma_f32 v[48:49], v[38:39], 2.0, 1.0 op_sel_hi:[1,0,0] neg_lo:[1,0,0] neg_hi:[1,0,0]
	v_rcp_f32_e32 v24, v24
	v_rcp_f32_e32 v25, v25
	s_waitcnt lgkmcnt(1)
	v_pk_fma_f32 v[46:47], v[42:43], v[48:49], v[46:47]
	v_pk_fma_f32 v[48:49], v[40:41], 2.0, 1.0 op_sel_hi:[1,0,0] neg_lo:[1,0,0] neg_hi:[1,0,0]
	v_pk_mul_f32 v[42:43], v[42:43], 4.0 op_sel_hi:[1,0]
	v_pk_fma_f32 v[38:39], v[38:39], v[38:39], v[38:39] neg_lo:[1,0,0] neg_hi:[1,0,0]
	v_pk_fma_f32 v[46:47], v[44:45], v[48:49], v[46:47]
	v_pk_mul_f32 v[42:43], v[42:43], v[38:39]
	v_pk_mul_f32 v[38:39], v[44:45], 4.0 op_sel_hi:[1,0]
	v_pk_fma_f32 v[40:41], v[40:41], v[40:41], v[40:41] neg_lo:[1,0,0] neg_hi:[1,0,0]
	v_pk_fma_f32 v[34:35], v[22:23], 2.0, 1.0 op_sel_hi:[1,0,0] neg_lo:[1,0,0] neg_hi:[1,0,0]
	v_pk_mul_f32 v[38:39], v[38:39], v[40:41]
	s_waitcnt lgkmcnt(0)
	v_pk_fma_f32 v[34:35], v[18:19], v[34:35], v[46:47]
	v_pk_fma_f32 v[36:37], v[24:25], 2.0, 1.0 op_sel_hi:[1,0,0] neg_lo:[1,0,0] neg_hi:[1,0,0]
	v_pk_mul_f32 v[18:19], v[18:19], 4.0 op_sel_hi:[1,0]
	v_pk_fma_f32 v[22:23], v[22:23], v[22:23], v[22:23] neg_lo:[1,0,0] neg_hi:[1,0,0]
	v_cvt_pk_f16_f32 v39, v38, v39
	v_cvt_pk_f16_f32 v38, v42, v43
	v_pk_fma_f32 v[42:43], v[20:21], v[36:37], v[34:35]
	v_pk_mul_f32 v[22:23], v[18:19], v[22:23]
	v_pk_mul_f32 v[18:19], v[20:21], 4.0 op_sel_hi:[1,0]
	v_pk_fma_f32 v[20:21], v[24:25], v[24:25], v[24:25] neg_lo:[1,0,0] neg_hi:[1,0,0]
	v_cvt_pk_f16_f32 v40, v22, v23
	v_pk_mul_f32 v[24:25], v[18:19], v[20:21]
	ds_read_b128 v[18:21], v66 offset:33088
	v_cvt_pk_f16_f32 v41, v24, v25
	ds_read_b128 v[22:25], v66 offset:33600
	ds_read_b128 v[34:37], v66 offset:33120
	s_lshl_b64 s[12:13], s[12:13], 10
	v_permlane32_swap_b32_e32 v38, v40
	s_waitcnt lgkmcnt(2)
	v_pk_fma_f32 v[18:19], v[26:27], s[2:3], v[18:19] op_sel_hi:[1,0,1]
	v_pk_fma_f32 v[20:21], v[28:29], s[2:3], v[20:21] op_sel_hi:[1,0,1]
	v_exp_f32_e32 v18, v18
	v_exp_f32_e32 v19, v19
	v_exp_f32_e32 v20, v20
	v_exp_f32_e32 v21, v21
	v_permlane32_swap_b32_e32 v39, v41
	v_pk_add_f32 v[18:19], v[18:19], 1.0 op_sel_hi:[1,0]
	s_nop 0
	v_rcp_f32_e32 v26, v18
	v_rcp_f32_e32 v27, v19
	v_pk_add_f32 v[18:19], v[20:21], 1.0 op_sel_hi:[1,0]
	v_pk_fma_f32 v[44:45], v[26:27], 2.0, 1.0 op_sel_hi:[1,0,0] neg_lo:[1,0,0] neg_hi:[1,0,0]
	v_rcp_f32_e32 v28, v18
	v_rcp_f32_e32 v29, v19
	s_waitcnt lgkmcnt(1)
	v_pk_fma_f32 v[42:43], v[22:23], v[44:45], v[42:43]
	v_pk_mul_f32 v[22:23], v[22:23], 4.0 op_sel_hi:[1,0]
	v_pk_fma_f32 v[26:27], v[26:27], v[26:27], v[26:27] neg_lo:[1,0,0] neg_hi:[1,0,0]
	v_pk_fma_f32 v[44:45], v[28:29], 2.0, 1.0 op_sel_hi:[1,0,0] neg_lo:[1,0,0] neg_hi:[1,0,0]
	v_pk_mul_f32 v[26:27], v[22:23], v[26:27]
	v_pk_fma_f32 v[42:43], v[24:25], v[44:45], v[42:43]
	v_pk_mul_f32 v[22:23], v[24:25], 4.0 op_sel_hi:[1,0]
	v_pk_fma_f32 v[24:25], v[28:29], v[28:29], v[28:29] neg_lo:[1,0,0] neg_hi:[1,0,0]
	s_waitcnt lgkmcnt(0)
	v_pk_fma_f32 v[28:29], v[32:33], s[2:3], v[36:37] op_sel_hi:[1,0,1]
	v_pk_mul_f32 v[22:23], v[22:23], v[24:25]
	v_pk_fma_f32 v[24:25], v[30:31], s[2:3], v[34:35] op_sel_hi:[1,0,1]
	v_exp_f32_e32 v28, v28
	v_exp_f32_e32 v24, v24
	v_exp_f32_e32 v25, v25
	v_exp_f32_e32 v29, v29
	ds_read_b128 v[18:21], v66 offset:33632
	v_cvt_pk_f16_f32 v23, v22, v23
	v_pk_add_f32 v[24:25], v[24:25], 1.0 op_sel_hi:[1,0]
	v_pk_add_f32 v[28:29], v[28:29], 1.0 op_sel_hi:[1,0]
	v_rcp_f32_e32 v24, v24
	v_rcp_f32_e32 v25, v25
	v_rcp_f32_e32 v28, v28
	v_rcp_f32_e32 v29, v29
	v_cvt_pk_f16_f32 v22, v26, v27
	v_pk_fma_f32 v[26:27], v[24:25], 2.0, 1.0 op_sel_hi:[1,0,0] neg_lo:[1,0,0] neg_hi:[1,0,0]
	s_waitcnt lgkmcnt(0)
	v_pk_mul_f32 v[32:33], v[18:19], 4.0 op_sel_hi:[1,0]
	v_pk_fma_f32 v[24:25], v[24:25], v[24:25], v[24:25] neg_lo:[1,0,0] neg_hi:[1,0,0]
	v_pk_fma_f32 v[30:31], v[28:29], 2.0, 1.0 op_sel_hi:[1,0,0] neg_lo:[1,0,0] neg_hi:[1,0,0]
	v_pk_mul_f32 v[32:33], v[32:33], v[24:25]
	v_pk_mul_f32 v[24:25], v[20:21], 4.0 op_sel_hi:[1,0]
	v_pk_fma_f32 v[28:29], v[28:29], v[28:29], v[28:29] neg_lo:[1,0,0] neg_hi:[1,0,0]
	v_pk_fma_f32 v[18:19], v[18:19], v[26:27], v[42:43]
	v_pk_mul_f32 v[24:25], v[24:25], v[28:29]
	v_lshl_add_u64 v[28:29], v[50:51], 0, s[12:13]
	s_or_b32 s12, s4, 5
	s_ashr_i32 s13, s12, 31
	v_cvt_pk_f16_f32 v25, v24, v25
	v_cvt_pk_f16_f32 v24, v32, v33
	s_lshl_b64 s[12:13], s[12:13], 10
	global_store_dwordx4 v[28:29], v[38:41], off sc1
	v_permlane32_swap_b32_e32 v22, v24
	v_permlane32_swap_b32_e32 v23, v25
	v_lshl_add_u64 v[28:29], v[50:51], 0, s[12:13]
	global_store_dwordx4 v[28:29], v[22:25], off sc1
	ds_read_b128 v[22:25], v66 offset:33152
	v_pk_fma_f32 v[30:31], v[20:21], v[30:31], v[18:19]
	ds_read_b128 v[18:21], v66 offset:33184
	ds_read_b128 v[26:29], v66 offset:33664
	s_waitcnt lgkmcnt(2)
	v_pk_fma_f32 v[2:3], v[2:3], s[2:3], v[22:23] op_sel_hi:[1,0,1]
	s_nop 0
	v_exp_f32_e32 v2, v2
	v_exp_f32_e32 v3, v3
	v_pk_fma_f32 v[4:5], v[4:5], s[2:3], v[24:25] op_sel_hi:[1,0,1]
	s_waitcnt lgkmcnt(1)
	v_pk_fma_f32 v[6:7], v[6:7], s[2:3], v[18:19] op_sel_hi:[1,0,1]
	v_exp_f32_e32 v4, v4
	v_exp_f32_e32 v5, v5
	v_exp_f32_e32 v6, v6
	v_exp_f32_e32 v7, v7
	v_pk_fma_f32 v[8:9], v[8:9], s[2:3], v[20:21] op_sel_hi:[1,0,1]
	v_pk_add_f32 v[2:3], v[2:3], 1.0 op_sel_hi:[1,0]
	v_exp_f32_e32 v8, v8
	v_exp_f32_e32 v9, v9
	v_rcp_f32_e32 v22, v2
	v_rcp_f32_e32 v23, v3
	v_pk_add_f32 v[2:3], v[4:5], 1.0 op_sel_hi:[1,0]
	v_pk_add_f32 v[6:7], v[6:7], 1.0 op_sel_hi:[1,0]
	v_rcp_f32_e32 v24, v2
	v_rcp_f32_e32 v25, v3
	ds_read_b128 v[2:5], v66 offset:33696
	v_rcp_f32_e32 v6, v6
	v_rcp_f32_e32 v7, v7
	v_pk_add_f32 v[8:9], v[8:9], 1.0 op_sel_hi:[1,0]
	v_pk_fma_f32 v[32:33], v[22:23], 2.0, 1.0 op_sel_hi:[1,0,0] neg_lo:[1,0,0] neg_hi:[1,0,0]
	v_rcp_f32_e32 v8, v8
	v_rcp_f32_e32 v9, v9
	s_waitcnt lgkmcnt(1)
	v_pk_fma_f32 v[30:31], v[26:27], v[32:33], v[30:31]
	v_pk_fma_f32 v[32:33], v[24:25], 2.0, 1.0 op_sel_hi:[1,0,0] neg_lo:[1,0,0] neg_hi:[1,0,0]
	v_pk_mul_f32 v[26:27], v[26:27], 4.0 op_sel_hi:[1,0]
	v_pk_fma_f32 v[22:23], v[22:23], v[22:23], v[22:23] neg_lo:[1,0,0] neg_hi:[1,0,0]
	v_pk_fma_f32 v[30:31], v[28:29], v[32:33], v[30:31]
	v_pk_mul_f32 v[26:27], v[26:27], v[22:23]
	v_pk_mul_f32 v[22:23], v[28:29], 4.0 op_sel_hi:[1,0]
	v_pk_fma_f32 v[24:25], v[24:25], v[24:25], v[24:25] neg_lo:[1,0,0] neg_hi:[1,0,0]
	v_pk_fma_f32 v[18:19], v[6:7], 2.0, 1.0 op_sel_hi:[1,0,0] neg_lo:[1,0,0] neg_hi:[1,0,0]
	v_pk_mul_f32 v[22:23], v[22:23], v[24:25]
	s_waitcnt lgkmcnt(0)
	v_pk_fma_f32 v[18:19], v[2:3], v[18:19], v[30:31]
	v_pk_fma_f32 v[20:21], v[8:9], 2.0, 1.0 op_sel_hi:[1,0,0] neg_lo:[1,0,0] neg_hi:[1,0,0]
	v_pk_mul_f32 v[2:3], v[2:3], 4.0 op_sel_hi:[1,0]
	v_pk_fma_f32 v[6:7], v[6:7], v[6:7], v[6:7] neg_lo:[1,0,0] neg_hi:[1,0,0]
	v_cvt_pk_f16_f32 v23, v22, v23
	v_cvt_pk_f16_f32 v22, v26, v27
	v_pk_fma_f32 v[26:27], v[4:5], v[20:21], v[18:19]
	v_pk_mul_f32 v[6:7], v[2:3], v[6:7]
	v_pk_mul_f32 v[2:3], v[4:5], 4.0 op_sel_hi:[1,0]
	v_pk_fma_f32 v[4:5], v[8:9], v[8:9], v[8:9] neg_lo:[1,0,0] neg_hi:[1,0,0]
	v_cvt_pk_f16_f32 v24, v6, v7
	v_pk_mul_f32 v[8:9], v[2:3], v[4:5]
	ds_read_b128 v[2:5], v66 offset:33216
	v_cvt_pk_f16_f32 v25, v8, v9
	ds_read_b128 v[6:9], v66 offset:33728
	ds_read_b128 v[18:21], v66 offset:33248
	v_permlane32_swap_b32_e32 v22, v24
	s_waitcnt lgkmcnt(2)
	v_pk_fma_f32 v[2:3], v[10:11], s[2:3], v[2:3] op_sel_hi:[1,0,1]
	v_pk_fma_f32 v[4:5], v[12:13], s[2:3], v[4:5] op_sel_hi:[1,0,1]
	v_exp_f32_e32 v2, v2
	v_exp_f32_e32 v3, v3
	v_exp_f32_e32 v4, v4
	v_exp_f32_e32 v5, v5
	v_permlane32_swap_b32_e32 v23, v25
	v_pk_add_f32 v[2:3], v[2:3], 1.0 op_sel_hi:[1,0]
	s_nop 0
	v_rcp_f32_e32 v10, v2
	v_rcp_f32_e32 v11, v3
	v_pk_add_f32 v[2:3], v[4:5], 1.0 op_sel_hi:[1,0]
	v_pk_fma_f32 v[28:29], v[10:11], 2.0, 1.0 op_sel_hi:[1,0,0] neg_lo:[1,0,0] neg_hi:[1,0,0]
	v_rcp_f32_e32 v12, v2
	v_rcp_f32_e32 v13, v3
	s_waitcnt lgkmcnt(1)
	v_pk_fma_f32 v[26:27], v[6:7], v[28:29], v[26:27]
	v_pk_mul_f32 v[6:7], v[6:7], 4.0 op_sel_hi:[1,0]
	v_pk_fma_f32 v[10:11], v[10:11], v[10:11], v[10:11] neg_lo:[1,0,0] neg_hi:[1,0,0]
	v_pk_fma_f32 v[28:29], v[12:13], 2.0, 1.0 op_sel_hi:[1,0,0] neg_lo:[1,0,0] neg_hi:[1,0,0]
	v_pk_mul_f32 v[10:11], v[6:7], v[10:11]
	v_pk_fma_f32 v[26:27], v[8:9], v[28:29], v[26:27]
	v_pk_mul_f32 v[6:7], v[8:9], 4.0 op_sel_hi:[1,0]
	v_pk_fma_f32 v[8:9], v[12:13], v[12:13], v[12:13] neg_lo:[1,0,0] neg_hi:[1,0,0]
	s_waitcnt lgkmcnt(0)
	v_pk_fma_f32 v[12:13], v[16:17], s[2:3], v[20:21] op_sel_hi:[1,0,1]
	v_pk_mul_f32 v[6:7], v[6:7], v[8:9]
	v_pk_fma_f32 v[8:9], v[14:15], s[2:3], v[18:19] op_sel_hi:[1,0,1]
	v_exp_f32_e32 v12, v12
	v_exp_f32_e32 v8, v8
	v_exp_f32_e32 v9, v9
	v_exp_f32_e32 v13, v13
	ds_read_b128 v[2:5], v66 offset:33760
	v_cvt_pk_f16_f32 v7, v6, v7
	v_pk_add_f32 v[8:9], v[8:9], 1.0 op_sel_hi:[1,0]
	v_pk_add_f32 v[12:13], v[12:13], 1.0 op_sel_hi:[1,0]
	v_rcp_f32_e32 v8, v8
	v_rcp_f32_e32 v9, v9
	v_rcp_f32_e32 v12, v12
	v_rcp_f32_e32 v13, v13
	v_cvt_pk_f16_f32 v6, v10, v11
	v_pk_fma_f32 v[10:11], v[8:9], 2.0, 1.0 op_sel_hi:[1,0,0] neg_lo:[1,0,0] neg_hi:[1,0,0]
	s_waitcnt lgkmcnt(0)
	v_pk_mul_f32 v[16:17], v[2:3], 4.0 op_sel_hi:[1,0]
	v_pk_fma_f32 v[14:15], v[12:13], 2.0, 1.0 op_sel_hi:[1,0,0] neg_lo:[1,0,0] neg_hi:[1,0,0]
	v_pk_fma_f32 v[2:3], v[2:3], v[10:11], v[26:27]
	v_pk_fma_f32 v[8:9], v[8:9], v[8:9], v[8:9] neg_lo:[1,0,0] neg_hi:[1,0,0]
	v_pk_fma_f32 v[2:3], v[4:5], v[14:15], v[2:3]
	v_pk_mul_f32 v[16:17], v[16:17], v[8:9]
	v_add_f32_e32 v2, v2, v3
	v_mbcnt_lo_u32_b32 v3, -1, 0
	v_mbcnt_hi_u32_b32 v3, -1, v3
	v_pk_mul_f32 v[8:9], v[4:5], 4.0 op_sel_hi:[1,0]
	v_and_b32_e32 v5, 64, v3
	v_xor_b32_e32 v4, 32, v3
	v_add_u32_e32 v5, 64, v5
	v_cmp_lt_i32_e32 vcc, v4, v5
	s_or_b32 s2, s4, 6
	s_ashr_i32 s3, s2, 31
	v_cndmask_b32_e32 v3, v3, v4, vcc
	v_lshlrev_b32_e32 v3, 2, v3
	v_pk_fma_f32 v[12:13], v[12:13], v[12:13], v[12:13] neg_lo:[1,0,0] neg_hi:[1,0,0]
	s_lshl_b64 s[2:3], s[2:3], 10
	ds_bpermute_b32 v3, v3, v2
	v_pk_mul_f32 v[8:9], v[8:9], v[12:13]
	v_lshl_add_u64 v[12:13], v[50:51], 0, s[2:3]
	s_or_b32 s2, s4, 7
	s_ashr_i32 s3, s2, 31
	v_cvt_pk_f16_f32 v9, v8, v9
	v_cvt_pk_f16_f32 v8, v16, v17
	s_lshl_b64 s[2:3], s[2:3], 10
	s_nop 0
	v_permlane32_swap_b32_e32 v6, v8
	v_permlane32_swap_b32_e32 v7, v9
	v_lshl_add_u64 v[4:5], v[50:51], 0, s[2:3]
	v_cmp_gt_u32_e32 vcc, 32, v1
	global_store_dwordx4 v[12:13], v[22:25], off sc1
	global_store_dwordx4 v[4:5], v[6:9], off sc1
	s_and_saveexec_b64 s[2:3], vcc
	s_cbranch_execz .LBB2_5
	s_load_dwordx2 s[4:5], s[0:1], 0x30
	s_lshl_b32 s7, s10, 12
	s_lshl_b32 s6, s6, 7
	s_or_b32 s6, s6, s7
	s_lshl_b32 s7, s8, 5
	s_or_b32 s6, s7, s6
	s_waitcnt lgkmcnt(0)
	v_add_f32_e32 v4, v2, v3
	v_or_b32_e32 v2, s6, v1
	v_ashrrev_i32_e32 v3, 31, v2
	v_lshl_add_u64 v[2:3], v[2:3], 2, s[4:5]
	global_store_dword v[2:3], v4, off sc1

.LBB2_6:
	s_load_dwordx2 s[2:3], s[0:1], 0x0
	s_load_dwordx4 s[4:7], s[0:1], 0x10
	s_lshl_b32 s0, s10, 8
	s_lshl_b32 s1, s9, 7
	s_add_i32 s0, s1, s0
	s_ashr_i32 s1, s0, 31
	s_lshl_b64 s[0:1], s[0:1], 10
	s_waitcnt lgkmcnt(0)
	s_add_u32 s0, s2, s0
	s_addc_u32 s1, s3, s1
	v_mov_b32_e32 v131, 0
	v_lshl_add_u64 v[2:3], s[0:1], 0, v[130:131]
	global_load_dwordx4 v[4:7], v130, s[0:1]
	global_load_dwordx4 v[8:11], v130, s[0:1] offset:1024
	global_load_dwordx4 v[12:15], v130, s[0:1] offset:2048
	global_load_dwordx4 v[16:19], v130, s[0:1] offset:3072
	s_mov_b32 s0, 0x10000
	v_add_co_u32_e32 v36, vcc, s0, v2
	s_mov_b32 s0, 0x11000
	s_nop 0
	v_addc_co_u32_e32 v37, vcc, 0, v3, vcc
	v_add_co_u32_e32 v80, vcc, s0, v2
	s_lshl_b32 s0, s10, 7
	s_ashr_i32 s1, s0, 31
	v_mov_b32_e32 v1, v131
	v_lshl_add_u64 v[32:33], s[0:1], 0, v[0:1]
	v_lshlrev_b64 v[32:33], 2, v[32:33]
	v_addc_co_u32_e32 v81, vcc, 0, v3, vcc
	v_lshl_add_u64 v[34:35], s[4:5], 0, v[32:33]
	global_load_dwordx4 v[20:23], v[80:81], off offset:-4096
	global_load_dwordx4 v[24:27], v[36:37], off offset:1024
	global_load_dwordx4 v[28:31], v[36:37], off offset:2048
	global_load_dword v1, v[34:35], off offset:-1024
	v_lshl_add_u64 v[38:39], s[6:7], 0, v[32:33]
	global_load_dword v102, v[38:39], off offset:-1024
	global_load_dwordx4 v[32:35], v[36:37], off offset:3072
	s_movk_i32 s1, 0x2000
	v_add_co_u32_e32 v82, vcc, s1, v2
	s_movk_i32 s0, 0x1000
	s_nop 0
	v_addc_co_u32_e32 v83, vcc, 0, v3, vcc
	global_load_dwordx4 v[36:39], v[82:83], off offset:-4096
	v_add_co_u32_e32 v84, vcc, s0, v2
	s_mov_b32 s1, 0x13000
	s_nop 0
	v_addc_co_u32_e32 v85, vcc, 0, v3, vcc
	global_load_dwordx4 v[40:43], v[84:85], off offset:1024
	global_load_dwordx4 v[44:47], v[84:85], off offset:2048
	global_load_dwordx4 v[48:51], v[84:85], off offset:3072
	global_load_dwordx4 v[52:55], v[80:81], off
	global_load_dwordx4 v[56:59], v[80:81], off offset:1024
	global_load_dwordx4 v[60:63], v[80:81], off offset:2048
	global_load_dwordx4 v[64:67], v[80:81], off offset:3072
	global_load_dwordx4 v[68:71], v[82:83], off
	global_load_dwordx4 v[72:75], v[82:83], off offset:1024
	global_load_dwordx4 v[76:79], v[82:83], off offset:2048
	v_add_co_u32_e32 v100, vcc, s1, v2
	s_mov_b32 s0, 0x12000
	global_load_dwordx4 v[80:83], v[82:83], off offset:3072
	v_addc_co_u32_e32 v101, vcc, 0, v3, vcc
	global_load_dwordx4 v[84:87], v[100:101], off offset:-4096
	v_add_co_u32_e32 v96, vcc, s0, v2
	v_lshlrev_b32_e32 v0, 2, v0
	s_nop 0
	v_addc_co_u32_e32 v97, vcc, 0, v3, vcc
	global_load_dwordx4 v[88:91], v[96:97], off offset:1024
	global_load_dwordx4 v[92:95], v[96:97], off offset:2048
	v_lshl_or_b32 v103, s9, 13, v130
	global_load_dwordx4 v[96:99], v[96:97], off offset:3072
	s_movk_i32 s1, 0x4000
	s_movk_i32 s0, 0x3000
	s_mov_b32 s2, 0x15000
	s_waitcnt vmcnt(25)
	ds_write_b128 v103, v[4:7]
	s_waitcnt vmcnt(24)
	ds_write_b128 v103, v[8:11] offset:1024
	s_waitcnt vmcnt(23)
	ds_write_b128 v103, v[12:15] offset:2048
	s_waitcnt vmcnt(22)
	ds_write_b128 v103, v[16:19] offset:3072
	s_waitcnt vmcnt(21)
	ds_write_b128 v103, v[20:23] offset:4096
	s_waitcnt vmcnt(20)
	ds_write_b128 v103, v[24:27] offset:5120
	s_waitcnt vmcnt(19)
	ds_write_b128 v103, v[28:31] offset:6144
	s_waitcnt vmcnt(18)
	v_mul_f32_e32 v1, 0x4038aa3b, v1
	s_waitcnt vmcnt(17)
	ds_write2st64_b32 v0, v1, v102 offset0:124 offset1:126
	s_waitcnt vmcnt(16)
	ds_write_b128 v103, v[32:35] offset:7168
	v_add_co_u32_e32 v102, vcc, s1, v2
	s_waitcnt lgkmcnt(0)
	s_nop 0
	v_addc_co_u32_e32 v103, vcc, 0, v3, vcc
	v_add_co_u32_e32 v0, vcc, s0, v2
	s_barrier
	s_nop 0
	v_addc_co_u32_e32 v1, vcc, 0, v3, vcc
	global_load_dwordx4 v[4:7], v[102:103], off offset:-4096
	global_load_dwordx4 v[8:11], v[0:1], off offset:1024
	global_load_dwordx4 v[12:15], v[0:1], off offset:2048
	global_load_dwordx4 v[16:19], v[0:1], off offset:3072
	global_load_dwordx4 v[20:23], v[100:101], off
	global_load_dwordx4 v[24:27], v[100:101], off offset:1024
	global_load_dwordx4 v[28:31], v[100:101], off offset:2048
	global_load_dwordx4 v[32:35], v[100:101], off offset:3072
	s_lshl_b32 s0, s8, 13
	s_and_b32 s0, s0, 0x6000
	v_or_b32_e32 v0, s0, v130
	s_mov_b32 s1, 0x14000
	s_waitcnt vmcnt(23)
	ds_write_b128 v0, v[36:39] offset:16384
	s_waitcnt vmcnt(22)
	ds_write_b128 v0, v[40:43] offset:17408
	s_waitcnt vmcnt(21)
	ds_write_b128 v0, v[44:47] offset:18432
	s_waitcnt vmcnt(20)
	ds_write_b128 v0, v[48:51] offset:19456
	s_waitcnt vmcnt(19)
	ds_write_b128 v0, v[52:55] offset:20480
	s_waitcnt vmcnt(18)
	ds_write_b128 v0, v[56:59] offset:21504
	s_waitcnt vmcnt(17)
	ds_write_b128 v0, v[60:63] offset:22528
	s_waitcnt vmcnt(16)
	ds_write_b128 v0, v[64:67] offset:23552
	s_waitcnt lgkmcnt(0)
	s_barrier
	s_waitcnt vmcnt(15)
	ds_write_b128 v0, v[68:71]
	v_add_co_u32_e32 v68, vcc, s1, v2
	s_waitcnt vmcnt(14)
	ds_write_b128 v0, v[72:75] offset:1024
	v_addc_co_u32_e32 v69, vcc, 0, v3, vcc
	v_add_co_u32_e32 v100, vcc, s2, v2
	s_movk_i32 s0, 0x6000
	global_load_dwordx4 v[36:39], v[102:103], off
	global_load_dwordx4 v[40:43], v[102:103], off offset:1024
	global_load_dwordx4 v[44:47], v[102:103], off offset:2048
	s_waitcnt vmcnt(16)
	ds_write_b128 v0, v[76:79] offset:2048
	v_addc_co_u32_e32 v101, vcc, 0, v3, vcc
	s_waitcnt vmcnt(15)
	ds_write_b128 v0, v[80:83] offset:3072
	global_load_dwordx4 v[48:51], v[102:103], off offset:3072
	global_load_dwordx4 v[52:55], v[100:101], off offset:-4096
	s_waitcnt vmcnt(16)
	ds_write_b128 v0, v[84:87] offset:4096
	v_add_co_u32_e32 v102, vcc, s0, v2
	global_load_dwordx4 v[56:59], v[68:69], off offset:1024
	global_load_dwordx4 v[60:63], v[68:69], off offset:2048
	global_load_dwordx4 v[64:67], v[68:69], off offset:3072
	v_addc_co_u32_e32 v103, vcc, 0, v3, vcc
	s_waitcnt vmcnt(18)
	ds_write_b128 v0, v[88:91] offset:5120
	s_waitcnt vmcnt(17)
	ds_write_b128 v0, v[92:95] offset:6144
	s_waitcnt vmcnt(16)
	ds_write_b128 v0, v[96:99] offset:7168
	s_waitcnt lgkmcnt(0)
	s_barrier
	global_load_dwordx4 v[68:71], v[102:103], off offset:-4096
	s_movk_i32 s1, 0x5000
	v_add_co_u32_e32 v104, vcc, s1, v2
	s_mov_b32 s1, 0x17000
	s_nop 0
	v_addc_co_u32_e32 v105, vcc, 0, v3, vcc
	global_load_dwordx4 v[72:75], v[104:105], off offset:1024
	global_load_dwordx4 v[76:79], v[104:105], off offset:2048
	global_load_dwordx4 v[80:83], v[104:105], off offset:3072
	global_load_dwordx4 v[84:87], v[100:101], off
	global_load_dwordx4 v[88:91], v[100:101], off offset:1024
	global_load_dwordx4 v[92:95], v[100:101], off offset:2048
	global_load_dwordx4 v[96:99], v[100:101], off offset:3072
	v_add_co_u32_e32 v100, vcc, s1, v2
	s_mov_b32 s0, 0x16000
	s_nop 0
	v_addc_co_u32_e32 v101, vcc, 0, v3, vcc
	s_mov_b32 s1, 0x8000
	s_mov_b32 s2, 0xb000
	s_waitcnt vmcnt(23)
	ds_write_b128 v0, v[4:7] offset:16384
	s_waitcnt vmcnt(22)
	ds_write_b128 v0, v[8:11] offset:17408
	s_waitcnt vmcnt(21)
	ds_write_b128 v0, v[12:15] offset:18432
	s_waitcnt vmcnt(20)
	ds_write_b128 v0, v[16:19] offset:19456
	s_waitcnt vmcnt(19)
	ds_write_b128 v0, v[20:23] offset:20480
	s_waitcnt vmcnt(18)
	ds_write_b128 v0, v[24:27] offset:21504
	s_waitcnt vmcnt(17)
	ds_write_b128 v0, v[28:31] offset:22528
	s_waitcnt vmcnt(16)
	ds_write_b128 v0, v[32:35] offset:23552
	s_waitcnt lgkmcnt(0)
	s_barrier
	global_load_dwordx4 v[4:7], v[102:103], off
	global_load_dwordx4 v[8:11], v[102:103], off offset:1024
	global_load_dwordx4 v[12:15], v[102:103], off offset:2048
	global_load_dwordx4 v[16:19], v[102:103], off offset:3072
	global_load_dwordx4 v[20:23], v[100:101], off offset:-4096
	v_add_co_u32_e32 v102, vcc, s0, v2
	s_movk_i32 s0, 0x7000
	s_nop 0
	v_addc_co_u32_e32 v103, vcc, 0, v3, vcc
	global_load_dwordx4 v[24:27], v[102:103], off offset:1024
	global_load_dwordx4 v[28:31], v[102:103], off offset:2048
	global_load_dwordx4 v[32:35], v[102:103], off offset:3072
	v_add_co_u32_e32 v102, vcc, s1, v2
	s_waitcnt vmcnt(23)
	ds_write_b128 v0, v[36:39]
	s_waitcnt vmcnt(22)
	ds_write_b128 v0, v[40:43] offset:1024
	s_waitcnt vmcnt(21)
	ds_write_b128 v0, v[44:47] offset:2048
	s_waitcnt vmcnt(20)
	ds_write_b128 v0, v[48:51] offset:3072
	s_waitcnt vmcnt(19)
	ds_write_b128 v0, v[52:55] offset:4096
	s_waitcnt vmcnt(18)
	ds_write_b128 v0, v[56:59] offset:5120
	s_waitcnt vmcnt(17)
	ds_write_b128 v0, v[60:63] offset:6144
	s_waitcnt vmcnt(16)
	ds_write_b128 v0, v[64:67] offset:7168
	v_addc_co_u32_e32 v103, vcc, 0, v3, vcc
	v_add_co_u32_e32 v56, vcc, s0, v2
	s_waitcnt lgkmcnt(0)
	s_barrier
	global_load_dwordx4 v[36:39], v[102:103], off offset:-4096
	s_waitcnt vmcnt(16)
	ds_write_b128 v0, v[68:71] offset:16384
	v_addc_co_u32_e32 v57, vcc, 0, v3, vcc
	s_waitcnt vmcnt(15)
	ds_write_b128 v0, v[72:75] offset:17408
	s_waitcnt vmcnt(14)
	ds_write_b128 v0, v[76:79] offset:18432
	global_load_dwordx4 v[40:43], v[56:57], off offset:1024
	global_load_dwordx4 v[44:47], v[56:57], off offset:2048
	s_waitcnt vmcnt(15)
	ds_write_b128 v0, v[80:83] offset:19456
	global_load_dwordx4 v[48:51], v[56:57], off offset:3072
	global_load_dwordx4 v[52:55], v[100:101], off
	s_waitcnt vmcnt(16)
	ds_write_b128 v0, v[84:87] offset:20480
	s_waitcnt vmcnt(15)
	ds_write_b128 v0, v[88:91] offset:21504
	global_load_dwordx4 v[56:59], v[100:101], off offset:1024
	global_load_dwordx4 v[60:63], v[100:101], off offset:2048
	s_mov_b32 s0, 0x18000
	v_add_co_u32_e32 v84, vcc, s0, v2
	s_waitcnt vmcnt(16)
	ds_write_b128 v0, v[92:95] offset:22528
	global_load_dwordx4 v[64:67], v[100:101], off offset:3072
	s_waitcnt vmcnt(16)
	ds_write_b128 v0, v[96:99] offset:23552
	s_waitcnt lgkmcnt(0)
	s_barrier
	global_load_dwordx4 v[68:71], v[102:103], off
	global_load_dwordx4 v[72:75], v[102:103], off offset:1024
	s_mov_b32 s1, 0x19000
	v_addc_co_u32_e32 v85, vcc, 0, v3, vcc
	global_load_dwordx4 v[76:79], v[102:103], off offset:2048
	global_load_dwordx4 v[80:83], v[102:103], off offset:3072
	v_add_co_u32_e32 v100, vcc, s1, v2
	s_waitcnt vmcnt(19)
	ds_write_b128 v0, v[4:7]
	s_waitcnt vmcnt(18)
	ds_write_b128 v0, v[8:11] offset:1024
	v_addc_co_u32_e32 v101, vcc, 0, v3, vcc
	s_mov_b32 s1, 0xa000
	global_load_dwordx4 v[4:7], v[100:101], off offset:-4096
	global_load_dwordx4 v[8:11], v[84:85], off offset:1024
	s_waitcnt vmcnt(19)
	ds_write_b128 v0, v[12:15] offset:2048
	s_waitcnt vmcnt(18)
	ds_write_b128 v0, v[16:19] offset:3072
	s_waitcnt vmcnt(17)
	ds_write_b128 v0, v[20:23] offset:4096
	v_add_co_u32_e32 v102, vcc, s1, v2
	global_load_dwordx4 v[12:15], v[84:85], off offset:2048
	s_waitcnt vmcnt(17)
	ds_write_b128 v0, v[24:27] offset:5120
	s_waitcnt vmcnt(16)
	ds_write_b128 v0, v[28:31] offset:6144
	v_addc_co_u32_e32 v103, vcc, 0, v3, vcc
	global_load_dwordx4 v[16:19], v[84:85], off offset:3072
	s_waitcnt vmcnt(16)
	ds_write_b128 v0, v[32:35] offset:7168
	s_waitcnt lgkmcnt(0)
	s_barrier
	global_load_dwordx4 v[20:23], v[102:103], off offset:-4096
	s_mov_b32 s0, 0x9000
	v_add_co_u32_e32 v104, vcc, s0, v2
	s_mov_b32 s0, 0x1a000
	s_nop 0
	v_addc_co_u32_e32 v105, vcc, 0, v3, vcc
	global_load_dwordx4 v[24:27], v[104:105], off offset:1024
	global_load_dwordx4 v[28:31], v[104:105], off offset:2048
	global_load_dwordx4 v[32:35], v[104:105], off offset:3072
	global_load_dwordx4 v[84:87], v[100:101], off
	global_load_dwordx4 v[88:91], v[100:101], off offset:1024
	global_load_dwordx4 v[92:95], v[100:101], off offset:2048
	global_load_dwordx4 v[96:99], v[100:101], off offset:3072
	s_waitcnt vmcnt(23)
	ds_write_b128 v0, v[36:39] offset:16384
	s_waitcnt vmcnt(22)
	ds_write_b128 v0, v[40:43] offset:17408
	s_waitcnt vmcnt(21)
	ds_write_b128 v0, v[44:47] offset:18432
	s_waitcnt vmcnt(20)
	ds_write_b128 v0, v[48:51] offset:19456
	s_waitcnt vmcnt(19)
	ds_write_b128 v0, v[52:55] offset:20480
	s_waitcnt vmcnt(18)
	ds_write_b128 v0, v[56:59] offset:21504
	s_waitcnt vmcnt(17)
	ds_write_b128 v0, v[60:63] offset:22528
	s_waitcnt vmcnt(16)
	ds_write_b128 v0, v[64:67] offset:23552
	v_add_co_u32_e32 v56, vcc, s0, v2
	s_mov_b32 s1, 0x1b000
	s_nop 0
	v_addc_co_u32_e32 v57, vcc, 0, v3, vcc
	v_add_co_u32_e32 v64, vcc, s1, v2
	s_waitcnt lgkmcnt(0)
	s_barrier
	s_waitcnt vmcnt(15)
	ds_write_b128 v0, v[68:71]
	s_waitcnt vmcnt(14)
	ds_write_b128 v0, v[72:75] offset:1024
	v_addc_co_u32_e32 v65, vcc, 0, v3, vcc
	s_mov_b32 s0, 0xc000
	global_load_dwordx4 v[36:39], v[102:103], off offset:1024
	global_load_dwordx4 v[40:43], v[102:103], off offset:2048
	s_waitcnt vmcnt(14)
	ds_write_b128 v0, v[80:83] offset:3072
	v_add_co_u32_e32 v80, vcc, s0, v2
	ds_write_b128 v0, v[76:79] offset:2048
	s_nop 0
	v_addc_co_u32_e32 v81, vcc, 0, v3, vcc
	global_load_dwordx4 v[44:47], v[102:103], off offset:3072
	global_load_dwordx4 v[48:51], v[64:65], off offset:-4096
	v_add_co_u32_e32 v66, vcc, s2, v2
	s_mov_b32 s0, 0x1c000
	s_nop 0
	v_addc_co_u32_e32 v67, vcc, 0, v3, vcc
	v_add_co_u32_e32 v100, vcc, s0, v2
	s_mov_b32 s0, 0x1d000
	s_nop 0
	v_addc_co_u32_e32 v101, vcc, 0, v3, vcc
	s_mov_b32 s1, 0xe000
	s_waitcnt vmcnt(15)
	ds_write_b128 v0, v[4:7] offset:4096
	s_waitcnt vmcnt(14)
	ds_write_b128 v0, v[8:11] offset:5120
	global_load_dwordx4 v[4:7], v[56:57], off offset:1024
	global_load_dwordx4 v[8:11], v[56:57], off offset:2048
	s_waitcnt vmcnt(15)
	ds_write_b128 v0, v[12:15] offset:6144
	global_load_dwordx4 v[12:15], v[102:103], off
	global_load_dwordx4 v[52:55], v[56:57], off offset:3072
	v_add_co_u32_e32 v102, vcc, s0, v2
	s_waitcnt vmcnt(16)
	ds_write_b128 v0, v[16:19] offset:7168
	s_waitcnt lgkmcnt(0)
	s_barrier
	global_load_dwordx4 v[16:19], v[80:81], off offset:-4096
	global_load_dwordx4 v[56:59], v[66:67], off offset:1024
	global_load_dwordx4 v[60:63], v[66:67], off offset:2048
	s_waitcnt vmcnt(18)
	ds_write_b128 v0, v[20:23] offset:16384
	s_waitcnt vmcnt(17)
	ds_write_b128 v0, v[24:27] offset:17408
	global_load_dwordx4 v[20:23], v[66:67], off offset:3072
	s_waitcnt vmcnt(17)
	ds_write_b128 v0, v[28:31] offset:18432
	s_waitcnt vmcnt(16)
	ds_write_b128 v0, v[32:35] offset:19456
	global_load_dwordx4 v[24:27], v[64:65], off
	global_load_dwordx4 v[28:31], v[64:65], off offset:1024
	s_waitcnt vmcnt(17)
	ds_write_b128 v0, v[84:87] offset:20480
	s_waitcnt vmcnt(16)
	ds_write_b128 v0, v[88:91] offset:21504
	global_load_dwordx4 v[32:35], v[64:65], off offset:2048
	s_waitcnt vmcnt(16)
	ds_write_b128 v0, v[92:95] offset:22528
	global_load_dwordx4 v[64:67], v[64:65], off offset:3072
	s_waitcnt vmcnt(16)
	ds_write_b128 v0, v[96:99] offset:23552
	s_waitcnt lgkmcnt(0)
	s_barrier
	global_load_dwordx4 v[68:71], v[80:81], off
	global_load_dwordx4 v[72:75], v[80:81], off offset:1024
	global_load_dwordx4 v[76:79], v[80:81], off offset:2048
	v_addc_co_u32_e32 v103, vcc, 0, v3, vcc
	global_load_dwordx4 v[80:83], v[80:81], off offset:3072
	s_nop 0
	global_load_dwordx4 v[84:87], v[102:103], off offset:-4096
	global_load_dwordx4 v[88:91], v[100:101], off offset:1024
	global_load_dwordx4 v[92:95], v[100:101], off offset:2048
	global_load_dwordx4 v[96:99], v[100:101], off offset:3072
	v_add_co_u32_e32 v100, vcc, s1, v2
	s_mov_b32 s0, 0xd000
	s_nop 0
	v_addc_co_u32_e32 v101, vcc, 0, v3, vcc
	v_add_co_u32_e32 v104, vcc, s0, v2
	s_mov_b32 s0, 0x1e000
	s_nop 0
	v_addc_co_u32_e32 v105, vcc, 0, v3, vcc
	s_waitcnt vmcnt(17)
	ds_write_b128 v0, v[12:15]
	ds_write_b128 v0, v[36:39] offset:1024
	ds_write_b128 v0, v[40:43] offset:2048
	ds_write_b128 v0, v[44:47] offset:3072
	ds_write_b128 v0, v[48:51] offset:4096
	ds_write_b128 v0, v[4:7] offset:5120
	ds_write_b128 v0, v[8:11] offset:6144
	s_waitcnt vmcnt(16)
	ds_write_b128 v0, v[52:55] offset:7168
	s_waitcnt lgkmcnt(0)
	s_barrier
	s_waitcnt vmcnt(15)
	ds_write_b128 v0, v[16:19] offset:16384
	s_waitcnt vmcnt(14)
	ds_write_b128 v0, v[56:59] offset:17408
	s_waitcnt vmcnt(13)
	ds_write_b128 v0, v[60:63] offset:18432
	global_load_dwordx4 v[4:7], v[104:105], off offset:1024
	global_load_dwordx4 v[8:11], v[104:105], off offset:2048
	s_waitcnt vmcnt(14)
	ds_write_b128 v0, v[20:23] offset:19456
	global_load_dwordx4 v[12:15], v[104:105], off offset:3072
	global_load_dwordx4 v[16:19], v[102:103], off
	s_waitcnt vmcnt(15)
	ds_write_b128 v0, v[24:27] offset:20480
	s_waitcnt vmcnt(14)
	ds_write_b128 v0, v[28:31] offset:21504
	global_load_dwordx4 v[20:23], v[102:103], off offset:1024
	global_load_dwordx4 v[24:27], v[102:103], off offset:2048
	s_waitcnt vmcnt(15)
	ds_write_b128 v0, v[32:35] offset:22528
	global_load_dwordx4 v[28:31], v[100:101], off offset:-4096
	global_load_dwordx4 v[32:35], v[102:103], off offset:3072
	s_waitcnt vmcnt(16)
	ds_write_b128 v0, v[64:67] offset:23552
	s_waitcnt lgkmcnt(0)
	s_barrier
	s_waitcnt vmcnt(15)
	ds_write_b128 v0, v[68:71]
	v_add_co_u32_e32 v68, vcc, s0, v2
	s_mov_b32 s0, 0x1f000
	s_nop 0
	v_addc_co_u32_e32 v69, vcc, 0, v3, vcc
	v_add_co_u32_e32 v102, vcc, s0, v2
	global_load_dwordx4 v[36:39], v[100:101], off offset:1024
	global_load_dwordx4 v[40:43], v[100:101], off offset:2048
	s_waitcnt vmcnt(16)
	ds_write_b128 v0, v[72:75] offset:1024
	v_addc_co_u32_e32 v103, vcc, 0, v3, vcc
	s_waitcnt vmcnt(15)
	ds_write_b128 v0, v[76:79] offset:2048
	s_waitcnt vmcnt(14)
	ds_write_b128 v0, v[80:83] offset:3072
	s_mov_b32 s0, 0xf000
	global_load_dwordx4 v[44:47], v[100:101], off offset:3072
	global_load_dwordx4 v[48:51], v[102:103], off offset:-4096
	s_waitcnt vmcnt(15)
	ds_write_b128 v0, v[84:87] offset:4096
	s_waitcnt vmcnt(14)
	ds_write_b128 v0, v[88:91] offset:5120
	v_add_co_u32_e32 v2, vcc, s0, v2
	global_load_dwordx4 v[52:55], v[68:69], off offset:1024
	global_load_dwordx4 v[56:59], v[68:69], off offset:2048
	s_waitcnt vmcnt(15)
	ds_write_b128 v0, v[92:95] offset:6144
	v_addc_co_u32_e32 v3, vcc, 0, v3, vcc
	global_load_dwordx4 v[60:63], v[100:101], off
	global_load_dwordx4 v[64:67], v[68:69], off offset:3072
	s_waitcnt vmcnt(16)
	ds_write_b128 v0, v[96:99] offset:7168
	s_waitcnt lgkmcnt(0)
	s_barrier
	global_load_dwordx4 v[68:71], v[2:3], off
	global_load_dwordx4 v[72:75], v[2:3], off offset:1024
	global_load_dwordx4 v[76:79], v[2:3], off offset:2048
	global_load_dwordx4 v[80:83], v[2:3], off offset:3072
	global_load_dwordx4 v[84:87], v[102:103], off
	global_load_dwordx4 v[88:91], v[102:103], off offset:1024
	global_load_dwordx4 v[92:95], v[102:103], off offset:2048
	global_load_dwordx4 v[96:99], v[102:103], off offset:3072
	s_waitcnt vmcnt(17)
	ds_write_b128 v0, v[28:31] offset:16384
	ds_write_b128 v0, v[4:7] offset:17408
	ds_write_b128 v0, v[8:11] offset:18432
	ds_write_b128 v0, v[12:15] offset:19456
	ds_write_b128 v0, v[16:19] offset:20480
	ds_write_b128 v0, v[20:23] offset:21504
	ds_write_b128 v0, v[24:27] offset:22528
	s_waitcnt vmcnt(16)
	ds_write_b128 v0, v[32:35] offset:23552
	s_waitcnt lgkmcnt(0)
	s_barrier
	s_waitcnt vmcnt(9)
	ds_write_b128 v0, v[60:63]
	ds_write_b128 v0, v[36:39] offset:1024
	ds_write_b128 v0, v[40:43] offset:2048
	ds_write_b128 v0, v[44:47] offset:3072
	ds_write_b128 v0, v[48:51] offset:4096
	ds_write_b128 v0, v[52:55] offset:5120
	ds_write_b128 v0, v[56:59] offset:6144
	s_waitcnt vmcnt(8)
	ds_write_b128 v0, v[64:67] offset:7168
	s_waitcnt lgkmcnt(0)
	s_barrier
	s_waitcnt vmcnt(7)
	ds_write_b128 v0, v[68:71] offset:16384
	s_waitcnt vmcnt(6)
	ds_write_b128 v0, v[72:75] offset:17408
	s_waitcnt vmcnt(5)
	ds_write_b128 v0, v[76:79] offset:18432
	s_waitcnt vmcnt(4)
	ds_write_b128 v0, v[80:83] offset:19456
	s_waitcnt vmcnt(3)
	ds_write_b128 v0, v[84:87] offset:20480
	s_waitcnt vmcnt(2)
	ds_write_b128 v0, v[88:91] offset:21504
	s_waitcnt vmcnt(1)
	ds_write_b128 v0, v[92:95] offset:22528
	s_waitcnt vmcnt(0)
	ds_write_b128 v0, v[96:99] offset:23552
	s_waitcnt lgkmcnt(0)
	s_barrier
	s_endpgm
	s_nop 0
	s_nop 0
	s_nop 0
	s_nop 0
	s_nop 0
	s_nop 0
	s_nop 0
	s_nop 0
	s_nop 0
	s_nop 0
	s_nop 0
	s_nop 0
	s_nop 0
	s_nop 0
	s_nop 0
	s_nop 0
	s_nop 0
	s_nop 0
	s_nop 0
	s_nop 0
	s_nop 0
	s_nop 0
	s_nop 0
	s_nop 0
	s_nop 0
	s_nop 0
	s_nop 0
	s_endpgm

.LBB3_3:
	s_setprio 2
	s_lshl_b32 s3, s2, 2
	s_and_b32 s3, s3, 28
	s_bfe_u32 s2, s2, 0x20003
	s_load_dwordx2 s[10:11], s[0:1], 0x8
	s_load_dwordx2 s[12:13], s[0:1], 0x20
	s_or_b32 s2, s3, s2
	s_lshl_b32 s2, s2, 2
	s_or_b32 s6, s5, s2
	s_lshl_b32 s2, s6, 16
	s_waitcnt lgkmcnt(0)
	s_add_u32 s2, s10, s2
	s_addc_u32 s3, s11, 0
	v_lshl_add_u64 v[168:169], s[2:3], 0, v[134:135]
	s_movk_i32 s7, 0x1000
	v_add_co_u32_e32 v6, vcc, s7, v168
	s_movk_i32 s7, 0x2000
	s_nop 0
	v_addc_co_u32_e32 v7, vcc, 0, v169, vcc
	v_add_co_u32_e32 v8, vcc, s7, v168
	global_load_dwordx4 v[90:93], v134, s[2:3] offset:1024
	global_load_dwordx4 v[102:105], v134, s[2:3] offset:2048
	v_addc_co_u32_e32 v9, vcc, 0, v169, vcc
	global_load_dwordx4 v[106:109], v134, s[2:3] offset:3072
	global_load_dwordx4 v[94:97], v[8:9], off offset:-4096
	global_load_dwordx4 v[98:101], v[6:7], off offset:1024
	global_load_dwordx4 v[86:89], v[6:7], off offset:2048
	global_load_dwordx4 v[2:5], v134, s[2:3]
	global_load_dwordx4 v[82:85], v[6:7], off offset:3072
	global_load_dwordx4 v[78:81], v[8:9], off
	global_load_dwordx4 v[74:77], v[8:9], off offset:1024
	global_load_dwordx4 v[70:73], v[8:9], off offset:2048
	global_load_dwordx4 v[66:69], v[8:9], off offset:3072
	s_barrier
	ds_read_b128 v[6:9], v134
	ds_read_b128 v[10:13], v134 offset:4096
	ds_read_b128 v[14:17], v134 offset:8192
	ds_read_b128 v[110:113], v134 offset:12288
	s_load_dwordx2 s[2:3], s[0:1], 0x40
	s_lshl_b32 s7, s6, 6
	v_and_b32_e32 v1, 31, v0
	s_lshl_b32 s9, s4, 3
	v_lshrrev_b32_e32 v18, 2, v0
	s_add_i32 s10, s9, s7
	v_and_b32_e32 v18, 8, v18
	v_mov_b32_e32 v19, v135
	s_ashr_i32 s11, s10, 31
	v_lshl_add_u64 v[18:19], s[12:13], 0, v[18:19]
	s_lshl_b64 s[12:13], s[10:11], 10
	v_lshlrev_b32_e32 v1, 4, v1
	v_or_b32_e32 v20, s12, v1
	s_or_b32 s12, s10, 1
	v_mov_b32_e32 v21, s13
	s_ashr_i32 s13, s12, 31
	s_lshl_b64 s[12:13], s[12:13], 10
	v_or_b32_e32 v22, s12, v1
	s_or_b32 s12, s10, 2
	v_mov_b32_e32 v23, s13
	s_ashr_i32 s13, s12, 31
	v_lshl_add_u64 v[20:21], v[18:19], 0, v[20:21]
	s_lshl_b64 s[12:13], s[12:13], 10
	v_lshl_add_u64 v[22:23], v[18:19], 0, v[22:23]
	global_load_dwordx2 v[166:167], v[20:21], off
	global_load_dwordx2 v[164:165], v[20:21], off offset:512
	global_load_dwordx2 v[162:163], v[22:23], off
	global_load_dwordx2 v[160:161], v[22:23], off offset:512
	v_or_b32_e32 v20, s12, v1
	s_or_b32 s12, s10, 3
	v_mov_b32_e32 v21, s13
	s_ashr_i32 s13, s12, 31
	s_lshl_b64 s[12:13], s[12:13], 10
	v_or_b32_e32 v22, s12, v1
	s_or_b32 s12, s10, 4
	v_mov_b32_e32 v23, s13
	s_ashr_i32 s13, s12, 31
	v_lshl_add_u64 v[20:21], v[18:19], 0, v[20:21]
	s_lshl_b64 s[12:13], s[12:13], 10
	v_lshl_add_u64 v[22:23], v[18:19], 0, v[22:23]
	global_load_dwordx2 v[158:159], v[20:21], off
	global_load_dwordx2 v[156:157], v[20:21], off offset:512
	global_load_dwordx2 v[154:155], v[22:23], off
	global_load_dwordx2 v[152:153], v[22:23], off offset:512
	v_or_b32_e32 v20, s12, v1
	s_or_b32 s12, s10, 5
	v_mov_b32_e32 v21, s13
	s_ashr_i32 s13, s12, 31
	s_lshl_b64 s[12:13], s[12:13], 10
	v_or_b32_e32 v22, s12, v1
	s_or_b32 s12, s10, 6
	v_mov_b32_e32 v23, s13
	s_ashr_i32 s13, s12, 31
	s_or_b32 s10, s10, 7
	v_lshl_add_u64 v[20:21], v[18:19], 0, v[20:21]
	s_lshl_b64 s[12:13], s[12:13], 10
	s_ashr_i32 s11, s10, 31
	v_lshl_add_u64 v[22:23], v[18:19], 0, v[22:23]
	global_load_dwordx2 v[150:151], v[20:21], off
	global_load_dwordx2 v[148:149], v[20:21], off offset:512
	global_load_dwordx2 v[146:147], v[22:23], off
	global_load_dwordx2 v[144:145], v[22:23], off offset:512
	v_or_b32_e32 v20, s12, v1
	v_mov_b32_e32 v21, s13
	s_lshl_b64 s[10:11], s[10:11], 10
	v_lshl_add_u64 v[20:21], v[18:19], 0, v[20:21]
	v_or_b32_e32 v22, s10, v1
	v_mov_b32_e32 v23, s11
	v_lshl_add_u64 v[18:19], v[18:19], 0, v[22:23]
	global_load_dwordx2 v[142:143], v[20:21], off
	global_load_dwordx2 v[140:141], v[20:21], off offset:512
	global_load_dwordx2 v[138:139], v[18:19], off
	global_load_dwordx2 v[136:137], v[18:19], off offset:512
	s_lshl_b32 s7, s4, 7
	ds_read_b128 v[118:121], v134 offset:1024
	s_waitcnt vmcnt(21) lgkmcnt(0)
	v_mfma_f32_32x32x16_f16 v[50:65], v[6:9], v[2:5], 0
	s_movk_i32 s9, 0x4000
	v_add_co_u32_e32 v178, vcc, s9, v168
	ds_read_b128 v[122:125], v134 offset:5120
	s_nop 0
	v_addc_co_u32_e32 v179, vcc, 0, v169, vcc
	global_load_dwordx4 v[114:117], v[178:179], off offset:-4096
	s_movk_i32 s9, 0x3000
	v_add_co_u32_e32 v180, vcc, s9, v168
	v_mfma_f32_32x32x16_f16 v[34:49], v[10:13], v[2:5], 0
	s_nop 0
	v_addc_co_u32_e32 v181, vcc, 0, v169, vcc
	ds_read_b128 v[126:129], v134 offset:9216
	v_mfma_f32_32x32x16_f16 v[18:33], v[14:17], v[2:5], 0
	ds_read_b128 v[130:133], v134 offset:13312
	v_mfma_f32_32x32x16_f16 v[2:17], v[110:113], v[2:5], 0
	ds_read_b128 v[110:113], v134 offset:2048
	v_mfma_f32_32x32x16_f16 v[50:65], v[118:121], v[90:93], v[50:65]
	global_load_dwordx4 v[118:121], v[180:181], off offset:1024
	ds_read_b128 v[170:173], v134 offset:6144
	s_waitcnt lgkmcnt(4)
	v_mfma_f32_32x32x16_f16 v[34:49], v[122:125], v[90:93], v[34:49]
	ds_read_b128 v[174:177], v134 offset:10240
	s_waitcnt lgkmcnt(4)
	v_mfma_f32_32x32x16_f16 v[18:33], v[126:129], v[90:93], v[18:33]
	ds_read_b128 v[126:129], v134 offset:14336
	s_waitcnt lgkmcnt(4)
	v_mfma_f32_32x32x16_f16 v[2:17], v[130:133], v[90:93], v[2:17]
	ds_read_b128 v[90:93], v134 offset:3072
	s_waitcnt lgkmcnt(4)
	v_mfma_f32_32x32x16_f16 v[50:65], v[110:113], v[102:105], v[50:65]
	global_load_dwordx4 v[122:125], v[180:181], off offset:2048
	ds_read_b128 v[110:113], v134 offset:7168
	s_waitcnt lgkmcnt(4)
	v_mfma_f32_32x32x16_f16 v[34:49], v[170:173], v[102:105], v[34:49]
	ds_read_b128 v[130:133], v134 offset:11264
	s_waitcnt lgkmcnt(4)
	v_mfma_f32_32x32x16_f16 v[18:33], v[174:177], v[102:105], v[18:33]
	ds_read_b128 v[170:173], v134 offset:15360
	s_waitcnt lgkmcnt(4)
	v_mfma_f32_32x32x16_f16 v[2:17], v[126:129], v[102:105], v[2:17]
	global_load_dwordx4 v[102:105], v[180:181], off offset:3072
	s_waitcnt lgkmcnt(3)
	v_mfma_f32_32x32x16_f16 v[50:65], v[90:93], v[106:109], v[50:65]
	s_waitcnt lgkmcnt(0)
	s_barrier
	ds_read_b128 v[90:93], v134 offset:16384
	ds_read_b128 v[126:129], v134 offset:20480
	v_mfma_f32_32x32x16_f16 v[34:49], v[110:113], v[106:109], v[34:49]
	ds_read_b128 v[110:113], v134 offset:24576
	v_mfma_f32_32x32x16_f16 v[18:33], v[130:133], v[106:109], v[18:33]
	ds_read_b128 v[130:133], v134 offset:28672
	v_mfma_f32_32x32x16_f16 v[2:17], v[170:173], v[106:109], v[2:17]
	ds_read_b128 v[106:109], v134 offset:17408
	s_waitcnt lgkmcnt(4)
	v_mfma_f32_32x32x16_f16 v[50:65], v[90:93], v[94:97], v[50:65]
	global_load_dwordx4 v[90:93], v[178:179], off
	ds_read_b128 v[170:173], v134 offset:21504
	s_waitcnt lgkmcnt(4)
	v_mfma_f32_32x32x16_f16 v[34:49], v[126:129], v[94:97], v[34:49]
	ds_read_b128 v[126:129], v134 offset:25600
	s_waitcnt lgkmcnt(4)
	v_mfma_f32_32x32x16_f16 v[18:33], v[110:113], v[94:97], v[18:33]
	ds_read_b128 v[110:113], v134 offset:29696
	s_waitcnt lgkmcnt(4)
	v_mfma_f32_32x32x16_f16 v[2:17], v[130:133], v[94:97], v[2:17]
	ds_read_b128 v[130:133], v134 offset:18432
	s_waitcnt lgkmcnt(4)
	v_mfma_f32_32x32x16_f16 v[50:65], v[106:109], v[98:101], v[50:65]
	global_load_dwordx4 v[94:97], v[178:179], off offset:1024
	ds_read_b128 v[106:109], v134 offset:22528
	s_waitcnt lgkmcnt(4)
	v_mfma_f32_32x32x16_f16 v[34:49], v[170:173], v[98:101], v[34:49]
	ds_read_b128 v[170:173], v134 offset:26624
	s_waitcnt lgkmcnt(4)
	v_mfma_f32_32x32x16_f16 v[18:33], v[126:129], v[98:101], v[18:33]
	ds_read_b128 v[126:129], v134 offset:30720
	s_waitcnt lgkmcnt(4)
	v_mfma_f32_32x32x16_f16 v[2:17], v[110:113], v[98:101], v[2:17]
	ds_read_b128 v[110:113], v134 offset:19456
	s_waitcnt lgkmcnt(4)
	v_mfma_f32_32x32x16_f16 v[50:65], v[130:133], v[86:89], v[50:65]
	global_load_dwordx4 v[98:101], v[178:179], off offset:2048
	ds_read_b128 v[130:133], v134 offset:23552
	s_waitcnt lgkmcnt(4)
	v_mfma_f32_32x32x16_f16 v[34:49], v[106:109], v[86:89], v[34:49]
	ds_read_b128 v[106:109], v134 offset:27648
	s_waitcnt lgkmcnt(4)
	v_mfma_f32_32x32x16_f16 v[18:33], v[170:173], v[86:89], v[18:33]
	ds_read_b128 v[170:173], v134 offset:31744
	s_waitcnt lgkmcnt(4)
	v_mfma_f32_32x32x16_f16 v[2:17], v[126:129], v[86:89], v[2:17]
	global_load_dwordx4 v[86:89], v[178:179], off offset:3072
	s_waitcnt vmcnt(28) lgkmcnt(3)
	v_mfma_f32_32x32x16_f16 v[50:65], v[110:113], v[82:85], v[50:65]
	s_waitcnt lgkmcnt(0)
	s_barrier
	ds_read_b128 v[110:113], v134
	ds_read_b128 v[126:129], v134 offset:4096
	v_mfma_f32_32x32x16_f16 v[34:49], v[130:133], v[82:85], v[34:49]
	ds_read_b128 v[130:133], v134 offset:8192
	v_mfma_f32_32x32x16_f16 v[18:33], v[106:109], v[82:85], v[18:33]
	ds_read_b128 v[106:109], v134 offset:12288
	v_mfma_f32_32x32x16_f16 v[2:17], v[170:173], v[82:85], v[2:17]
	ds_read_b128 v[82:85], v134 offset:1024
	s_waitcnt vmcnt(27) lgkmcnt(4)
	v_mfma_f32_32x32x16_f16 v[50:65], v[110:113], v[78:81], v[50:65]
	s_movk_i32 s9, 0x6000
	v_add_co_u32_e32 v178, vcc, s9, v168
	ds_read_b128 v[170:173], v134 offset:5120
	s_nop 0
	v_addc_co_u32_e32 v179, vcc, 0, v169, vcc
	global_load_dwordx4 v[110:113], v[178:179], off offset:-4096
	s_movk_i32 s9, 0x5000
	v_add_co_u32_e32 v180, vcc, s9, v168
	s_waitcnt lgkmcnt(4)
	v_mfma_f32_32x32x16_f16 v[34:49], v[126:129], v[78:81], v[34:49]
	v_addc_co_u32_e32 v181, vcc, 0, v169, vcc
	ds_read_b128 v[174:177], v134 offset:9216
	s_waitcnt lgkmcnt(4)
	v_mfma_f32_32x32x16_f16 v[18:33], v[130:133], v[78:81], v[18:33]
	ds_read_b128 v[130:133], v134 offset:13312
	s_waitcnt lgkmcnt(4)
	v_mfma_f32_32x32x16_f16 v[2:17], v[106:109], v[78:81], v[2:17]
	ds_read_b128 v[78:81], v134 offset:2048
	s_waitcnt vmcnt(27) lgkmcnt(4)
	v_mfma_f32_32x32x16_f16 v[50:65], v[82:85], v[74:77], v[50:65]
	global_load_dwordx4 v[126:129], v[180:181], off offset:1024
	ds_read_b128 v[82:85], v134 offset:6144
	s_waitcnt lgkmcnt(4)
	v_mfma_f32_32x32x16_f16 v[34:49], v[170:173], v[74:77], v[34:49]
	ds_read_b128 v[106:109], v134 offset:10240
	s_waitcnt lgkmcnt(4)
	v_mfma_f32_32x32x16_f16 v[18:33], v[174:177], v[74:77], v[18:33]
	ds_read_b128 v[170:173], v134 offset:14336
	s_waitcnt lgkmcnt(4)
	v_mfma_f32_32x32x16_f16 v[2:17], v[130:133], v[74:77], v[2:17]
	ds_read_b128 v[74:77], v134 offset:3072
	s_waitcnt vmcnt(27) lgkmcnt(4)
	v_mfma_f32_32x32x16_f16 v[50:65], v[78:81], v[70:73], v[50:65]
	global_load_dwordx4 v[130:133], v[180:181], off offset:2048
	ds_read_b128 v[78:81], v134 offset:7168
	s_waitcnt lgkmcnt(4)
	v_mfma_f32_32x32x16_f16 v[34:49], v[82:85], v[70:73], v[34:49]
	ds_read_b128 v[82:85], v134 offset:11264
	s_waitcnt lgkmcnt(4)
	v_mfma_f32_32x32x16_f16 v[18:33], v[106:109], v[70:73], v[18:33]
	ds_read_b128 v[174:177], v134 offset:15360
	s_waitcnt lgkmcnt(4)
	v_mfma_f32_32x32x16_f16 v[2:17], v[170:173], v[70:73], v[2:17]
	global_load_dwordx4 v[106:109], v[180:181], off offset:3072
	s_waitcnt vmcnt(28) lgkmcnt(3)
	v_mfma_f32_32x32x16_f16 v[50:65], v[74:77], v[66:69], v[50:65]
	s_waitcnt lgkmcnt(0)
	s_barrier
	ds_read_b128 v[70:73], v134 offset:16384
	ds_read_b128 v[170:173], v134 offset:20480
	v_mfma_f32_32x32x16_f16 v[34:49], v[78:81], v[66:69], v[34:49]
	ds_read_b128 v[78:81], v134 offset:24576
	v_mfma_f32_32x32x16_f16 v[18:33], v[82:85], v[66:69], v[18:33]
	ds_read_b128 v[82:85], v134 offset:28672
	v_mfma_f32_32x32x16_f16 v[2:17], v[174:177], v[66:69], v[2:17]
	ds_read_b128 v[66:69], v134 offset:17408
	s_waitcnt vmcnt(11) lgkmcnt(4)
	v_mfma_f32_32x32x16_f16 v[50:65], v[70:73], v[114:117], v[50:65]
	global_load_dwordx4 v[74:77], v[178:179], off
	ds_read_b128 v[70:73], v134 offset:21504
	s_waitcnt lgkmcnt(4)
	v_mfma_f32_32x32x16_f16 v[34:49], v[170:173], v[114:117], v[34:49]
	ds_read_b128 v[170:173], v134 offset:25600
	s_waitcnt lgkmcnt(4)
	v_mfma_f32_32x32x16_f16 v[18:33], v[78:81], v[114:117], v[18:33]
	ds_read_b128 v[174:177], v134 offset:29696
	s_waitcnt lgkmcnt(4)
	v_mfma_f32_32x32x16_f16 v[2:17], v[82:85], v[114:117], v[2:17]
	ds_read_b128 v[82:85], v134 offset:18432
	s_waitcnt vmcnt(11) lgkmcnt(4)
	v_mfma_f32_32x32x16_f16 v[50:65], v[66:69], v[118:121], v[50:65]
	global_load_dwordx4 v[78:81], v[178:179], off offset:1024
	ds_read_b128 v[66:69], v134 offset:22528
	s_waitcnt lgkmcnt(4)
	v_mfma_f32_32x32x16_f16 v[34:49], v[70:73], v[118:121], v[34:49]
	ds_read_b128 v[70:73], v134 offset:26624
	s_waitcnt lgkmcnt(4)
	v_mfma_f32_32x32x16_f16 v[18:33], v[170:173], v[118:121], v[18:33]
	ds_read_b128 v[114:117], v134 offset:30720
	s_waitcnt lgkmcnt(4)
	v_mfma_f32_32x32x16_f16 v[2:17], v[174:177], v[118:121], v[2:17]
	ds_read_b128 v[118:121], v134 offset:19456
	s_waitcnt vmcnt(11) lgkmcnt(4)
	v_mfma_f32_32x32x16_f16 v[50:65], v[82:85], v[122:125], v[50:65]
	global_load_dwordx4 v[82:85], v[178:179], off offset:2048
	ds_read_b128 v[170:173], v134 offset:23552
	s_waitcnt lgkmcnt(4)
	v_mfma_f32_32x32x16_f16 v[34:49], v[66:69], v[122:125], v[34:49]
	ds_read_b128 v[174:177], v134 offset:27648
	s_waitcnt lgkmcnt(4)
	v_mfma_f32_32x32x16_f16 v[18:33], v[70:73], v[122:125], v[18:33]
	ds_read_b128 v[70:73], v134 offset:31744
	s_waitcnt lgkmcnt(4)
	v_mfma_f32_32x32x16_f16 v[2:17], v[114:117], v[122:125], v[2:17]
	global_load_dwordx4 v[66:69], v[178:179], off offset:3072
	s_waitcnt vmcnt(12) lgkmcnt(3)
	v_mfma_f32_32x32x16_f16 v[50:65], v[118:121], v[102:105], v[50:65]
	s_waitcnt lgkmcnt(0)
	s_barrier
	ds_read_b128 v[114:117], v134
	ds_read_b128 v[118:121], v134 offset:4096
	v_mfma_f32_32x32x16_f16 v[34:49], v[170:173], v[102:105], v[34:49]
	ds_read_b128 v[122:125], v134 offset:8192
	v_mfma_f32_32x32x16_f16 v[18:33], v[174:177], v[102:105], v[18:33]
	ds_read_b128 v[170:173], v134 offset:12288
	v_mfma_f32_32x32x16_f16 v[2:17], v[70:73], v[102:105], v[2:17]
	ds_read_b128 v[70:73], v134 offset:1024
	s_waitcnt vmcnt(11) lgkmcnt(4)
	v_mfma_f32_32x32x16_f16 v[50:65], v[114:117], v[90:93], v[50:65]
	s_mov_b32 s9, 0x8000
	v_add_co_u32_e32 v178, vcc, s9, v168
	ds_read_b128 v[102:105], v134 offset:5120
	s_nop 0
	v_addc_co_u32_e32 v179, vcc, 0, v169, vcc
	global_load_dwordx4 v[114:117], v[178:179], off offset:-4096
	s_movk_i32 s9, 0x7000
	v_add_co_u32_e32 v180, vcc, s9, v168
	s_waitcnt lgkmcnt(4)
	v_mfma_f32_32x32x16_f16 v[34:49], v[118:121], v[90:93], v[34:49]
	v_addc_co_u32_e32 v181, vcc, 0, v169, vcc
	ds_read_b128 v[174:177], v134 offset:9216
	s_waitcnt lgkmcnt(4)
	v_mfma_f32_32x32x16_f16 v[18:33], v[122:125], v[90:93], v[18:33]
	ds_read_b128 v[122:125], v134 offset:13312
	s_waitcnt lgkmcnt(4)
	v_mfma_f32_32x32x16_f16 v[2:17], v[170:173], v[90:93], v[2:17]
	ds_read_b128 v[90:93], v134 offset:2048
	s_waitcnt vmcnt(11) lgkmcnt(4)
	v_mfma_f32_32x32x16_f16 v[50:65], v[70:73], v[94:97], v[50:65]
	global_load_dwordx4 v[118:121], v[180:181], off offset:1024
	ds_read_b128 v[70:73], v134 offset:6144
	s_waitcnt lgkmcnt(4)
	v_mfma_f32_32x32x16_f16 v[34:49], v[102:105], v[94:97], v[34:49]
	ds_read_b128 v[102:105], v134 offset:10240
	s_waitcnt lgkmcnt(4)
	v_mfma_f32_32x32x16_f16 v[18:33], v[174:177], v[94:97], v[18:33]
	ds_read_b128 v[170:173], v134 offset:14336
	s_waitcnt lgkmcnt(4)
	v_mfma_f32_32x32x16_f16 v[2:17], v[122:125], v[94:97], v[2:17]
	ds_read_b128 v[94:97], v134 offset:3072
	s_waitcnt vmcnt(11) lgkmcnt(4)
	v_mfma_f32_32x32x16_f16 v[50:65], v[90:93], v[98:101], v[50:65]
	global_load_dwordx4 v[122:125], v[180:181], off offset:2048
	ds_read_b128 v[90:93], v134 offset:7168
	s_waitcnt lgkmcnt(4)
	v_mfma_f32_32x32x16_f16 v[34:49], v[70:73], v[98:101], v[34:49]
	ds_read_b128 v[70:73], v134 offset:11264
	s_waitcnt lgkmcnt(4)
	v_mfma_f32_32x32x16_f16 v[18:33], v[102:105], v[98:101], v[18:33]
	ds_read_b128 v[174:177], v134 offset:15360
	s_waitcnt lgkmcnt(4)
	v_mfma_f32_32x32x16_f16 v[2:17], v[170:173], v[98:101], v[2:17]
	global_load_dwordx4 v[102:105], v[180:181], off offset:3072
	s_waitcnt vmcnt(12) lgkmcnt(3)
	v_mfma_f32_32x32x16_f16 v[50:65], v[94:97], v[86:89], v[50:65]
	s_waitcnt lgkmcnt(0)
	s_barrier
	ds_read_b128 v[94:97], v134 offset:16384
	ds_read_b128 v[98:101], v134 offset:20480
	v_mfma_f32_32x32x16_f16 v[34:49], v[90:93], v[86:89], v[34:49]
	ds_read_b128 v[90:93], v134 offset:24576
	v_mfma_f32_32x32x16_f16 v[18:33], v[70:73], v[86:89], v[18:33]
	ds_read_b128 v[70:73], v134 offset:28672
	v_mfma_f32_32x32x16_f16 v[2:17], v[174:177], v[86:89], v[2:17]
	ds_read_b128 v[170:173], v134 offset:17408
	s_waitcnt vmcnt(11) lgkmcnt(4)
	v_mfma_f32_32x32x16_f16 v[50:65], v[94:97], v[110:113], v[50:65]
	global_load_dwordx4 v[86:89], v[178:179], off
	ds_read_b128 v[94:97], v134 offset:21504
	s_waitcnt lgkmcnt(4)
	v_mfma_f32_32x32x16_f16 v[34:49], v[98:101], v[110:113], v[34:49]
	ds_read_b128 v[98:101], v134 offset:25600
	s_waitcnt lgkmcnt(4)
	v_mfma_f32_32x32x16_f16 v[18:33], v[90:93], v[110:113], v[18:33]
	ds_read_b128 v[174:177], v134 offset:29696
	s_waitcnt lgkmcnt(4)
	v_mfma_f32_32x32x16_f16 v[2:17], v[70:73], v[110:113], v[2:17]
	ds_read_b128 v[70:73], v134 offset:18432
	s_waitcnt vmcnt(11) lgkmcnt(4)
	v_mfma_f32_32x32x16_f16 v[50:65], v[170:173], v[126:129], v[50:65]
	global_load_dwordx4 v[90:93], v[178:179], off offset:1024
	ds_read_b128 v[110:113], v134 offset:22528
	s_waitcnt lgkmcnt(4)
	v_mfma_f32_32x32x16_f16 v[34:49], v[94:97], v[126:129], v[34:49]
	ds_read_b128 v[170:173], v134 offset:26624
	s_waitcnt lgkmcnt(4)
	v_mfma_f32_32x32x16_f16 v[18:33], v[98:101], v[126:129], v[18:33]
	ds_read_b128 v[98:101], v134 offset:30720
	s_waitcnt lgkmcnt(4)
	v_mfma_f32_32x32x16_f16 v[2:17], v[174:177], v[126:129], v[2:17]
	ds_read_b128 v[126:129], v134 offset:19456
	s_waitcnt vmcnt(11) lgkmcnt(4)
	v_mfma_f32_32x32x16_f16 v[50:65], v[70:73], v[130:133], v[50:65]
	global_load_dwordx4 v[94:97], v[178:179], off offset:2048
	ds_read_b128 v[174:177], v134 offset:23552
	s_waitcnt lgkmcnt(4)
	v_mfma_f32_32x32x16_f16 v[34:49], v[110:113], v[130:133], v[34:49]
	ds_read_b128 v[110:113], v134 offset:27648
	s_waitcnt lgkmcnt(4)
	v_mfma_f32_32x32x16_f16 v[18:33], v[170:173], v[130:133], v[18:33]
	ds_read_b128 v[170:173], v134 offset:31744
	s_waitcnt lgkmcnt(4)
	v_mfma_f32_32x32x16_f16 v[2:17], v[98:101], v[130:133], v[2:17]
	global_load_dwordx4 v[70:73], v[178:179], off offset:3072
	s_waitcnt vmcnt(12) lgkmcnt(3)
	v_mfma_f32_32x32x16_f16 v[50:65], v[126:129], v[106:109], v[50:65]
	s_waitcnt lgkmcnt(0)
	s_barrier
	ds_read_b128 v[98:101], v134
	ds_read_b128 v[126:129], v134 offset:4096
	v_mfma_f32_32x32x16_f16 v[34:49], v[174:177], v[106:109], v[34:49]
	ds_read_b128 v[130:133], v134 offset:8192
	v_mfma_f32_32x32x16_f16 v[18:33], v[110:113], v[106:109], v[18:33]
	ds_read_b128 v[174:177], v134 offset:12288
	v_mfma_f32_32x32x16_f16 v[2:17], v[170:173], v[106:109], v[2:17]
	ds_read_b128 v[106:109], v134 offset:1024
	s_waitcnt vmcnt(11) lgkmcnt(4)
	v_mfma_f32_32x32x16_f16 v[50:65], v[98:101], v[74:77], v[50:65]
	s_mov_b32 s9, 0xa000
	v_add_co_u32_e32 v178, vcc, s9, v168
	ds_read_b128 v[98:101], v134 offset:5120
	s_nop 0
	v_addc_co_u32_e32 v179, vcc, 0, v169, vcc
	global_load_dwordx4 v[110:113], v[178:179], off offset:-4096
	s_mov_b32 s9, 0x9000
	v_add_co_u32_e32 v180, vcc, s9, v168
	s_waitcnt lgkmcnt(4)
	v_mfma_f32_32x32x16_f16 v[34:49], v[126:129], v[74:77], v[34:49]
	v_addc_co_u32_e32 v181, vcc, 0, v169, vcc
	ds_read_b128 v[170:173], v134 offset:9216
	s_waitcnt lgkmcnt(4)
	v_mfma_f32_32x32x16_f16 v[18:33], v[130:133], v[74:77], v[18:33]
	ds_read_b128 v[130:133], v134 offset:13312
	s_waitcnt lgkmcnt(4)
	v_mfma_f32_32x32x16_f16 v[2:17], v[174:177], v[74:77], v[2:17]
	ds_read_b128 v[74:77], v134 offset:2048
	s_waitcnt vmcnt(11) lgkmcnt(4)
	v_mfma_f32_32x32x16_f16 v[50:65], v[106:109], v[78:81], v[50:65]
	global_load_dwordx4 v[126:129], v[180:181], off offset:1024
	ds_read_b128 v[106:109], v134 offset:6144
	s_waitcnt lgkmcnt(4)
	v_mfma_f32_32x32x16_f16 v[34:49], v[98:101], v[78:81], v[34:49]
	ds_read_b128 v[98:101], v134 offset:10240
	s_waitcnt lgkmcnt(4)
	v_mfma_f32_32x32x16_f16 v[18:33], v[170:173], v[78:81], v[18:33]
	ds_read_b128 v[170:173], v134 offset:14336
	s_waitcnt lgkmcnt(4)
	v_mfma_f32_32x32x16_f16 v[2:17], v[130:133], v[78:81], v[2:17]
	ds_read_b128 v[78:81], v134 offset:3072
	s_waitcnt vmcnt(11) lgkmcnt(4)
	v_mfma_f32_32x32x16_f16 v[50:65], v[74:77], v[82:85], v[50:65]
	global_load_dwordx4 v[130:133], v[180:181], off offset:2048
	ds_read_b128 v[74:77], v134 offset:7168
	s_waitcnt lgkmcnt(4)
	v_mfma_f32_32x32x16_f16 v[34:49], v[106:109], v[82:85], v[34:49]
	ds_read_b128 v[174:177], v134 offset:11264
	s_waitcnt lgkmcnt(4)
	v_mfma_f32_32x32x16_f16 v[18:33], v[98:101], v[82:85], v[18:33]
	ds_read_b128 v[98:101], v134 offset:15360
	s_waitcnt lgkmcnt(4)
	v_mfma_f32_32x32x16_f16 v[2:17], v[170:173], v[82:85], v[2:17]
	global_load_dwordx4 v[106:109], v[180:181], off offset:3072
	s_waitcnt vmcnt(12) lgkmcnt(3)
	v_mfma_f32_32x32x16_f16 v[50:65], v[78:81], v[66:69], v[50:65]
	s_waitcnt lgkmcnt(0)
	s_barrier
	ds_read_b128 v[78:81], v134 offset:16384
	ds_read_b128 v[82:85], v134 offset:20480
	v_mfma_f32_32x32x16_f16 v[34:49], v[74:77], v[66:69], v[34:49]
	ds_read_b128 v[74:77], v134 offset:24576
	v_mfma_f32_32x32x16_f16 v[18:33], v[174:177], v[66:69], v[18:33]
	ds_read_b128 v[170:173], v134 offset:28672
	v_mfma_f32_32x32x16_f16 v[2:17], v[98:101], v[66:69], v[2:17]
	ds_read_b128 v[66:69], v134 offset:17408
	s_waitcnt vmcnt(11) lgkmcnt(4)
	v_mfma_f32_32x32x16_f16 v[50:65], v[78:81], v[114:117], v[50:65]
	global_load_dwordx4 v[78:81], v[178:179], off
	ds_read_b128 v[98:101], v134 offset:21504
	s_waitcnt lgkmcnt(4)
	v_mfma_f32_32x32x16_f16 v[34:49], v[82:85], v[114:117], v[34:49]
	ds_read_b128 v[174:177], v134 offset:25600
	s_waitcnt lgkmcnt(4)
	v_mfma_f32_32x32x16_f16 v[18:33], v[74:77], v[114:117], v[18:33]
	ds_read_b128 v[74:77], v134 offset:29696
	s_waitcnt lgkmcnt(4)
	v_mfma_f32_32x32x16_f16 v[2:17], v[170:173], v[114:117], v[2:17]
	ds_read_b128 v[114:117], v134 offset:18432
	s_waitcnt vmcnt(11) lgkmcnt(4)
	v_mfma_f32_32x32x16_f16 v[50:65], v[66:69], v[118:121], v[50:65]
	global_load_dwordx4 v[82:85], v[178:179], off offset:1024
	ds_read_b128 v[66:69], v134 offset:22528
	s_waitcnt lgkmcnt(4)
	v_mfma_f32_32x32x16_f16 v[34:49], v[98:101], v[118:121], v[34:49]
	ds_read_b128 v[170:173], v134 offset:26624
	s_waitcnt lgkmcnt(4)
	v_mfma_f32_32x32x16_f16 v[18:33], v[174:177], v[118:121], v[18:33]
	ds_read_b128 v[174:177], v134 offset:30720
	s_waitcnt lgkmcnt(4)
	v_mfma_f32_32x32x16_f16 v[2:17], v[74:77], v[118:121], v[2:17]
	ds_read_b128 v[118:121], v134 offset:19456
	s_waitcnt vmcnt(11) lgkmcnt(4)
	v_mfma_f32_32x32x16_f16 v[50:65], v[114:117], v[122:125], v[50:65]
	global_load_dwordx4 v[98:101], v[178:179], off offset:2048
	ds_read_b128 v[114:117], v134 offset:23552
	s_waitcnt lgkmcnt(4)
	v_mfma_f32_32x32x16_f16 v[34:49], v[66:69], v[122:125], v[34:49]
	ds_read_b128 v[66:69], v134 offset:27648
	s_waitcnt lgkmcnt(4)
	v_mfma_f32_32x32x16_f16 v[18:33], v[170:173], v[122:125], v[18:33]
	ds_read_b128 v[170:173], v134 offset:31744
	s_waitcnt lgkmcnt(4)
	v_mfma_f32_32x32x16_f16 v[2:17], v[174:177], v[122:125], v[2:17]
	global_load_dwordx4 v[74:77], v[178:179], off offset:3072
	s_waitcnt vmcnt(12) lgkmcnt(3)
	v_mfma_f32_32x32x16_f16 v[50:65], v[118:121], v[102:105], v[50:65]
	s_waitcnt lgkmcnt(0)
	s_barrier
	ds_read_b128 v[118:121], v134
	ds_read_b128 v[122:125], v134 offset:4096
	v_mfma_f32_32x32x16_f16 v[34:49], v[114:117], v[102:105], v[34:49]
	ds_read_b128 v[174:177], v134 offset:8192
	v_mfma_f32_32x32x16_f16 v[18:33], v[66:69], v[102:105], v[18:33]
	ds_read_b128 v[66:69], v134 offset:12288
	v_mfma_f32_32x32x16_f16 v[2:17], v[170:173], v[102:105], v[2:17]
	ds_read_b128 v[102:105], v134 offset:1024
	s_waitcnt vmcnt(11) lgkmcnt(4)
	v_mfma_f32_32x32x16_f16 v[50:65], v[118:121], v[86:89], v[50:65]
	s_mov_b32 s9, 0xc000
	v_add_co_u32_e32 v178, vcc, s9, v168
	s_waitcnt lgkmcnt(3)
	v_mfma_f32_32x32x16_f16 v[34:49], v[122:125], v[86:89], v[34:49]
	v_addc_co_u32_e32 v179, vcc, 0, v169, vcc
	global_load_dwordx4 v[114:117], v[178:179], off offset:-4096
	ds_read_b128 v[122:125], v134 offset:5120
	s_mov_b32 s9, 0xb000
	v_add_co_u32_e32 v180, vcc, s9, v168
	s_nop 1
	v_addc_co_u32_e32 v181, vcc, 0, v169, vcc
	ds_read_b128 v[170:173], v134 offset:9216
	s_waitcnt lgkmcnt(4)
	v_mfma_f32_32x32x16_f16 v[18:33], v[174:177], v[86:89], v[18:33]
	ds_read_b128 v[174:177], v134 offset:13312
	s_waitcnt lgkmcnt(4)
	v_mfma_f32_32x32x16_f16 v[2:17], v[66:69], v[86:89], v[2:17]
	ds_read_b128 v[66:69], v134 offset:2048
	s_waitcnt vmcnt(11) lgkmcnt(4)
	v_mfma_f32_32x32x16_f16 v[50:65], v[102:105], v[90:93], v[50:65]
	global_load_dwordx4 v[118:121], v[180:181], off offset:1024
	ds_read_b128 v[86:89], v134 offset:6144
	s_waitcnt lgkmcnt(4)
	v_mfma_f32_32x32x16_f16 v[34:49], v[122:125], v[90:93], v[34:49]
	ds_read_b128 v[102:105], v134 offset:10240
	s_waitcnt lgkmcnt(4)
	v_mfma_f32_32x32x16_f16 v[18:33], v[170:173], v[90:93], v[18:33]
	ds_read_b128 v[170:173], v134 offset:14336
	s_waitcnt lgkmcnt(4)
	v_mfma_f32_32x32x16_f16 v[2:17], v[174:177], v[90:93], v[2:17]
	ds_read_b128 v[90:93], v134 offset:3072
	s_waitcnt vmcnt(11) lgkmcnt(4)
	v_mfma_f32_32x32x16_f16 v[50:65], v[66:69], v[94:97], v[50:65]
	global_load_dwordx4 v[122:125], v[180:181], off offset:2048
	ds_read_b128 v[66:69], v134 offset:7168
	s_waitcnt lgkmcnt(4)
	v_mfma_f32_32x32x16_f16 v[34:49], v[86:89], v[94:97], v[34:49]
	ds_read_b128 v[86:89], v134 offset:11264
	s_waitcnt lgkmcnt(4)
	v_mfma_f32_32x32x16_f16 v[18:33], v[102:105], v[94:97], v[18:33]
	ds_read_b128 v[102:105], v134 offset:15360
	s_waitcnt lgkmcnt(4)
	v_mfma_f32_32x32x16_f16 v[2:17], v[170:173], v[94:97], v[2:17]
	global_load_dwordx4 v[94:97], v[180:181], off offset:3072
	s_waitcnt vmcnt(12) lgkmcnt(3)
	v_mfma_f32_32x32x16_f16 v[50:65], v[90:93], v[70:73], v[50:65]
	s_waitcnt lgkmcnt(0)
	s_barrier
	ds_read_b128 v[90:93], v134 offset:16384
	ds_read_b128 v[170:173], v134 offset:20480
	v_mfma_f32_32x32x16_f16 v[34:49], v[66:69], v[70:73], v[34:49]
	ds_read_b128 v[66:69], v134 offset:24576
	v_mfma_f32_32x32x16_f16 v[18:33], v[86:89], v[70:73], v[18:33]
	ds_read_b128 v[86:89], v134 offset:28672
	v_mfma_f32_32x32x16_f16 v[2:17], v[102:105], v[70:73], v[2:17]
	ds_read_b128 v[70:73], v134 offset:17408
	s_waitcnt vmcnt(11) lgkmcnt(4)
	v_mfma_f32_32x32x16_f16 v[50:65], v[90:93], v[110:113], v[50:65]
	global_load_dwordx4 v[102:105], v[178:179], off
	ds_read_b128 v[90:93], v134 offset:21504
	s_waitcnt lgkmcnt(4)
	v_mfma_f32_32x32x16_f16 v[34:49], v[170:173], v[110:113], v[34:49]
	ds_read_b128 v[170:173], v134 offset:25600
	s_waitcnt lgkmcnt(4)
	v_mfma_f32_32x32x16_f16 v[18:33], v[66:69], v[110:113], v[18:33]
	ds_read_b128 v[66:69], v134 offset:29696
	s_waitcnt lgkmcnt(4)
	v_mfma_f32_32x32x16_f16 v[2:17], v[86:89], v[110:113], v[2:17]
	ds_read_b128 v[110:113], v134 offset:18432
	s_waitcnt vmcnt(11) lgkmcnt(4)
	v_mfma_f32_32x32x16_f16 v[50:65], v[70:73], v[126:129], v[50:65]
	global_load_dwordx4 v[86:89], v[178:179], off offset:1024
	ds_read_b128 v[174:177], v134 offset:22528
	s_waitcnt lgkmcnt(4)
	v_mfma_f32_32x32x16_f16 v[34:49], v[90:93], v[126:129], v[34:49]
	ds_read_b128 v[90:93], v134 offset:26624
	s_waitcnt lgkmcnt(4)
	v_mfma_f32_32x32x16_f16 v[18:33], v[170:173], v[126:129], v[18:33]
	ds_read_b128 v[170:173], v134 offset:30720
	s_waitcnt lgkmcnt(4)
	v_mfma_f32_32x32x16_f16 v[2:17], v[66:69], v[126:129], v[2:17]
	ds_read_b128 v[126:129], v134 offset:19456
	s_waitcnt vmcnt(11) lgkmcnt(4)
	v_mfma_f32_32x32x16_f16 v[50:65], v[110:113], v[130:133], v[50:65]
	global_load_dwordx4 v[70:73], v[178:179], off offset:2048
	ds_read_b128 v[110:113], v134 offset:23552
	s_waitcnt lgkmcnt(4)
	v_mfma_f32_32x32x16_f16 v[34:49], v[174:177], v[130:133], v[34:49]
	ds_read_b128 v[174:177], v134 offset:27648
	s_waitcnt lgkmcnt(4)
	v_mfma_f32_32x32x16_f16 v[18:33], v[90:93], v[130:133], v[18:33]
	ds_read_b128 v[90:93], v134 offset:31744
	s_waitcnt lgkmcnt(4)
	v_mfma_f32_32x32x16_f16 v[2:17], v[170:173], v[130:133], v[2:17]
	global_load_dwordx4 v[66:69], v[178:179], off offset:3072
	s_waitcnt vmcnt(12) lgkmcnt(3)
	v_mfma_f32_32x32x16_f16 v[50:65], v[126:129], v[106:109], v[50:65]
	s_waitcnt lgkmcnt(0)
	s_barrier
	ds_read_b128 v[126:129], v134
	ds_read_b128 v[130:133], v134 offset:4096
	v_mfma_f32_32x32x16_f16 v[34:49], v[110:113], v[106:109], v[34:49]
	ds_read_b128 v[110:113], v134 offset:8192
	v_mfma_f32_32x32x16_f16 v[18:33], v[174:177], v[106:109], v[18:33]
	ds_read_b128 v[170:173], v134 offset:12288
	v_mfma_f32_32x32x16_f16 v[2:17], v[90:93], v[106:109], v[2:17]
	ds_read_b128 v[106:109], v134 offset:1024
	s_waitcnt vmcnt(11) lgkmcnt(4)
	v_mfma_f32_32x32x16_f16 v[50:65], v[126:129], v[78:81], v[50:65]
	s_mov_b32 s9, 0xe000
	v_add_co_u32_e32 v178, vcc, s9, v168
	ds_read_b128 v[126:129], v134 offset:5120
	s_nop 0
	v_addc_co_u32_e32 v179, vcc, 0, v169, vcc
	global_load_dwordx4 v[90:93], v[178:179], off offset:-4096
	s_mov_b32 s9, 0xd000
	v_add_co_u32_e32 v180, vcc, s9, v168
	s_waitcnt lgkmcnt(4)
	v_mfma_f32_32x32x16_f16 v[34:49], v[130:133], v[78:81], v[34:49]
	v_addc_co_u32_e32 v181, vcc, 0, v169, vcc
	ds_read_b128 v[130:133], v134 offset:9216
	s_waitcnt lgkmcnt(4)
	v_mfma_f32_32x32x16_f16 v[18:33], v[110:113], v[78:81], v[18:33]
	ds_read_b128 v[110:113], v134 offset:13312
	s_waitcnt lgkmcnt(4)
	v_mfma_f32_32x32x16_f16 v[2:17], v[170:173], v[78:81], v[2:17]
	ds_read_b128 v[78:81], v134 offset:2048
	s_waitcnt vmcnt(11) lgkmcnt(4)
	v_mfma_f32_32x32x16_f16 v[50:65], v[106:109], v[82:85], v[50:65]
	global_load_dwordx4 v[106:109], v[180:181], off offset:1024
	ds_read_b128 v[170:173], v134 offset:6144
	s_waitcnt lgkmcnt(4)
	v_mfma_f32_32x32x16_f16 v[34:49], v[126:129], v[82:85], v[34:49]
	ds_read_b128 v[126:129], v134 offset:10240
	s_waitcnt lgkmcnt(4)
	v_mfma_f32_32x32x16_f16 v[18:33], v[130:133], v[82:85], v[18:33]
	ds_read_b128 v[130:133], v134 offset:14336
	s_waitcnt lgkmcnt(4)
	v_mfma_f32_32x32x16_f16 v[2:17], v[110:113], v[82:85], v[2:17]
	ds_read_b128 v[110:113], v134 offset:3072
	s_waitcnt vmcnt(11) lgkmcnt(4)
	v_mfma_f32_32x32x16_f16 v[50:65], v[78:81], v[98:101], v[50:65]
	global_load_dwordx4 v[82:85], v[180:181], off offset:2048
	ds_read_b128 v[174:177], v134 offset:7168
	s_waitcnt lgkmcnt(4)
	v_mfma_f32_32x32x16_f16 v[34:49], v[170:173], v[98:101], v[34:49]
	ds_read_b128 v[170:173], v134 offset:11264
	s_waitcnt lgkmcnt(4)
	v_mfma_f32_32x32x16_f16 v[18:33], v[126:129], v[98:101], v[18:33]
	ds_read_b128 v[126:129], v134 offset:15360
	s_waitcnt lgkmcnt(4)
	v_mfma_f32_32x32x16_f16 v[2:17], v[130:133], v[98:101], v[2:17]
	global_load_dwordx4 v[78:81], v[180:181], off offset:3072
	s_waitcnt vmcnt(12) lgkmcnt(3)
	v_mfma_f32_32x32x16_f16 v[50:65], v[110:113], v[74:77], v[50:65]
	s_waitcnt lgkmcnt(0)
	s_barrier
	ds_read_b128 v[98:101], v134 offset:16384
	ds_read_b128 v[110:113], v134 offset:20480
	v_mfma_f32_32x32x16_f16 v[34:49], v[174:177], v[74:77], v[34:49]
	ds_read_b128 v[130:133], v134 offset:24576
	v_mfma_f32_32x32x16_f16 v[18:33], v[170:173], v[74:77], v[18:33]
	ds_read_b128 v[170:173], v134 offset:28672
	v_mfma_f32_32x32x16_f16 v[2:17], v[126:129], v[74:77], v[2:17]
	ds_read_b128 v[74:77], v134 offset:17408
	s_waitcnt vmcnt(11) lgkmcnt(4)
	v_mfma_f32_32x32x16_f16 v[50:65], v[98:101], v[114:117], v[50:65]
	global_load_dwordx4 v[98:101], v[178:179], off
	ds_read_b128 v[126:129], v134 offset:21504
	s_waitcnt lgkmcnt(4)
	v_mfma_f32_32x32x16_f16 v[34:49], v[110:113], v[114:117], v[34:49]
	ds_read_b128 v[174:177], v134 offset:25600
	s_waitcnt lgkmcnt(4)
	v_mfma_f32_32x32x16_f16 v[18:33], v[130:133], v[114:117], v[18:33]
	ds_read_b128 v[130:133], v134 offset:29696
	s_waitcnt lgkmcnt(4)
	v_mfma_f32_32x32x16_f16 v[2:17], v[170:173], v[114:117], v[2:17]
	ds_read_b128 v[114:117], v134 offset:18432
	s_waitcnt vmcnt(11) lgkmcnt(4)
	v_mfma_f32_32x32x16_f16 v[50:65], v[74:77], v[118:121], v[50:65]
	global_load_dwordx4 v[110:113], v[178:179], off offset:1024
	ds_read_b128 v[74:77], v134 offset:22528
	s_waitcnt lgkmcnt(4)
	v_mfma_f32_32x32x16_f16 v[34:49], v[126:129], v[118:121], v[34:49]
	ds_read_b128 v[126:129], v134 offset:26624
	s_waitcnt lgkmcnt(4)
	v_mfma_f32_32x32x16_f16 v[18:33], v[174:177], v[118:121], v[18:33]
	ds_read_b128 v[170:173], v134 offset:30720
	s_waitcnt lgkmcnt(4)
	v_mfma_f32_32x32x16_f16 v[2:17], v[130:133], v[118:121], v[2:17]
	ds_read_b128 v[118:121], v134 offset:19456
	s_waitcnt vmcnt(11) lgkmcnt(4)
	v_mfma_f32_32x32x16_f16 v[50:65], v[114:117], v[122:125], v[50:65]
	global_load_dwordx4 v[114:117], v[178:179], off offset:2048
	ds_read_b128 v[130:133], v134 offset:23552
	s_waitcnt lgkmcnt(4)
	v_mfma_f32_32x32x16_f16 v[34:49], v[74:77], v[122:125], v[34:49]
	ds_read_b128 v[174:177], v134 offset:27648
	s_waitcnt lgkmcnt(4)
	v_mfma_f32_32x32x16_f16 v[18:33], v[126:129], v[122:125], v[18:33]
	ds_read_b128 v[126:129], v134 offset:31744
	s_waitcnt lgkmcnt(4)
	v_mfma_f32_32x32x16_f16 v[2:17], v[170:173], v[122:125], v[2:17]
	global_load_dwordx4 v[74:77], v[178:179], off offset:3072
	s_waitcnt vmcnt(12) lgkmcnt(3)
	v_mfma_f32_32x32x16_f16 v[50:65], v[118:121], v[94:97], v[50:65]
	s_waitcnt lgkmcnt(0)
	s_barrier
	ds_read_b128 v[118:121], v134
	ds_read_b128 v[122:125], v134 offset:4096
	v_mfma_f32_32x32x16_f16 v[34:49], v[130:133], v[94:97], v[34:49]
	ds_read_b128 v[130:133], v134 offset:8192
	v_mfma_f32_32x32x16_f16 v[18:33], v[174:177], v[94:97], v[18:33]
	v_mfma_f32_32x32x16_f16 v[2:17], v[126:129], v[94:97], v[2:17]
	ds_read_b128 v[126:129], v134 offset:12288
	ds_read_b128 v[170:173], v134 offset:1024
	s_waitcnt vmcnt(11) lgkmcnt(4)
	v_mfma_f32_32x32x16_f16 v[50:65], v[118:121], v[102:105], v[50:65]
	s_mov_b32 s9, 0xf000
	v_add_co_u32_e32 v174, vcc, s9, v168
	ds_read_b128 v[118:121], v134 offset:5120
	s_nop 0
	v_addc_co_u32_e32 v175, vcc, 0, v169, vcc
	global_load_dwordx4 v[94:97], v[174:175], off
	s_waitcnt lgkmcnt(4)
	v_mfma_f32_32x32x16_f16 v[34:49], v[122:125], v[102:105], v[34:49]
	ds_read_b128 v[122:125], v134 offset:9216
	s_waitcnt lgkmcnt(4)
	v_mfma_f32_32x32x16_f16 v[18:33], v[130:133], v[102:105], v[18:33]
	s_waitcnt lgkmcnt(3)
	v_mfma_f32_32x32x16_f16 v[2:17], v[126:129], v[102:105], v[2:17]
	ds_read_b128 v[126:129], v134 offset:13312
	ds_read_b128 v[130:133], v134 offset:2048
	s_waitcnt vmcnt(11) lgkmcnt(4)
	v_mfma_f32_32x32x16_f16 v[50:65], v[170:173], v[86:89], v[50:65]
	global_load_dwordx4 v[102:105], v[174:175], off offset:1024
	s_waitcnt lgkmcnt(3)
	v_mfma_f32_32x32x16_f16 v[34:49], v[118:121], v[86:89], v[34:49]
	ds_read_b128 v[118:121], v134 offset:6144
	s_waitcnt lgkmcnt(3)
	v_mfma_f32_32x32x16_f16 v[18:33], v[122:125], v[86:89], v[18:33]
	ds_read_b128 v[122:125], v134 offset:10240
	s_waitcnt lgkmcnt(3)
	v_mfma_f32_32x32x16_f16 v[2:17], v[126:129], v[86:89], v[2:17]
	ds_read_b128 v[126:129], v134 offset:14336
	ds_read_b128 v[168:171], v134 offset:3072
	s_waitcnt vmcnt(11) lgkmcnt(4)
	v_mfma_f32_32x32x16_f16 v[50:65], v[130:133], v[70:73], v[50:65]
	global_load_dwordx4 v[86:89], v[174:175], off offset:2048
	s_waitcnt lgkmcnt(3)
	v_mfma_f32_32x32x16_f16 v[34:49], v[118:121], v[70:73], v[34:49]
	ds_read_b128 v[118:121], v134 offset:7168
	s_waitcnt lgkmcnt(3)
	v_mfma_f32_32x32x16_f16 v[18:33], v[122:125], v[70:73], v[18:33]
	ds_read_b128 v[122:125], v134 offset:11264
	s_waitcnt lgkmcnt(3)
	v_mfma_f32_32x32x16_f16 v[2:17], v[126:129], v[70:73], v[2:17]
	ds_read_b128 v[126:129], v134 offset:15360
	global_load_dwordx4 v[70:73], v[174:175], off offset:3072
	s_waitcnt vmcnt(12) lgkmcnt(3)
	v_mfma_f32_32x32x16_f16 v[50:65], v[168:171], v[66:69], v[50:65]
	s_waitcnt lgkmcnt(0)
	s_barrier
	ds_read_b128 v[130:133], v134 offset:16384
	v_mfma_f32_32x32x16_f16 v[34:49], v[118:121], v[66:69], v[34:49]
	ds_read_b128 v[118:121], v134 offset:20480
	v_mfma_f32_32x32x16_f16 v[18:33], v[122:125], v[66:69], v[18:33]
	ds_read_b128 v[122:125], v134 offset:24576
	v_mfma_f32_32x32x16_f16 v[2:17], v[126:129], v[66:69], v[2:17]
	ds_read_b128 v[66:69], v134 offset:28672
	ds_read_b128 v[126:129], v134 offset:17408
	s_waitcnt vmcnt(11) lgkmcnt(4)
	v_mfma_f32_32x32x16_f16 v[50:65], v[130:133], v[90:93], v[50:65]
	ds_read_b128 v[130:133], v134 offset:21504
	s_waitcnt lgkmcnt(4)
	v_mfma_f32_32x32x16_f16 v[34:49], v[118:121], v[90:93], v[34:49]
	ds_read_b128 v[118:121], v134 offset:25600
	s_waitcnt lgkmcnt(4)
	v_mfma_f32_32x32x16_f16 v[18:33], v[122:125], v[90:93], v[18:33]
	ds_read_b128 v[122:125], v134 offset:29696
	s_waitcnt lgkmcnt(4)
	v_mfma_f32_32x32x16_f16 v[2:17], v[66:69], v[90:93], v[2:17]
	ds_read_b128 v[66:69], v134 offset:18432
	s_waitcnt vmcnt(10) lgkmcnt(4)
	v_mfma_f32_32x32x16_f16 v[50:65], v[126:129], v[106:109], v[50:65]
	ds_read_b128 v[90:93], v134 offset:22528
	s_waitcnt lgkmcnt(4)
	v_mfma_f32_32x32x16_f16 v[34:49], v[130:133], v[106:109], v[34:49]
	ds_read_b128 v[126:129], v134 offset:26624
	s_waitcnt lgkmcnt(4)
	v_mfma_f32_32x32x16_f16 v[18:33], v[118:121], v[106:109], v[18:33]
	ds_read_b128 v[118:121], v134 offset:30720
	s_waitcnt lgkmcnt(4)
	v_mfma_f32_32x32x16_f16 v[2:17], v[122:125], v[106:109], v[2:17]
	ds_read_b128 v[106:109], v134 offset:19456
	s_waitcnt vmcnt(9) lgkmcnt(4)
	v_mfma_f32_32x32x16_f16 v[50:65], v[66:69], v[82:85], v[50:65]
	ds_read_b128 v[66:69], v134 offset:23552
	s_waitcnt lgkmcnt(4)
	v_mfma_f32_32x32x16_f16 v[34:49], v[90:93], v[82:85], v[34:49]
	ds_read_b128 v[90:93], v134 offset:27648
	s_waitcnt lgkmcnt(4)
	v_mfma_f32_32x32x16_f16 v[18:33], v[126:129], v[82:85], v[18:33]
	ds_read_b128 v[122:125], v134 offset:31744
	s_waitcnt lgkmcnt(4)
	v_mfma_f32_32x32x16_f16 v[2:17], v[118:121], v[82:85], v[2:17]
	s_waitcnt vmcnt(8) lgkmcnt(3)
	v_mfma_f32_32x32x16_f16 v[50:65], v[106:109], v[78:81], v[50:65]
	s_waitcnt lgkmcnt(0)
	s_barrier
	ds_read_b128 v[82:85], v134
	ds_read_b128 v[106:109], v134 offset:4096
	v_mfma_f32_32x32x16_f16 v[34:49], v[66:69], v[78:81], v[34:49]
	ds_read_b128 v[66:69], v134 offset:8192
	v_mfma_f32_32x32x16_f16 v[18:33], v[90:93], v[78:81], v[18:33]
	ds_read_b128 v[90:93], v134 offset:12288
	v_mfma_f32_32x32x16_f16 v[2:17], v[122:125], v[78:81], v[2:17]
	ds_read_b128 v[78:81], v134 offset:1024
	s_waitcnt vmcnt(7) lgkmcnt(4)
	v_mfma_f32_32x32x16_f16 v[50:65], v[82:85], v[98:101], v[50:65]
	ds_read_b128 v[82:85], v134 offset:5120
	s_waitcnt lgkmcnt(4)
	v_mfma_f32_32x32x16_f16 v[34:49], v[106:109], v[98:101], v[34:49]
	ds_read_b128 v[106:109], v134 offset:9216
	s_waitcnt lgkmcnt(4)
	v_mfma_f32_32x32x16_f16 v[18:33], v[66:69], v[98:101], v[18:33]
	ds_read_b128 v[66:69], v134 offset:13312
	s_waitcnt lgkmcnt(4)
	v_mfma_f32_32x32x16_f16 v[2:17], v[90:93], v[98:101], v[2:17]
	ds_read_b128 v[90:93], v134 offset:2048
	s_waitcnt vmcnt(6) lgkmcnt(4)
	v_mfma_f32_32x32x16_f16 v[50:65], v[78:81], v[110:113], v[50:65]
	ds_read_b128 v[78:81], v134 offset:6144
	s_waitcnt lgkmcnt(4)
	v_mfma_f32_32x32x16_f16 v[34:49], v[82:85], v[110:113], v[34:49]
	ds_read_b128 v[82:85], v134 offset:10240
	s_waitcnt lgkmcnt(4)
	v_mfma_f32_32x32x16_f16 v[18:33], v[106:109], v[110:113], v[18:33]
	ds_read_b128 v[98:101], v134 offset:14336
	s_waitcnt lgkmcnt(4)
	v_mfma_f32_32x32x16_f16 v[2:17], v[66:69], v[110:113], v[2:17]
	ds_read_b128 v[66:69], v134 offset:3072
	s_waitcnt vmcnt(5) lgkmcnt(4)
	v_mfma_f32_32x32x16_f16 v[50:65], v[90:93], v[114:117], v[50:65]
	ds_read_b128 v[90:93], v134 offset:7168
	s_waitcnt lgkmcnt(4)
	v_mfma_f32_32x32x16_f16 v[34:49], v[78:81], v[114:117], v[34:49]
	ds_read_b128 v[78:81], v134 offset:11264
	s_waitcnt lgkmcnt(4)
	v_mfma_f32_32x32x16_f16 v[18:33], v[82:85], v[114:117], v[18:33]
	ds_read_b128 v[82:85], v134 offset:15360
	s_waitcnt lgkmcnt(4)
	v_mfma_f32_32x32x16_f16 v[2:17], v[98:101], v[114:117], v[2:17]
	s_waitcnt vmcnt(4) lgkmcnt(3)
	v_mfma_f32_32x32x16_f16 v[50:65], v[66:69], v[74:77], v[50:65]
	s_waitcnt lgkmcnt(0)
	s_barrier
	ds_read_b128 v[66:69], v134 offset:16384
	ds_read_b128 v[98:101], v134 offset:20480
	v_mfma_f32_32x32x16_f16 v[34:49], v[90:93], v[74:77], v[34:49]
	ds_read_b128 v[90:93], v134 offset:24576
	v_mfma_f32_32x32x16_f16 v[18:33], v[78:81], v[74:77], v[18:33]
	ds_read_b128 v[78:81], v134 offset:28672
	v_mfma_f32_32x32x16_f16 v[2:17], v[82:85], v[74:77], v[2:17]
	ds_read_b128 v[74:77], v134 offset:17408
	s_waitcnt vmcnt(3) lgkmcnt(4)
	v_mfma_f32_32x32x16_f16 v[50:65], v[66:69], v[94:97], v[50:65]
	ds_read_b128 v[66:69], v134 offset:21504
	s_waitcnt lgkmcnt(4)
	v_mfma_f32_32x32x16_f16 v[34:49], v[98:101], v[94:97], v[34:49]
	ds_read_b128 v[82:85], v134 offset:25600
	s_waitcnt lgkmcnt(4)
	v_mfma_f32_32x32x16_f16 v[18:33], v[90:93], v[94:97], v[18:33]
	ds_read_b128 v[90:93], v134 offset:29696
	s_waitcnt lgkmcnt(4)
	v_mfma_f32_32x32x16_f16 v[2:17], v[78:81], v[94:97], v[2:17]
	s_waitcnt vmcnt(2) lgkmcnt(3)
	v_mfma_f32_32x32x16_f16 v[50:65], v[74:77], v[102:105], v[50:65]
	ds_read_b128 v[74:77], v134 offset:18432
	s_waitcnt lgkmcnt(3)
	v_mfma_f32_32x32x16_f16 v[34:49], v[66:69], v[102:105], v[34:49]
	ds_read_b128 v[66:69], v134 offset:22528
	ds_read_b128 v[78:81], v134 offset:26624
	s_waitcnt lgkmcnt(4)
	v_mfma_f32_32x32x16_f16 v[18:33], v[82:85], v[102:105], v[18:33]
	ds_read_b128 v[82:85], v134 offset:30720
	s_waitcnt lgkmcnt(4)
	v_mfma_f32_32x32x16_f16 v[2:17], v[90:93], v[102:105], v[2:17]
	ds_read_b128 v[90:93], v134 offset:19456
	s_waitcnt vmcnt(1) lgkmcnt(4)
	v_mfma_f32_32x32x16_f16 v[50:65], v[74:77], v[86:89], v[50:65]
	ds_read_b128 v[74:77], v134 offset:23552
	s_waitcnt lgkmcnt(4)
	v_mfma_f32_32x32x16_f16 v[34:49], v[66:69], v[86:89], v[34:49]
	ds_read_b128 v[66:69], v134 offset:27648
	s_waitcnt lgkmcnt(4)
	v_mfma_f32_32x32x16_f16 v[18:33], v[78:81], v[86:89], v[18:33]
	ds_read_b128 v[78:81], v134 offset:31744
	s_waitcnt lgkmcnt(4)
	v_mfma_f32_32x32x16_f16 v[2:17], v[82:85], v[86:89], v[2:17]
	s_waitcnt vmcnt(0) lgkmcnt(3)
	v_mfma_f32_32x32x16_f16 v[50:65], v[90:93], v[70:73], v[50:65]
	s_waitcnt lgkmcnt(2)
	v_mfma_f32_32x32x16_f16 v[34:49], v[74:77], v[70:73], v[34:49]
	s_waitcnt lgkmcnt(1)
	v_mfma_f32_32x32x16_f16 v[18:33], v[66:69], v[70:73], v[18:33]
	s_waitcnt lgkmcnt(0)
	v_mfma_f32_32x32x16_f16 v[2:17], v[78:81], v[70:73], v[2:17]
	v_cvt_f32_f16_e32 v66, v166
	v_cvt_f32_f16_sdwa v67, v166 dst_sel:DWORD dst_unused:UNUSED_PAD src0_sel:WORD_1
	v_cvt_f32_f16_e32 v68, v167
	v_cvt_f32_f16_sdwa v69, v167 dst_sel:DWORD dst_unused:UNUSED_PAD src0_sel:WORD_1
	v_cvt_f32_f16_e32 v70, v164
	v_cvt_f32_f16_sdwa v71, v164 dst_sel:DWORD dst_unused:UNUSED_PAD src0_sel:WORD_1
	v_cvt_f32_f16_e32 v72, v165
	v_cvt_f32_f16_sdwa v73, v165 dst_sel:DWORD dst_unused:UNUSED_PAD src0_sel:WORD_1
	v_cvt_f32_f16_e32 v74, v162
	v_cvt_f32_f16_sdwa v75, v162 dst_sel:DWORD dst_unused:UNUSED_PAD src0_sel:WORD_1
	v_pk_fma_f32 v[66:67], v[66:67], v[66:67], 1.0 op_sel_hi:[1,1,0] neg_lo:[1,0,0] neg_hi:[1,0,0]
	v_cvt_f32_f16_e32 v76, v163
	v_cvt_f32_f16_sdwa v77, v163 dst_sel:DWORD dst_unused:UNUSED_PAD src0_sel:WORD_1
	v_pk_mul_f32 v[66:67], v[50:51], v[66:67]
	v_pk_fma_f32 v[50:51], v[68:69], v[68:69], 1.0 op_sel_hi:[1,1,0] neg_lo:[1,0,0] neg_hi:[1,0,0]
	s_nop 0
	v_pk_mul_f32 v[68:69], v[52:53], v[50:51]
	v_pk_fma_f32 v[50:51], v[70:71], v[70:71], 1.0 op_sel_hi:[1,1,0] neg_lo:[1,0,0] neg_hi:[1,0,0]
	s_barrier
	v_pk_mul_f32 v[54:55], v[54:55], v[50:51]
	v_pk_fma_f32 v[50:51], v[72:73], v[72:73], 1.0 op_sel_hi:[1,1,0] neg_lo:[1,0,0] neg_hi:[1,0,0]
	s_nop 0
	v_pk_mul_f32 v[56:57], v[56:57], v[50:51]
	v_pk_fma_f32 v[50:51], v[74:75], v[74:75], 1.0 op_sel_hi:[1,1,0] neg_lo:[1,0,0] neg_hi:[1,0,0]
	v_cvt_f32_f16_e32 v78, v160
	v_pk_mul_f32 v[90:91], v[58:59], v[50:51]
	v_pk_fma_f32 v[50:51], v[76:77], v[76:77], 1.0 op_sel_hi:[1,1,0] neg_lo:[1,0,0] neg_hi:[1,0,0]
	v_cvt_f32_f16_sdwa v79, v160 dst_sel:DWORD dst_unused:UNUSED_PAD src0_sel:WORD_1
	v_pk_mul_f32 v[92:93], v[60:61], v[50:51]
	ds_read_b128 v[50:53], v134 offset:33792
	v_cvt_f32_f16_e32 v86, v161
	v_cvt_f32_f16_sdwa v87, v161 dst_sel:DWORD dst_unused:UNUSED_PAD src0_sel:WORD_1
	v_cvt_pk_f16_f32 v57, v56, v57
	v_cvt_pk_f16_f32 v56, v54, v55
	v_cvt_pk_f16_f32 v55, v68, v69
	v_cvt_pk_f16_f32 v54, v66, v67
	v_pk_fma_f32 v[58:59], v[78:79], v[78:79], 1.0 op_sel_hi:[1,1,0] neg_lo:[1,0,0] neg_hi:[1,0,0]
	v_cvt_f32_f16_e32 v94, v152
	s_waitcnt lgkmcnt(0)
	v_mfma_f32_32x32x16_f16 v[66:81], v[50:53], v[54:57], 0
	v_fma_f32 v50, -v86, v86, 1.0
	v_fma_f32 v51, -v87, v87, 1.0
	v_mul_f32_e64 v62, v62, v58
	v_mul_f32_e64 v63, v63, v59
	ds_read_b128 v[58:61], v134 offset:34816
	ds_read_b128 v[82:85], v134 offset:35840
	v_pk_mul_f32 v[50:51], v[64:65], v[50:51]
	v_cvt_f32_f16_e32 v52, v159
	v_cvt_pk_f16_f32 v89, v50, v51
	v_cvt_f32_f16_e32 v50, v158
	v_cvt_f32_f16_sdwa v51, v158 dst_sel:DWORD dst_unused:UNUSED_PAD src0_sel:WORD_1
	v_cvt_f32_f16_sdwa v53, v159 dst_sel:DWORD dst_unused:UNUSED_PAD src0_sel:WORD_1
	v_cvt_pk_f16_f32 v88, v62, v63
	v_cvt_f32_f16_e32 v62, v156
	v_cvt_f32_f16_sdwa v63, v156 dst_sel:DWORD dst_unused:UNUSED_PAD src0_sel:WORD_1
	v_cvt_pk_f16_f32 v87, v92, v93
	v_cvt_pk_f16_f32 v86, v90, v91
	v_cvt_f32_f16_e32 v64, v157
	v_cvt_f32_f16_sdwa v65, v157 dst_sel:DWORD dst_unused:UNUSED_PAD src0_sel:WORD_1
	s_waitcnt lgkmcnt(0)
	v_mfma_f32_32x32x16_f16 v[66:81], v[82:85], v[86:89], v[66:81]
	v_cvt_f32_f16_e32 v82, v154
	v_cvt_f32_f16_sdwa v83, v154 dst_sel:DWORD dst_unused:UNUSED_PAD src0_sel:WORD_1
	v_fma_f32 v50, -v50, v50, 1.0
	v_fma_f32 v51, -v51, v51, 1.0
	v_cvt_f32_f16_e32 v84, v155
	v_cvt_f32_f16_sdwa v85, v155 dst_sel:DWORD dst_unused:UNUSED_PAD src0_sel:WORD_1
	v_pk_mul_f32 v[98:99], v[34:35], v[50:51]
	v_pk_fma_f32 v[34:35], v[52:53], v[52:53], 1.0 op_sel_hi:[1,1,0] neg_lo:[1,0,0] neg_hi:[1,0,0]
	v_cvt_f32_f16_sdwa v95, v152 dst_sel:DWORD dst_unused:UNUSED_PAD src0_sel:WORD_1
	v_pk_mul_f32 v[100:101], v[36:37], v[34:35]
	v_pk_fma_f32 v[34:35], v[62:63], v[62:63], 1.0 op_sel_hi:[1,1,0] neg_lo:[1,0,0] neg_hi:[1,0,0]
	ds_read_b128 v[90:93], v134 offset:36864
	v_pk_mul_f32 v[38:39], v[38:39], v[34:35]
	v_pk_fma_f32 v[34:35], v[64:65], v[64:65], 1.0 op_sel_hi:[1,1,0] neg_lo:[1,0,0] neg_hi:[1,0,0]
	v_mfma_f32_32x32x16_f16 v[50:65], v[58:61], v[54:57], 0
	v_mul_f32_e64 v40, v40, v34
	v_mul_f32_e64 v41, v41, v35
	v_fma_f32 v34, -v82, v82, 1.0
	v_fma_f32 v35, -v83, v83, 1.0
	v_cvt_pk_f16_f32 v41, v40, v41
	v_pk_mul_f32 v[82:83], v[42:43], v[34:35]
	v_pk_fma_f32 v[34:35], v[84:85], v[84:85], 1.0 op_sel_hi:[1,1,0] neg_lo:[1,0,0] neg_hi:[1,0,0]
	v_cvt_pk_f16_f32 v40, v38, v39
	v_pk_mul_f32 v[84:85], v[44:45], v[34:35]
	v_pk_fma_f32 v[34:35], v[94:95], v[94:95], 1.0 op_sel_hi:[1,1,0] neg_lo:[1,0,0] neg_hi:[1,0,0]
	v_cvt_pk_f16_f32 v39, v100, v101
	v_pk_mul_f32 v[46:47], v[46:47], v[34:35]
	ds_read_b128 v[34:37], v134 offset:37888
	v_cvt_pk_f16_f32 v38, v98, v99
	v_cvt_f32_f16_e32 v96, v153
	v_cvt_f32_f16_sdwa v97, v153 dst_sel:DWORD dst_unused:UNUSED_PAD src0_sel:WORD_1
	s_waitcnt lgkmcnt(0)
	v_mfma_f32_32x32x16_f16 v[66:81], v[34:37], v[38:41], v[66:81]
	v_cvt_f32_f16_e32 v34, v150
	v_cvt_f32_f16_sdwa v35, v150 dst_sel:DWORD dst_unused:UNUSED_PAD src0_sel:WORD_1
	v_cvt_f32_f16_e32 v36, v151
	v_cvt_f32_f16_sdwa v37, v151 dst_sel:DWORD dst_unused:UNUSED_PAD src0_sel:WORD_1
	v_fma_f32 v42, -v96, v96, 1.0
	v_fma_f32 v43, -v97, v97, 1.0
	v_pk_fma_f32 v[34:35], v[34:35], v[34:35], 1.0 op_sel_hi:[1,1,0] neg_lo:[1,0,0] neg_hi:[1,0,0]
	v_pk_mul_f32 v[48:49], v[48:49], v[42:43]
	v_mfma_f32_32x32x16_f16 v[50:65], v[90:93], v[86:89], v[50:65]
	v_cvt_f32_f16_e32 v86, v148
	v_cvt_f32_f16_sdwa v87, v148 dst_sel:DWORD dst_unused:UNUSED_PAD src0_sel:WORD_1
	v_cvt_f32_f16_e32 v88, v149
	v_cvt_f32_f16_sdwa v89, v149 dst_sel:DWORD dst_unused:UNUSED_PAD src0_sel:WORD_1
	v_cvt_f32_f16_e32 v90, v146
	v_cvt_f32_f16_sdwa v91, v146 dst_sel:DWORD dst_unused:UNUSED_PAD src0_sel:WORD_1
	ds_read_b128 v[42:45], v134 offset:38912
	v_cvt_f32_f16_e32 v92, v147
	v_cvt_f32_f16_sdwa v93, v147 dst_sel:DWORD dst_unused:UNUSED_PAD src0_sel:WORD_1
	v_pk_mul_f32 v[34:35], v[18:19], v[34:35]
	v_pk_fma_f32 v[18:19], v[36:37], v[36:37], 1.0 op_sel_hi:[1,1,0] neg_lo:[1,0,0] neg_hi:[1,0,0]
	v_cvt_f32_f16_e32 v94, v144
	v_cvt_f32_f16_sdwa v95, v144 dst_sel:DWORD dst_unused:UNUSED_PAD src0_sel:WORD_1
	v_pk_mul_f32 v[36:37], v[20:21], v[18:19]
	v_pk_fma_f32 v[18:19], v[86:87], v[86:87], 1.0 op_sel_hi:[1,1,0] neg_lo:[1,0,0] neg_hi:[1,0,0]
	v_cvt_f32_f16_e32 v96, v145
	v_pk_mul_f32 v[86:87], v[22:23], v[18:19]
	v_pk_fma_f32 v[18:19], v[88:89], v[88:89], 1.0 op_sel_hi:[1,1,0] neg_lo:[1,0,0] neg_hi:[1,0,0]
	v_cvt_f32_f16_sdwa v97, v145 dst_sel:DWORD dst_unused:UNUSED_PAD src0_sel:WORD_1
	v_pk_mul_f32 v[88:89], v[24:25], v[18:19]
	v_pk_fma_f32 v[18:19], v[90:91], v[90:91], 1.0 op_sel_hi:[1,1,0] neg_lo:[1,0,0] neg_hi:[1,0,0]
	v_cvt_pk_f16_f32 v25, v48, v49
	v_pk_mul_f32 v[90:91], v[26:27], v[18:19]
	v_pk_fma_f32 v[18:19], v[92:93], v[92:93], 1.0 op_sel_hi:[1,1,0] neg_lo:[1,0,0] neg_hi:[1,0,0]
	v_cvt_pk_f16_f32 v24, v46, v47
	v_pk_mul_f32 v[92:93], v[28:29], v[18:19]
	v_pk_fma_f32 v[18:19], v[94:95], v[94:95], 1.0 op_sel_hi:[1,1,0] neg_lo:[1,0,0] neg_hi:[1,0,0]
	ds_read_b128 v[26:29], v134 offset:40960
	v_pk_mul_f32 v[30:31], v[30:31], v[18:19]
	ds_read_b128 v[18:21], v134 offset:39936
	s_waitcnt lgkmcnt(2)
	v_mfma_f32_32x32x16_f16 v[50:65], v[42:45], v[38:41], v[50:65]
	v_cvt_f32_f16_e32 v40, v142
	v_cvt_f32_f16_sdwa v41, v142 dst_sel:DWORD dst_unused:UNUSED_PAD src0_sel:WORD_1
	v_fma_f32 v38, -v96, v96, 1.0
	v_fma_f32 v39, -v97, v97, 1.0
	v_cvt_pk_f16_f32 v23, v84, v85
	v_cvt_pk_f16_f32 v22, v82, v83
	v_pk_mul_f32 v[32:33], v[32:33], v[38:39]
	v_cvt_f32_f16_e32 v38, v143
	s_waitcnt lgkmcnt(0)
	v_mfma_f32_32x32x16_f16 v[66:81], v[18:21], v[22:25], v[66:81]
	v_cvt_f32_f16_sdwa v39, v143 dst_sel:DWORD dst_unused:UNUSED_PAD src0_sel:WORD_1
	v_fma_f32 v18, -v40, v40, 1.0
	v_fma_f32 v19, -v41, v41, 1.0
	s_or_b32 s6, s6, s7
	v_mul_f32_e64 v40, v2, v18
	v_mul_f32_e64 v41, v3, v19
	ds_read_b128 v[18:21], v134 offset:41984
	v_pk_fma_f32 v[2:3], v[38:39], v[38:39], 1.0 op_sel_hi:[1,1,0] neg_lo:[1,0,0] neg_hi:[1,0,0]
	v_cvt_f32_f16_e32 v38, v140
	v_mfma_f32_32x32x16_f16 v[50:65], v[26:29], v[22:25], v[50:65]
	ds_read_b128 v[26:29], v134 offset:43008
	v_cvt_f32_f16_sdwa v39, v140 dst_sel:DWORD dst_unused:UNUSED_PAD src0_sel:WORD_1
	v_cvt_pk_f16_f32 v22, v34, v35
	v_mul_f32_e64 v34, v4, v2
	v_mul_f32_e64 v35, v5, v3
	v_cvt_pk_f16_f32 v25, v88, v89
	v_pk_fma_f32 v[2:3], v[38:39], v[38:39], 1.0 op_sel_hi:[1,1,0] neg_lo:[1,0,0] neg_hi:[1,0,0]
	v_cvt_pk_f16_f32 v24, v86, v87
	v_cvt_pk_f16_f32 v23, v36, v37
	v_pk_mul_f32 v[6:7], v[6:7], v[2:3]
	ds_read_b128 v[2:5], v134 offset:44032
	s_waitcnt lgkmcnt(2)
	v_mfma_f32_32x32x16_f16 v[66:81], v[18:21], v[22:25], v[66:81]
	v_cvt_f32_f16_e32 v18, v141
	v_cvt_f32_f16_sdwa v19, v141 dst_sel:DWORD dst_unused:UNUSED_PAD src0_sel:WORD_1
	v_cvt_pk_f16_f32 v21, v32, v33
	v_cvt_pk_f16_f32 v20, v30, v31
	s_ashr_i32 s7, s6, 31
	s_lshl_b64 s[6:7], s[6:7], 12
	s_add_u32 s2, s2, s6
	s_waitcnt lgkmcnt(1)
	v_mfma_f32_32x32x16_f16 v[50:65], v[26:29], v[22:25], v[50:65]
	ds_read_b128 v[22:25], v134 offset:45056
	v_cvt_f32_f16_e32 v28, v138
	v_cvt_f32_f16_sdwa v29, v138 dst_sel:DWORD dst_unused:UNUSED_PAD src0_sel:WORD_1
	v_fma_f32 v26, -v18, v18, 1.0
	v_fma_f32 v27, -v19, v19, 1.0
	v_cvt_pk_f16_f32 v19, v92, v93
	v_cvt_pk_f16_f32 v18, v90, v91
	v_pk_mul_f32 v[8:9], v[8:9], v[26:27]
	v_cvt_f32_f16_e32 v26, v139
	s_waitcnt lgkmcnt(1)
	v_mfma_f32_32x32x16_f16 v[66:81], v[2:5], v[18:21], v[66:81]
	v_fma_f32 v2, -v28, v28, 1.0
	v_fma_f32 v3, -v29, v29, 1.0
	v_cvt_f32_f16_sdwa v27, v139 dst_sel:DWORD dst_unused:UNUSED_PAD src0_sel:WORD_1
	v_mul_f32_e64 v10, v10, v2
	v_mul_f32_e64 v11, v11, v3
	ds_read_b128 v[2:5], v134 offset:46080
	v_cvt_pk_f16_f32 v9, v8, v9
	v_cvt_pk_f16_f32 v8, v6, v7
	v_cvt_pk_f16_f32 v7, v34, v35
	s_waitcnt lgkmcnt(1)
	v_mfma_f32_32x32x16_f16 v[50:65], v[22:25], v[18:21], v[50:65]
	ds_read_b128 v[18:21], v134 offset:47104
	v_fma_f32 v22, -v26, v26, 1.0
	v_fma_f32 v23, -v27, v27, 1.0
	v_cvt_f32_f16_e32 v24, v136
	v_cvt_f32_f16_sdwa v25, v136 dst_sel:DWORD dst_unused:UNUSED_PAD src0_sel:WORD_1
	v_pk_mul_f32 v[12:13], v[12:13], v[22:23]
	v_cvt_f32_f16_e32 v22, v137
	v_cvt_f32_f16_sdwa v23, v137 dst_sel:DWORD dst_unused:UNUSED_PAD src0_sel:WORD_1
	v_cvt_pk_f16_f32 v6, v40, v41
	s_addc_u32 s3, s3, s7
	s_waitcnt lgkmcnt(1)
	v_mfma_f32_32x32x16_f16 v[66:81], v[2:5], v[6:9], v[66:81]
	v_fma_f32 v2, -v24, v24, 1.0
	v_fma_f32 v3, -v25, v25, 1.0
	v_mul_f32_e64 v14, v14, v2
	v_mul_f32_e64 v15, v15, v3
	ds_read_b128 v[2:5], v134 offset:48128
	s_waitcnt lgkmcnt(1)
	v_mfma_f32_32x32x16_f16 v[50:65], v[18:21], v[6:9], v[50:65]
	v_fma_f32 v6, -v22, v22, 1.0
	v_fma_f32 v7, -v23, v23, 1.0
	v_cvt_pk_f16_f32 v8, v14, v15
	v_mul_f32_e64 v6, v16, v6
	v_mul_f32_e64 v7, v17, v7
	v_cvt_pk_f16_f32 v9, v6, v7
	v_cvt_pk_f16_f32 v7, v12, v13
	v_cvt_pk_f16_f32 v6, v10, v11
	ds_read_b128 v[10:13], v134 offset:49152
	s_waitcnt lgkmcnt(1)
	v_mfma_f32_32x32x16_f16 v[66:81], v[2:5], v[6:9], v[66:81]
	s_waitcnt lgkmcnt(0)
	v_mfma_f32_32x32x16_f16 v[50:65], v[10:13], v[6:9], v[50:65]
	s_nop 9
	v_cvt_pk_f16_f32 v5, v72, v73
	v_cvt_pk_f16_f32 v4, v70, v71
	v_cvt_pk_f16_f32 v3, v68, v69
	v_cvt_pk_f16_f32 v2, v66, v67
	global_store_dwordx4 v134, v[2:5], s[2:3] sc1
	s_nop 1
	v_cvt_pk_f16_f32 v5, v80, v81
	v_cvt_pk_f16_f32 v4, v78, v79
	v_cvt_pk_f16_f32 v3, v76, v77
	v_cvt_pk_f16_f32 v2, v74, v75
	global_store_dwordx4 v134, v[2:5], s[2:3] offset:1024 sc1
	s_nop 1
	v_cvt_pk_f16_f32 v5, v56, v57
	v_cvt_pk_f16_f32 v4, v54, v55
	v_cvt_pk_f16_f32 v3, v52, v53
	v_cvt_pk_f16_f32 v2, v50, v51
	global_store_dwordx4 v134, v[2:5], s[2:3] offset:2048 sc1
	s_nop 1
	v_cvt_pk_f16_f32 v5, v64, v65
	v_cvt_pk_f16_f32 v4, v62, v63
	v_cvt_pk_f16_f32 v3, v60, v61
	v_cvt_pk_f16_f32 v2, v58, v59
	global_store_dwordx4 v134, v[2:5], s[2:3] offset:3072 sc1
	s_cbranch_execnz .LBB3_2
.LBB3_4:
	s_load_dwordx2 s[6:7], s[0:1], 0x0
	s_load_dwordx2 s[2:3], s[0:1], 0x38
	s_lshr_b32 s0, s8, 6
	s_lshl_b32 s1, s4, 8
	s_lshl_b32 s8, s5, 7
	s_add_i32 s8, s8, s1
	s_ashr_i32 s9, s8, 31
	s_lshl_b64 s[8:9], s[8:9], 10
	s_waitcnt lgkmcnt(0)
	s_add_u32 s6, s6, s8
	s_addc_u32 s7, s7, s9
	v_mov_b32_e32 v135, 0
	v_lshl_add_u64 v[2:3], s[6:7], 0, v[134:135]
	s_mov_b32 s1, 0x10000
	v_add_co_u32_e32 v36, vcc, s1, v2
	s_mov_b32 s1, 0x11000
	s_nop 0
	v_addc_co_u32_e32 v37, vcc, 0, v3, vcc
	v_add_co_u32_e32 v68, vcc, s1, v2
	global_load_dwordx4 v[4:7], v134, s[6:7]
	global_load_dwordx4 v[8:11], v134, s[6:7] offset:1024
	global_load_dwordx4 v[12:15], v134, s[6:7] offset:2048
	v_addc_co_u32_e32 v69, vcc, 0, v3, vcc
	global_load_dwordx4 v[16:19], v134, s[6:7] offset:3072
	global_load_dwordx4 v[20:23], v[68:69], off offset:-4096
	global_load_dwordx4 v[24:27], v[36:37], off offset:1024
	global_load_dwordx4 v[28:31], v[36:37], off offset:2048
	global_load_dwordx4 v[32:35], v[36:37], off offset:3072
	s_movk_i32 s7, 0x2000
	v_add_co_u32_e32 v100, vcc, s7, v2
	s_movk_i32 s6, 0x1000
	s_nop 0
	v_addc_co_u32_e32 v101, vcc, 0, v3, vcc
	v_add_co_u32_e32 v70, vcc, s6, v2
	global_load_dwordx4 v[36:39], v[100:101], off offset:-4096
	s_nop 0
	v_addc_co_u32_e32 v71, vcc, 0, v3, vcc
	global_load_dwordx4 v[40:43], v[70:71], off offset:1024
	global_load_dwordx4 v[44:47], v[70:71], off offset:2048
	global_load_dwordx4 v[48:51], v[70:71], off offset:3072
	global_load_dwordx4 v[52:55], v[68:69], off
	global_load_dwordx4 v[56:59], v[68:69], off offset:1024
	global_load_dwordx4 v[60:63], v[68:69], off offset:2048
	global_load_dwordx4 v[64:67], v[68:69], off offset:3072
	s_mov_b32 s1, 0x12000
	v_add_co_u32_e32 v102, vcc, s1, v2
	s_mov_b32 s8, 0x13000
	s_nop 0
	v_addc_co_u32_e32 v103, vcc, 0, v3, vcc
	v_add_co_u32_e32 v104, vcc, s8, v2
	s_movk_i32 s9, 0x4000
	s_nop 0
	v_addc_co_u32_e32 v105, vcc, 0, v3, vcc
	v_add_co_u32_e32 v106, vcc, s9, v2
	global_load_dwordx4 v[68:71], v[100:101], off
	global_load_dwordx4 v[72:75], v[100:101], off offset:1024
	global_load_dwordx4 v[76:79], v[100:101], off offset:2048
	global_load_dwordx4 v[80:83], v[100:101], off offset:3072
	global_load_dwordx4 v[84:87], v[104:105], off offset:-4096
	global_load_dwordx4 v[88:91], v[102:103], off offset:1024
	global_load_dwordx4 v[92:95], v[102:103], off offset:2048
	global_load_dwordx4 v[96:99], v[102:103], off offset:3072
	v_lshl_or_b32 v1, s5, 13, v134
	s_movk_i32 s5, 0x3000
	v_addc_co_u32_e32 v107, vcc, 0, v3, vcc
	v_add_co_u32_e32 v108, vcc, s5, v2
	s_mov_b32 s8, 0x14000
	s_nop 0
	v_addc_co_u32_e32 v109, vcc, 0, v3, vcc
	s_ashr_i32 s5, s4, 31
	s_lshl_b32 s10, s0, 13
	s_lshl_b64 s[0:1], s[4:5], 14
	v_add_co_u32_e32 v100, vcc, s8, v2
	s_mov_b32 s9, 0x15000
	s_add_u32 s0, s2, s0
	v_addc_co_u32_e32 v101, vcc, 0, v3, vcc
	s_addc_u32 s1, s3, s1
	s_and_b32 s2, s10, 0x6000
	v_add_co_u32_e32 v102, vcc, s9, v2
	s_movk_i32 s3, 0x5000
	s_nop 0
	v_addc_co_u32_e32 v103, vcc, 0, v3, vcc
	s_waitcnt vmcnt(23)
	ds_write_b128 v1, v[4:7]
	s_waitcnt vmcnt(22)
	ds_write_b128 v1, v[8:11] offset:1024
	s_waitcnt vmcnt(21)
	ds_write_b128 v1, v[12:15] offset:2048
	s_waitcnt vmcnt(20)
	ds_write_b128 v1, v[16:19] offset:3072
	s_waitcnt vmcnt(19)
	ds_write_b128 v1, v[20:23] offset:4096
	s_waitcnt vmcnt(18)
	ds_write_b128 v1, v[24:27] offset:5120
	s_waitcnt vmcnt(17)
	ds_write_b128 v1, v[28:31] offset:6144
	s_waitcnt vmcnt(16)
	ds_write_b128 v1, v[32:35] offset:7168
	s_waitcnt lgkmcnt(0)
	s_barrier
	global_load_dwordx4 v[4:7], v[106:107], off offset:-4096
	global_load_dwordx4 v[8:11], v[108:109], off offset:1024
	global_load_dwordx4 v[12:15], v[108:109], off offset:2048
	global_load_dwordx4 v[16:19], v[108:109], off offset:3072
	global_load_dwordx4 v[20:23], v[104:105], off
	global_load_dwordx4 v[24:27], v[104:105], off offset:1024
	global_load_dwordx4 v[28:31], v[104:105], off offset:2048
	global_load_dwordx4 v[32:35], v[104:105], off offset:3072
	v_or_b32_e32 v1, s2, v134
	s_waitcnt vmcnt(23)
	ds_write_b128 v1, v[36:39] offset:16384
	s_waitcnt vmcnt(22)
	ds_write_b128 v1, v[40:43] offset:17408
	s_waitcnt vmcnt(21)
	ds_write_b128 v1, v[44:47] offset:18432
	s_waitcnt vmcnt(20)
	ds_write_b128 v1, v[48:51] offset:19456
	s_waitcnt vmcnt(19)
	ds_write_b128 v1, v[52:55] offset:20480
	s_waitcnt vmcnt(18)
	ds_write_b128 v1, v[56:59] offset:21504
	s_waitcnt vmcnt(17)
	ds_write_b128 v1, v[60:63] offset:22528
	s_waitcnt vmcnt(16)
	ds_write_b128 v1, v[64:67] offset:23552
	s_waitcnt lgkmcnt(0)
	s_barrier
	global_load_dwordx4 v[36:39], v[106:107], off
	global_load_dwordx4 v[40:43], v[106:107], off offset:1024
	global_load_dwordx4 v[44:47], v[106:107], off offset:2048
	global_load_dwordx4 v[48:51], v[106:107], off offset:3072
	global_load_dwordx4 v[52:55], v[102:103], off offset:-4096
	global_load_dwordx4 v[56:59], v[100:101], off offset:1024
	global_load_dwordx4 v[60:63], v[100:101], off offset:2048
	global_load_dwordx4 v[64:67], v[100:101], off offset:3072
	s_movk_i32 s2, 0x6000
	v_add_co_u32_e32 v100, vcc, s2, v2
	s_waitcnt vmcnt(23)
	ds_write_b128 v1, v[68:71]
	s_waitcnt vmcnt(22)
	ds_write_b128 v1, v[72:75] offset:1024
	s_waitcnt vmcnt(21)
	ds_write_b128 v1, v[76:79] offset:2048
	s_waitcnt vmcnt(20)
	ds_write_b128 v1, v[80:83] offset:3072
	s_waitcnt vmcnt(19)
	ds_write_b128 v1, v[84:87] offset:4096
	s_waitcnt vmcnt(18)
	ds_write_b128 v1, v[88:91] offset:5120
	s_waitcnt vmcnt(17)
	ds_write_b128 v1, v[92:95] offset:6144
	s_waitcnt vmcnt(16)
	ds_write_b128 v1, v[96:99] offset:7168
	v_addc_co_u32_e32 v101, vcc, 0, v3, vcc
	v_add_co_u32_e32 v104, vcc, s3, v2
	s_waitcnt lgkmcnt(0)
	s_nop 0
	v_addc_co_u32_e32 v105, vcc, 0, v3, vcc
	s_barrier
	global_load_dwordx4 v[68:71], v[104:105], off offset:1024
	global_load_dwordx4 v[72:75], v[104:105], off offset:2048
	global_load_dwordx4 v[76:79], v[104:105], off offset:3072
	global_load_dwordx4 v[80:83], v[102:103], off
	global_load_dwordx4 v[84:87], v[102:103], off offset:1024
	global_load_dwordx4 v[88:91], v[102:103], off offset:2048
	global_load_dwordx4 v[92:95], v[100:101], off offset:-4096
	global_load_dwordx4 v[96:99], v[102:103], off offset:3072
	s_mov_b32 s2, 0x16000
	v_add_co_u32_e32 v102, vcc, s2, v2
	s_mov_b32 s3, 0x17000
	s_nop 0
	v_addc_co_u32_e32 v103, vcc, 0, v3, vcc
	v_add_co_u32_e32 v104, vcc, s3, v2
	s_mov_b32 s3, 0x8000
	s_nop 0
	v_addc_co_u32_e32 v105, vcc, 0, v3, vcc
	s_movk_i32 s2, 0x7000
	v_lshlrev_b32_e32 v134, 4, v0
	s_waitcnt vmcnt(23)
	ds_write_b128 v1, v[4:7] offset:16384
	s_waitcnt vmcnt(22)
	ds_write_b128 v1, v[8:11] offset:17408
	s_waitcnt vmcnt(21)
	ds_write_b128 v1, v[12:15] offset:18432
	s_waitcnt vmcnt(20)
	ds_write_b128 v1, v[16:19] offset:19456
	s_waitcnt vmcnt(19)
	ds_write_b128 v1, v[20:23] offset:20480
	s_waitcnt vmcnt(18)
	ds_write_b128 v1, v[24:27] offset:21504
	s_waitcnt vmcnt(17)
	ds_write_b128 v1, v[28:31] offset:22528
	s_waitcnt vmcnt(16)
	ds_write_b128 v1, v[32:35] offset:23552
	s_waitcnt lgkmcnt(0)
	s_barrier
	global_load_dwordx4 v[4:7], v[100:101], off
	global_load_dwordx4 v[8:11], v[100:101], off offset:1024
	global_load_dwordx4 v[12:15], v[100:101], off offset:2048
	global_load_dwordx4 v[16:19], v[100:101], off offset:3072
	global_load_dwordx4 v[20:23], v[104:105], off offset:-4096
	global_load_dwordx4 v[24:27], v[102:103], off offset:1024
	global_load_dwordx4 v[28:31], v[102:103], off offset:2048
	global_load_dwordx4 v[32:35], v[102:103], off offset:3072
	v_add_co_u32_e32 v100, vcc, s3, v2
	s_waitcnt vmcnt(23)
	ds_write_b128 v1, v[36:39]
	s_waitcnt vmcnt(22)
	ds_write_b128 v1, v[40:43] offset:1024
	s_waitcnt vmcnt(21)
	ds_write_b128 v1, v[44:47] offset:2048
	v_addc_co_u32_e32 v101, vcc, 0, v3, vcc
	v_add_co_u32_e32 v102, vcc, s2, v2
	s_waitcnt vmcnt(20)
	ds_write_b128 v1, v[48:51] offset:3072
	v_addc_co_u32_e32 v103, vcc, 0, v3, vcc
	s_waitcnt vmcnt(19)
	ds_write_b128 v1, v[52:55] offset:4096
	s_waitcnt vmcnt(18)
	ds_write_b128 v1, v[56:59] offset:5120
	s_waitcnt vmcnt(17)
	ds_write_b128 v1, v[60:63] offset:6144
	s_waitcnt vmcnt(16)
	ds_write_b128 v1, v[64:67] offset:7168
	s_waitcnt lgkmcnt(0)
	s_barrier
	global_load_dwordx4 v[36:39], v[100:101], off offset:-4096
	global_load_dwordx4 v[40:43], v[102:103], off offset:1024
	global_load_dwordx4 v[44:47], v[102:103], off offset:2048
	global_load_dwordx4 v[48:51], v[102:103], off offset:3072
	global_load_dwordx4 v[52:55], v[104:105], off
	global_load_dwordx4 v[56:59], v[104:105], off offset:1024
	global_load_dwordx4 v[60:63], v[104:105], off offset:2048
	global_load_dwordx4 v[64:67], v[104:105], off offset:3072
	s_mov_b32 s2, 0x18000
	v_add_co_u32_e32 v102, vcc, s2, v2
	s_mov_b32 s3, 0x19000
	s_nop 0
	v_addc_co_u32_e32 v103, vcc, 0, v3, vcc
	v_add_co_u32_e32 v104, vcc, s3, v2
	s_waitcnt vmcnt(17)
	ds_write_b128 v1, v[92:95] offset:16384
	ds_write_b128 v1, v[68:71] offset:17408
	ds_write_b128 v1, v[72:75] offset:18432
	ds_write_b128 v1, v[76:79] offset:19456
	ds_write_b128 v1, v[80:83] offset:20480
	ds_write_b128 v1, v[84:87] offset:21504
	ds_write_b128 v1, v[88:91] offset:22528
	s_waitcnt vmcnt(16)
	ds_write_b128 v1, v[96:99] offset:23552
	v_addc_co_u32_e32 v105, vcc, 0, v3, vcc
	s_waitcnt lgkmcnt(0)
	s_barrier
	global_load_dwordx4 v[68:71], v[100:101], off
	global_load_dwordx4 v[72:75], v[100:101], off offset:1024
	global_load_dwordx4 v[76:79], v[100:101], off offset:2048
	global_load_dwordx4 v[80:83], v[100:101], off offset:3072
	global_load_dwordx4 v[84:87], v[104:105], off offset:-4096
	global_load_dwordx4 v[88:91], v[102:103], off offset:1024
	global_load_dwordx4 v[92:95], v[102:103], off offset:2048
	s_mov_b32 s3, 0xa000
	v_add_co_u32_e32 v100, vcc, s3, v2
	s_mov_b32 s2, 0x9000
	s_nop 0
	v_addc_co_u32_e32 v101, vcc, 0, v3, vcc
	s_mov_b32 s3, 0xc000
	s_waitcnt vmcnt(22)
	ds_write_b128 v1, v[4:7]
	s_waitcnt vmcnt(21)
	ds_write_b128 v1, v[8:11] offset:1024
	s_waitcnt vmcnt(20)
	ds_write_b128 v1, v[12:15] offset:2048
	global_load_dwordx4 v[4:7], v[102:103], off offset:3072
	s_waitcnt vmcnt(20)
	ds_write_b128 v1, v[16:19] offset:3072
	s_waitcnt vmcnt(19)
	ds_write_b128 v1, v[20:23] offset:4096
	s_waitcnt vmcnt(18)
	ds_write_b128 v1, v[24:27] offset:5120
	s_waitcnt vmcnt(17)
	ds_write_b128 v1, v[28:31] offset:6144
	s_waitcnt vmcnt(16)
	ds_write_b128 v1, v[32:35] offset:7168
	s_waitcnt lgkmcnt(0)
	s_barrier
	global_load_dwordx4 v[8:11], v[100:101], off offset:-4096
	v_add_co_u32_e32 v102, vcc, s2, v2
	s_mov_b32 s2, 0x1a000
	s_nop 0
	v_addc_co_u32_e32 v103, vcc, 0, v3, vcc
	global_load_dwordx4 v[12:15], v[102:103], off offset:1024
	global_load_dwordx4 v[16:19], v[102:103], off offset:2048
	global_load_dwordx4 v[20:23], v[102:103], off offset:3072
	global_load_dwordx4 v[24:27], v[104:105], off
	global_load_dwordx4 v[28:31], v[104:105], off offset:1024
	global_load_dwordx4 v[32:35], v[104:105], off offset:2048
	global_load_dwordx4 v[96:99], v[104:105], off offset:3072
	v_add_co_u32_e32 v102, vcc, s2, v2
	s_mov_b32 s2, 0x1b000
	s_nop 0
	v_addc_co_u32_e32 v103, vcc, 0, v3, vcc
	s_waitcnt vmcnt(23)
	ds_write_b128 v1, v[36:39] offset:16384
	s_waitcnt vmcnt(22)
	ds_write_b128 v1, v[40:43] offset:17408
	s_waitcnt vmcnt(21)
	ds_write_b128 v1, v[44:47] offset:18432
	s_waitcnt vmcnt(20)
	ds_write_b128 v1, v[48:51] offset:19456
	s_waitcnt vmcnt(19)
	ds_write_b128 v1, v[52:55] offset:20480
	s_waitcnt vmcnt(18)
	ds_write_b128 v1, v[56:59] offset:21504
	s_waitcnt vmcnt(17)
	ds_write_b128 v1, v[60:63] offset:22528
	s_waitcnt vmcnt(16)
	ds_write_b128 v1, v[64:67] offset:23552
	s_waitcnt lgkmcnt(0)
	s_barrier
	global_load_dwordx4 v[36:39], v[100:101], off
	global_load_dwordx4 v[40:43], v[100:101], off offset:1024
	global_load_dwordx4 v[44:47], v[100:101], off offset:2048
	v_add_co_u32_e32 v104, vcc, s2, v2
	s_mov_b32 s2, 0xb000
	s_nop 0
	v_addc_co_u32_e32 v105, vcc, 0, v3, vcc
	global_load_dwordx4 v[48:51], v[100:101], off offset:3072
	global_load_dwordx4 v[52:55], v[104:105], off offset:-4096
	global_load_dwordx4 v[56:59], v[102:103], off offset:1024
	global_load_dwordx4 v[60:63], v[102:103], off offset:2048
	global_load_dwordx4 v[64:67], v[102:103], off offset:3072
	s_waitcnt vmcnt(23)
	ds_write_b128 v1, v[68:71]
	s_waitcnt vmcnt(22)
	ds_write_b128 v1, v[72:75] offset:1024
	s_waitcnt vmcnt(21)
	ds_write_b128 v1, v[76:79] offset:2048
	s_waitcnt vmcnt(20)
	ds_write_b128 v1, v[80:83] offset:3072
	s_waitcnt vmcnt(19)
	ds_write_b128 v1, v[84:87] offset:4096
	s_waitcnt vmcnt(18)
	ds_write_b128 v1, v[88:91] offset:5120
	s_waitcnt vmcnt(17)
	ds_write_b128 v1, v[92:95] offset:6144
	s_waitcnt vmcnt(16)
	ds_write_b128 v1, v[4:7] offset:7168
	v_add_co_u32_e32 v84, vcc, s3, v2
	s_waitcnt lgkmcnt(0)
	s_nop 0
	v_addc_co_u32_e32 v85, vcc, 0, v3, vcc
	v_add_co_u32_e32 v80, vcc, s2, v2
	s_barrier
	s_nop 0
	v_addc_co_u32_e32 v81, vcc, 0, v3, vcc
	global_load_dwordx4 v[4:7], v[84:85], off offset:-4096
	global_load_dwordx4 v[68:71], v[80:81], off offset:1024
	global_load_dwordx4 v[72:75], v[80:81], off offset:2048
	s_waitcnt vmcnt(18)
	ds_write_b128 v1, v[8:11] offset:16384
	global_load_dwordx4 v[8:11], v[80:81], off offset:3072
	global_load_dwordx4 v[76:79], v[104:105], off
	s_waitcnt vmcnt(19)
	ds_write_b128 v1, v[12:15] offset:17408
	s_waitcnt vmcnt(18)
	ds_write_b128 v1, v[16:19] offset:18432
	s_mov_b32 s2, 0x1c000
	global_load_dwordx4 v[12:15], v[104:105], off offset:1024
	global_load_dwordx4 v[16:19], v[104:105], off offset:2048
	global_load_dwordx4 v[80:83], v[104:105], off offset:3072
	v_add_co_u32_e32 v88, vcc, s2, v2
	s_mov_b32 s2, 0x1d000
	s_nop 0
	v_addc_co_u32_e32 v89, vcc, 0, v3, vcc
	v_add_co_u32_e32 v100, vcc, s2, v2
	s_mov_b32 s3, 0xe000
	s_nop 0
	v_addc_co_u32_e32 v101, vcc, 0, v3, vcc
	s_waitcnt vmcnt(20)
	ds_write_b128 v1, v[20:23] offset:19456
	s_waitcnt vmcnt(19)
	ds_write_b128 v1, v[24:27] offset:20480
	s_waitcnt vmcnt(18)
	ds_write_b128 v1, v[28:31] offset:21504
	s_waitcnt vmcnt(17)
	ds_write_b128 v1, v[32:35] offset:22528
	s_waitcnt vmcnt(16)
	ds_write_b128 v1, v[96:99] offset:23552
	s_waitcnt lgkmcnt(0)
	s_barrier
	global_load_dwordx4 v[20:23], v[84:85], off
	global_load_dwordx4 v[24:27], v[84:85], off offset:1024
	global_load_dwordx4 v[28:31], v[84:85], off offset:2048
	s_waitcnt vmcnt(18)
	ds_write_b128 v1, v[36:39]
	v_add_co_u32_e32 v102, vcc, s3, v2
	global_load_dwordx4 v[32:35], v[84:85], off offset:3072
	global_load_dwordx4 v[36:39], v[100:101], off offset:-4096
	s_waitcnt vmcnt(19)
	ds_write_b128 v1, v[40:43] offset:1024
	s_waitcnt vmcnt(18)
	ds_write_b128 v1, v[44:47] offset:2048
	s_mov_b32 s2, 0xd000
	v_addc_co_u32_e32 v103, vcc, 0, v3, vcc
	global_load_dwordx4 v[40:43], v[88:89], off offset:1024
	global_load_dwordx4 v[44:47], v[88:89], off offset:2048
	global_load_dwordx4 v[84:87], v[88:89], off offset:3072
	s_waitcnt vmcnt(20)
	ds_write_b128 v1, v[48:51] offset:3072
	s_waitcnt vmcnt(19)
	ds_write_b128 v1, v[52:55] offset:4096
	s_waitcnt vmcnt(18)
	ds_write_b128 v1, v[56:59] offset:5120
	s_waitcnt vmcnt(17)
	ds_write_b128 v1, v[60:63] offset:6144
	s_waitcnt vmcnt(16)
	ds_write_b128 v1, v[64:67] offset:7168
	s_waitcnt lgkmcnt(0)
	s_barrier
	global_load_dwordx4 v[48:51], v[102:103], off offset:-4096
	v_add_co_u32_e32 v104, vcc, s2, v2
	s_mov_b32 s2, 0x1e000
	s_nop 0
	v_addc_co_u32_e32 v105, vcc, 0, v3, vcc
	global_load_dwordx4 v[52:55], v[104:105], off offset:1024
	global_load_dwordx4 v[56:59], v[104:105], off offset:2048
	global_load_dwordx4 v[60:63], v[104:105], off offset:3072
	global_load_dwordx4 v[64:67], v[100:101], off
	global_load_dwordx4 v[88:91], v[100:101], off offset:1024
	global_load_dwordx4 v[92:95], v[100:101], off offset:2048
	global_load_dwordx4 v[96:99], v[100:101], off offset:3072
	v_add_u32_e32 v100, 0xffffff00, v0
	v_ashrrev_i32_e32 v101, 31, v100
	v_lshlrev_b32_e32 v0, 4, v100
	s_waitcnt vmcnt(23)
	ds_write_b128 v1, v[4:7] offset:16384
	s_waitcnt vmcnt(22)
	ds_write_b128 v1, v[68:71] offset:17408
	s_waitcnt vmcnt(21)
	ds_write_b128 v1, v[72:75] offset:18432
	s_waitcnt vmcnt(20)
	ds_write_b128 v1, v[8:11] offset:19456
	s_waitcnt vmcnt(19)
	ds_write_b128 v1, v[76:79] offset:20480
	s_waitcnt vmcnt(18)
	ds_write_b128 v1, v[12:15] offset:21504
	s_waitcnt vmcnt(17)
	ds_write_b128 v1, v[16:19] offset:22528
	s_waitcnt vmcnt(16)
	ds_write_b128 v1, v[80:83] offset:23552
	v_add_co_u32_e32 v68, vcc, s2, v2
	s_mov_b32 s2, 0x1f000
	s_nop 0
	v_addc_co_u32_e32 v69, vcc, 0, v3, vcc
	v_add_co_u32_e32 v76, vcc, s2, v2
	s_waitcnt lgkmcnt(0)
	s_barrier
	global_load_dwordx4 v[4:7], v[102:103], off offset:1024
	global_load_dwordx4 v[8:11], v[102:103], off offset:2048
	v_addc_co_u32_e32 v77, vcc, 0, v3, vcc
	s_waitcnt vmcnt(17)
	ds_write_b128 v1, v[20:23]
	s_mov_b32 s2, 0xf000
	global_load_dwordx4 v[12:15], v[102:103], off offset:3072
	global_load_dwordx4 v[16:19], v[76:77], off offset:-4096
	s_waitcnt vmcnt(18)
	ds_write_b128 v1, v[24:27] offset:1024
	s_waitcnt vmcnt(17)
	ds_write_b128 v1, v[28:31] offset:2048
	v_add_co_u32_e32 v2, vcc, s2, v2
	global_load_dwordx4 v[20:23], v[68:69], off offset:1024
	global_load_dwordx4 v[24:27], v[68:69], off offset:2048
	s_waitcnt vmcnt(18)
	ds_write_b128 v1, v[32:35] offset:3072
	v_addc_co_u32_e32 v3, vcc, 0, v3, vcc
	global_load_dwordx4 v[28:31], v[102:103], off
	global_load_dwordx4 v[32:35], v[68:69], off offset:3072
	s_waitcnt vmcnt(19)
	ds_write_b128 v1, v[36:39] offset:4096
	s_waitcnt vmcnt(18)
	ds_write_b128 v1, v[40:43] offset:5120
	s_waitcnt vmcnt(17)
	ds_write_b128 v1, v[44:47] offset:6144
	s_waitcnt vmcnt(16)
	ds_write_b128 v1, v[84:87] offset:7168
	s_waitcnt lgkmcnt(0)
	s_barrier
	global_load_dwordx4 v[36:39], v[2:3], off
	global_load_dwordx4 v[40:43], v[2:3], off offset:1024
	global_load_dwordx4 v[44:47], v[2:3], off offset:2048
	global_load_dwordx4 v[68:71], v[2:3], off offset:3072
	s_waitcnt vmcnt(19)
	ds_write_b128 v1, v[48:51] offset:16384
	global_load_dwordx4 v[48:51], v[76:77], off
	global_load_dwordx4 v[72:75], v[76:77], off offset:1024
	s_waitcnt vmcnt(20)
	ds_write_b128 v1, v[52:55] offset:17408
	s_waitcnt vmcnt(19)
	ds_write_b128 v1, v[56:59] offset:18432
	v_lshl_add_u64 v[2:3], v[100:101], 4, s[0:1]
	global_load_dwordx4 v[52:55], v[76:77], off offset:2048
	global_load_dwordx4 v[56:59], v[76:77], off offset:3072
	s_waitcnt vmcnt(20)
	ds_write_b128 v1, v[60:63] offset:19456
	s_waitcnt vmcnt(19)
	ds_write_b128 v1, v[64:67] offset:20480
	s_waitcnt vmcnt(18)
	ds_write_b128 v1, v[88:91] offset:21504
	s_waitcnt vmcnt(17)
	ds_write_b128 v1, v[92:95] offset:22528
	s_waitcnt vmcnt(16)
	ds_write_b128 v1, v[96:99] offset:23552
	s_waitcnt lgkmcnt(0)
	s_barrier
	global_load_dwordx4 v[60:63], v[2:3], off
	v_lshl_add_u64 v[2:3], s[0:1], 0, v[134:135]
	v_add_co_u32_e32 v102, vcc, s6, v2
	global_load_dwordx4 v[64:67], v134, s[0:1] offset:-2048
	global_load_dwordx4 v[76:79], v134, s[0:1]
	v_addc_co_u32_e32 v103, vcc, 0, v3, vcc
	v_add_co_u32_e32 v2, vcc, s7, v2
	s_nop 1
	v_addc_co_u32_e32 v3, vcc, 0, v3, vcc
	global_load_dwordx4 v[80:83], v134, s[0:1] offset:2048
	global_load_dwordx4 v[84:87], v[2:3], off offset:-4096
	global_load_dwordx4 v[88:91], v[102:103], off offset:2048
	global_load_dwordx4 v[92:95], v[2:3], off
	global_load_dwordx4 v[96:99], v[2:3], off offset:2048
	s_waitcnt vmcnt(17)
	ds_write_b128 v1, v[28:31]
	ds_write_b128 v1, v[4:7] offset:1024
	ds_write_b128 v1, v[8:11] offset:2048
	ds_write_b128 v1, v[12:15] offset:3072
	ds_write_b128 v1, v[16:19] offset:4096
	ds_write_b128 v1, v[20:23] offset:5120
	ds_write_b128 v1, v[24:27] offset:6144
	s_waitcnt vmcnt(16)
	ds_write_b128 v1, v[32:35] offset:7168
	s_waitcnt lgkmcnt(0)
	s_barrier
	s_waitcnt vmcnt(15)
	ds_write_b128 v1, v[36:39] offset:16384
	s_waitcnt vmcnt(14)
	ds_write_b128 v1, v[40:43] offset:17408
	s_waitcnt vmcnt(13)
	ds_write_b128 v1, v[44:47] offset:18432
	s_waitcnt vmcnt(12)
	ds_write_b128 v1, v[68:71] offset:19456
	s_waitcnt vmcnt(11)
	ds_write_b128 v1, v[48:51] offset:20480
	s_waitcnt vmcnt(10)
	ds_write_b128 v1, v[72:75] offset:21504
	s_waitcnt vmcnt(9)
	ds_write_b128 v1, v[52:55] offset:22528
	s_waitcnt vmcnt(8)
	ds_write_b128 v1, v[56:59] offset:23552
	s_waitcnt lgkmcnt(0)
	s_barrier
	s_waitcnt vmcnt(7)
	ds_write_b128 v0, v[60:63] offset:33792
	s_waitcnt vmcnt(6)
	ds_write_b128 v0, v[64:67] offset:35840
	s_waitcnt vmcnt(5)
	ds_write_b128 v0, v[76:79] offset:37888
	s_waitcnt vmcnt(4)
	ds_write_b128 v0, v[80:83] offset:39936
	s_waitcnt vmcnt(3)
	ds_write_b128 v0, v[84:87] offset:41984
	s_waitcnt vmcnt(2)
	ds_write_b128 v0, v[88:91] offset:44032
	s_waitcnt vmcnt(1)
	ds_write_b128 v0, v[92:95] offset:46080
	s_waitcnt vmcnt(0)
	ds_write_b128 v0, v[96:99] offset:48128
	s_waitcnt lgkmcnt(0)
	s_barrier
	s_endpgm
	s_nop 0
	s_nop 0
	s_nop 0
	s_nop 0
	s_nop 0
	s_nop 0
	s_nop 0
	s_nop 0
	s_nop 0
	s_nop 0
	s_nop 0
	s_nop 0
	s_nop 0
	s_nop 0
	s_nop 0
	s_nop 0
	s_nop 0
	s_nop 0
	s_nop 0
	s_nop 0
	s_nop 0
	s_nop 0
	s_nop 0
	s_endpgm
